# P9 RG-LRU gates+scan epilogue hand-written with packed f32 VALU and fused DPP scans
# speedup vs baseline: 1.0099x; 1.0099x over previous
; #define LAS __attribute__((address_space(3)))
; __device__ __forceinline__ float fast_exp(float x) { return __builtin_amdgcn_exp2f(x * 1.4426950408889634f); }
; __device__ __forceinline__ float fast_sigmoid(float x) { return __builtin_amdgcn_rcpf(1.0f + fast_exp(-x)); }
;     __device__ __forceinline__ void operator()(Acc& acc, const Unit& u, int wr, int wc, int fr_, int fq_, LAS unsigned char* le, int wid, int lane, int&) const {
;         asm volatile("" : "+v"(lane));
;         const int fr = lane & 15, fq = lane >> 4;
;         const int row0 = u.pm * 256, chb = (u.pn >> 1) * 256 + (u.pn & 1) * 128, ch0 = chb + wc * 32 + fq * 4, tid = wid * 64 + lane;
;         size_t roff = (size_t)(row0 + wr * 64 + 4 * fr) * DM + ch0;
;         LAS float* X = (LAS float*)le;
;         LAS float* C0 = X + 1024;
;         u32x2 xpre[2][4][2];
; #pragma unroll
;         for (int ai = 0; ai < 2; ++ai)
; #pragma unroll
;             for (int m = 0; m < 4; ++m)
; #pragma unroll
;                 for (int n = 0; n < 2; ++n) xpre[ai][m][n] = *(const u32x2*)(xc + roff + (size_t)(ai * 128 + m) * DM + n * 16);
;         float EA[2][2][4], EH[2][2][4];
; #pragma unroll
;         for (int ai = 0; ai < 2; ++ai) {
; #pragma unroll
;             for (int m = 0; m < 4; ++m) {
; #pragma unroll
;                 for (int n = 0; n < 2; ++n) {
;                     const f32x4 ba = *(const f32x4*)(b_a + ch0 + n * 16), bi = *(const f32x4*)(b_i + ch0 + n * 16), sl = *(const f32x4*)(spl + ch0 + n * 16);
;                     const u32x2 xw = xpre[ai][m][n]; const float xv[4] = {bflo(xw.x), bfhi(xw.x), bflo(xw.y), bfhi(xw.y)};
;                     const f32x4 ra = acc[ai][0][m][n] + ba, ri = acc[ai][1][m][n] + bi;
; #pragma unroll
;                     for (int j = 0; j < 4; ++j) { const float r = fast_sigmoid(ra[j]), ig = fast_sigmoid(ri[j]);
;                         const float la = -8.0f * r * sl[j];
;                         const float a = fast_exp(la); const float x2 = 2.0f * la;
;                         const float ser = -x2 * (1.0f + x2 * (0.5f + x2 * (1.0f / 6.0f + x2 * (1.0f / 24.0f + x2 * (1.0f / 120.0f)))));
;                         const float om = (x2 > -0.3f) ? ser : (1.0f - a * a);
.LBB0_1598:
	v_mbcnt_lo_u32_b32 v226, -1, 0
	v_mbcnt_hi_u32_b32 v226, -1, v226
	s_lshr_b32 s8, s91, 6
	s_lshr_b32 s9, s8, 2
	s_and_b32 s10, s8, 3
	v_and_b32_e32 v227, 15, v226
	v_lshrrev_b32_e32 v224, 4, v226
	v_add_u32_e32 v228, s91, v226
	s_lshl_b32 s11, s16, 7
	s_lshl_b32 s12, s10, 5
	s_add_i32 s12, s12, s11
	v_lshl_add_u32 v237, v224, 2, s12
	s_lshl_b32 s13, s18, 8
	s_lshl_b32 s15, s9, 6
	s_add_i32 s13, s13, s15
	v_lshl_add_u32 v238, v227, 2, s13
	v_lshl_add_u32 v238, v238, 11, v237
	v_lshlrev_b32_e32 v229, 1, v238
	v_add_u32_e32 v230, 0x1000, v229
	v_add_u32_e32 v231, 0x2000, v229
	v_add_u32_e32 v232, 0x3000, v229
	v_add_u32_e32 v233, 0x80000, v229
	v_add_u32_e32 v234, 0x81000, v229
	v_add_u32_e32 v235, 0x82000, v229
	v_add_u32_e32 v236, 0x83000, v229
	v_lshlrev_b32_e32 v239, 2, v237
	global_load_dwordx4 v[68:71], v239, s[42:43] offset:0
	global_load_dwordx4 v[100:103], v239, s[2:3] offset:0
	global_load_dwordx4 v[88:91], v239, s[44:45] offset:0
	global_load_dwordx4 v[72:75], v239, s[42:43] offset:64
	global_load_dwordx4 v[104:107], v239, s[2:3] offset:64
	global_load_dwordx4 v[198:201], v239, s[44:45] offset:64
	global_load_dwordx2 v[166:167], v229, s[40:41] offset:0
	global_load_dwordx2 v[168:169], v229, s[40:41] offset:32
	global_load_dwordx2 v[170:171], v230, s[40:41] offset:0
	global_load_dwordx2 v[172:173], v230, s[40:41] offset:32
	global_load_dwordx2 v[174:175], v231, s[40:41] offset:0
	global_load_dwordx2 v[176:177], v231, s[40:41] offset:32
	global_load_dwordx2 v[178:179], v232, s[40:41] offset:0
	global_load_dwordx2 v[180:181], v232, s[40:41] offset:32
	global_load_dwordx2 v[182:183], v233, s[40:41] offset:0
	global_load_dwordx2 v[184:185], v233, s[40:41] offset:32
	global_load_dwordx2 v[186:187], v234, s[40:41] offset:0
	global_load_dwordx2 v[188:189], v234, s[40:41] offset:32
	global_load_dwordx2 v[190:191], v235, s[40:41] offset:0
	global_load_dwordx2 v[192:193], v235, s[40:41] offset:32
	global_load_dwordx2 v[194:195], v236, s[40:41] offset:0
	global_load_dwordx2 v[196:197], v236, s[40:41] offset:32
	v_mov_b32_e32 v246, 0xbfb8aa3b
	v_mov_b32_e32 v247, 0x3fb8aa3b
	v_mov_b32_e32 v248, 1.0
	v_mov_b32_e32 v249, 0x3c088889
	v_mov_b32_e32 v250, 0x3d2aaaab
	v_mov_b32_e32 v251, 0x3e2aaaab
	v_mov_b32_e32 v252, 0.5
	v_mov_b32_e32 v253, 0xbe99999a
	s_mov_b32 s22, 0xffff0000
	s_waitcnt vmcnt(0)
	v_mul_f32_e32 v88, 0xc1000000, v88
	v_mul_f32_e32 v89, 0xc1000000, v89
	v_mul_f32_e32 v90, 0xc1000000, v90
	v_mul_f32_e32 v91, 0xc1000000, v91
	v_mul_f32_e32 v198, 0xc1000000, v198
	v_mul_f32_e32 v199, 0xc1000000, v199
	v_mul_f32_e32 v200, 0xc1000000, v200
	v_mul_f32_e32 v201, 0xc1000000, v201
	v_pk_add_f32 v[202:203], v[148:149], v[68:69] op_sel:[0,0] op_sel_hi:[1,1]
	v_pk_add_f32 v[204:205], v[150:151], v[70:71] op_sel:[0,0] op_sel_hi:[1,1]
	v_pk_add_f32 v[206:207], v[132:133], v[100:101] op_sel:[0,0] op_sel_hi:[1,1]
	v_pk_add_f32 v[208:209], v[134:135], v[102:103] op_sel:[0,0] op_sel_hi:[1,1]
	v_pk_mul_f32 v[202:203], v[202:203], v[246:247] op_sel:[0,0] op_sel_hi:[1,0]
	v_pk_mul_f32 v[204:205], v[204:205], v[246:247] op_sel:[0,0] op_sel_hi:[1,0]
	v_pk_mul_f32 v[206:207], v[206:207], v[246:247] op_sel:[0,0] op_sel_hi:[1,0]
	v_pk_mul_f32 v[208:209], v[208:209], v[246:247] op_sel:[0,0] op_sel_hi:[1,0]
	v_exp_f32_e32 v202, v202
	v_exp_f32_e32 v203, v203
	v_exp_f32_e32 v204, v204
	v_exp_f32_e32 v205, v205
	v_exp_f32_e32 v206, v206
	v_exp_f32_e32 v207, v207
	v_exp_f32_e32 v208, v208
	v_exp_f32_e32 v209, v209
	v_pk_add_f32 v[202:203], v[202:203], v[248:249] op_sel:[0,0] op_sel_hi:[1,0]
	v_pk_add_f32 v[204:205], v[204:205], v[248:249] op_sel:[0,0] op_sel_hi:[1,0]
	v_pk_add_f32 v[206:207], v[206:207], v[248:249] op_sel:[0,0] op_sel_hi:[1,0]
	v_pk_add_f32 v[208:209], v[208:209], v[248:249] op_sel:[0,0] op_sel_hi:[1,0]
	v_rcp_f32_e32 v202, v202
	v_rcp_f32_e32 v203, v203
	v_rcp_f32_e32 v204, v204
	v_rcp_f32_e32 v205, v205
	v_rcp_f32_e32 v206, v206
	v_rcp_f32_e32 v207, v207
	v_rcp_f32_e32 v208, v208
	v_rcp_f32_e32 v209, v209
	v_lshlrev_b32_e32 v242, 16, v166
	v_and_b32_e32 v243, s22, v166
	v_lshlrev_b32_e32 v244, 16, v167
	v_and_b32_e32 v245, s22, v167
	v_pk_mul_f32 v[210:211], v[202:203], v[88:89] op_sel:[0,0] op_sel_hi:[1,1]
	v_pk_mul_f32 v[212:213], v[204:205], v[90:91] op_sel:[0,0] op_sel_hi:[1,1]
	v_pk_mul_f32 v[206:207], v[206:207], v[242:243] op_sel:[0,0] op_sel_hi:[1,1]
	v_pk_mul_f32 v[208:209], v[208:209], v[244:245] op_sel:[0,0] op_sel_hi:[1,1]
	v_pk_mul_f32 v[214:215], v[210:211], v[246:247] op_sel:[0,1] op_sel_hi:[1,1]
	v_pk_mul_f32 v[216:217], v[212:213], v[246:247] op_sel:[0,1] op_sel_hi:[1,1]
	v_pk_add_f32 v[210:211], v[210:211], v[210:211] op_sel:[0,0] op_sel_hi:[1,1]
	v_pk_add_f32 v[212:213], v[212:213], v[212:213] op_sel:[0,0] op_sel_hi:[1,1]
	v_exp_f32_e32 v148, v214
	v_exp_f32_e32 v149, v215
	v_exp_f32_e32 v150, v216
	v_exp_f32_e32 v151, v217
	v_pk_fma_f32 v[238:239], v[210:211], v[248:249], v[250:251] op_sel:[0,1,0] op_sel_hi:[1,1,0]
	v_pk_fma_f32 v[240:241], v[212:213], v[248:249], v[250:251] op_sel:[0,1,0] op_sel_hi:[1,1,0]
	v_pk_fma_f32 v[238:239], v[210:211], v[238:239], v[250:251] op_sel:[0,0,1] op_sel_hi:[1,1,1]
	v_pk_fma_f32 v[240:241], v[212:213], v[240:241], v[250:251] op_sel:[0,0,1] op_sel_hi:[1,1,1]
	v_pk_fma_f32 v[238:239], v[210:211], v[238:239], v[252:253] op_sel:[0,0,0] op_sel_hi:[1,1,0]
	v_pk_fma_f32 v[240:241], v[212:213], v[240:241], v[252:253] op_sel:[0,0,0] op_sel_hi:[1,1,0]
	v_pk_fma_f32 v[238:239], v[210:211], v[238:239], v[248:249] op_sel:[0,0,0] op_sel_hi:[1,1,0]
	v_pk_fma_f32 v[240:241], v[212:213], v[240:241], v[248:249] op_sel:[0,0,0] op_sel_hi:[1,1,0]
; __device__ __forceinline__ float fast_exp(float x) { return __builtin_amdgcn_exp2f(x * 1.4426950408889634f); }
; __device__ __forceinline__ float fast_sigmoid(float x) { return __builtin_amdgcn_rcpf(1.0f + fast_exp(-x)); }
;     __device__ __forceinline__ void operator()(Acc& acc, const Unit& u, int wr, int wc, int fr_, int fq_, LAS unsigned char* le, int wid, int lane, int&) const {
;     ...
;                     const f32x4 ba = *(const f32x4*)(b_a + ch0 + n * 16), bi = *(const f32x4*)(b_i + ch0 + n * 16), sl = *(const f32x4*)(spl + ch0 + n * 16);
;                     const u32x2 xw = xpre[ai][m][n]; const float xv[4] = {bflo(xw.x), bfhi(xw.x), bflo(xw.y), bfhi(xw.y)};
;                     const f32x4 ra = acc[ai][0][m][n] + ba, ri = acc[ai][1][m][n] + bi;
; #pragma unroll
;                     for (int j = 0; j < 4; ++j) { const float r = fast_sigmoid(ra[j]), ig = fast_sigmoid(ri[j]);
;                         const float la = -8.0f * r * sl[j];
;                         const float a = fast_exp(la); const float x2 = 2.0f * la;
;                         const float ser = -x2 * (1.0f + x2 * (0.5f + x2 * (1.0f / 6.0f + x2 * (1.0f / 24.0f + x2 * (1.0f / 120.0f)))));
;                         const float om = (x2 > -0.3f) ? ser : (1.0f - a * a);
;                         const float uu = __builtin_amdgcn_sqrtf(om) * (ig * xv[j]);
;                         if (m == 0) { acc[ai][0][m][n][j] = a; acc[ai][1][m][n][j] = uu; }
;                         else { acc[ai][1][m][n][j] = a * acc[ai][1][m - 1][n][j] + uu; acc[ai][0][m][n][j] = acc[ai][0][m - 1][n][j] * a; } } } }
	v_pk_mul_f32 v[238:239], v[210:211], v[238:239] op_sel:[0,0] op_sel_hi:[1,1] neg_lo:[1,0] neg_hi:[1,0]
	v_pk_mul_f32 v[240:241], v[212:213], v[240:241] op_sel:[0,0] op_sel_hi:[1,1] neg_lo:[1,0] neg_hi:[1,0]
	v_pk_fma_f32 v[242:243], v[148:149], v[148:149], v[248:249] op_sel:[0,0,0] op_sel_hi:[1,1,0] neg_lo:[1,0,0] neg_hi:[1,0,0]
	v_pk_fma_f32 v[244:245], v[150:151], v[150:151], v[248:249] op_sel:[0,0,0] op_sel_hi:[1,1,0] neg_lo:[1,0,0] neg_hi:[1,0,0]
	v_cmp_lt_f32_e64 s[24:25], v253, v210
	v_cmp_lt_f32_e64 s[26:27], v253, v211
	v_cmp_lt_f32_e64 s[30:31], v253, v212
	v_cmp_lt_f32_e64 s[34:35], v253, v213
	v_cndmask_b32_e64 v238, v242, v238, s[24:25]
	v_cndmask_b32_e64 v239, v243, v239, s[26:27]
	v_cndmask_b32_e64 v240, v244, v240, s[30:31]
	v_cndmask_b32_e64 v241, v245, v241, s[34:35]
	v_sqrt_f32_e32 v238, v238
	v_sqrt_f32_e32 v239, v239
	v_sqrt_f32_e32 v240, v240
	v_sqrt_f32_e32 v241, v241
	v_pk_mul_f32 v[132:133], v[238:239], v[206:207] op_sel:[0,0] op_sel_hi:[1,1]
	v_pk_mul_f32 v[134:135], v[240:241], v[208:209] op_sel:[0,0] op_sel_hi:[1,1]
	v_pk_add_f32 v[202:203], v[116:117], v[72:73] op_sel:[0,0] op_sel_hi:[1,1]
	v_pk_add_f32 v[204:205], v[118:119], v[74:75] op_sel:[0,0] op_sel_hi:[1,1]
	v_pk_add_f32 v[206:207], v[92:93], v[104:105] op_sel:[0,0] op_sel_hi:[1,1]
	v_pk_add_f32 v[208:209], v[94:95], v[106:107] op_sel:[0,0] op_sel_hi:[1,1]
	v_pk_mul_f32 v[202:203], v[202:203], v[246:247] op_sel:[0,0] op_sel_hi:[1,0]
	v_pk_mul_f32 v[204:205], v[204:205], v[246:247] op_sel:[0,0] op_sel_hi:[1,0]
	v_pk_mul_f32 v[206:207], v[206:207], v[246:247] op_sel:[0,0] op_sel_hi:[1,0]
	v_pk_mul_f32 v[208:209], v[208:209], v[246:247] op_sel:[0,0] op_sel_hi:[1,0]
	v_exp_f32_e32 v202, v202
	v_exp_f32_e32 v203, v203
	v_exp_f32_e32 v204, v204
	v_exp_f32_e32 v205, v205
	v_exp_f32_e32 v206, v206
	v_exp_f32_e32 v207, v207
	v_exp_f32_e32 v208, v208
	v_exp_f32_e32 v209, v209
	v_pk_add_f32 v[202:203], v[202:203], v[248:249] op_sel:[0,0] op_sel_hi:[1,0]
	v_pk_add_f32 v[204:205], v[204:205], v[248:249] op_sel:[0,0] op_sel_hi:[1,0]
	v_pk_add_f32 v[206:207], v[206:207], v[248:249] op_sel:[0,0] op_sel_hi:[1,0]
	v_pk_add_f32 v[208:209], v[208:209], v[248:249] op_sel:[0,0] op_sel_hi:[1,0]
	v_rcp_f32_e32 v202, v202
	v_rcp_f32_e32 v203, v203
	v_rcp_f32_e32 v204, v204
	v_rcp_f32_e32 v205, v205
	v_rcp_f32_e32 v206, v206
	v_rcp_f32_e32 v207, v207
	v_rcp_f32_e32 v208, v208
	v_rcp_f32_e32 v209, v209
	v_lshlrev_b32_e32 v242, 16, v168
	v_and_b32_e32 v243, s22, v168
	v_lshlrev_b32_e32 v244, 16, v169
	v_and_b32_e32 v245, s22, v169
	v_pk_mul_f32 v[210:211], v[202:203], v[198:199] op_sel:[0,0] op_sel_hi:[1,1]
	v_pk_mul_f32 v[212:213], v[204:205], v[200:201] op_sel:[0,0] op_sel_hi:[1,1]
	v_pk_mul_f32 v[206:207], v[206:207], v[242:243] op_sel:[0,0] op_sel_hi:[1,1]
	v_pk_mul_f32 v[208:209], v[208:209], v[244:245] op_sel:[0,0] op_sel_hi:[1,1]
	v_pk_mul_f32 v[214:215], v[210:211], v[246:247] op_sel:[0,1] op_sel_hi:[1,1]
	v_pk_mul_f32 v[216:217], v[212:213], v[246:247] op_sel:[0,1] op_sel_hi:[1,1]
	v_pk_add_f32 v[210:211], v[210:211], v[210:211] op_sel:[0,0] op_sel_hi:[1,1]
	v_pk_add_f32 v[212:213], v[212:213], v[212:213] op_sel:[0,0] op_sel_hi:[1,1]
	v_exp_f32_e32 v116, v214
	v_exp_f32_e32 v117, v215
	v_exp_f32_e32 v118, v216
	v_exp_f32_e32 v119, v217
	v_pk_fma_f32 v[238:239], v[210:211], v[248:249], v[250:251] op_sel:[0,1,0] op_sel_hi:[1,1,0]
	v_pk_fma_f32 v[240:241], v[212:213], v[248:249], v[250:251] op_sel:[0,1,0] op_sel_hi:[1,1,0]
	v_pk_fma_f32 v[238:239], v[210:211], v[238:239], v[250:251] op_sel:[0,0,1] op_sel_hi:[1,1,1]
	v_pk_fma_f32 v[240:241], v[212:213], v[240:241], v[250:251] op_sel:[0,0,1] op_sel_hi:[1,1,1]
	v_pk_fma_f32 v[238:239], v[210:211], v[238:239], v[252:253] op_sel:[0,0,0] op_sel_hi:[1,1,0]
	v_pk_fma_f32 v[240:241], v[212:213], v[240:241], v[252:253] op_sel:[0,0,0] op_sel_hi:[1,1,0]
	v_pk_fma_f32 v[238:239], v[210:211], v[238:239], v[248:249] op_sel:[0,0,0] op_sel_hi:[1,1,0]
	v_pk_fma_f32 v[240:241], v[212:213], v[240:241], v[248:249] op_sel:[0,0,0] op_sel_hi:[1,1,0]
	v_pk_mul_f32 v[238:239], v[210:211], v[238:239] op_sel:[0,0] op_sel_hi:[1,1] neg_lo:[1,0] neg_hi:[1,0]
	v_pk_mul_f32 v[240:241], v[212:213], v[240:241] op_sel:[0,0] op_sel_hi:[1,1] neg_lo:[1,0] neg_hi:[1,0]
	v_pk_fma_f32 v[242:243], v[116:117], v[116:117], v[248:249] op_sel:[0,0,0] op_sel_hi:[1,1,0] neg_lo:[1,0,0] neg_hi:[1,0,0]
	v_pk_fma_f32 v[244:245], v[118:119], v[118:119], v[248:249] op_sel:[0,0,0] op_sel_hi:[1,1,0] neg_lo:[1,0,0] neg_hi:[1,0,0]
	v_cmp_lt_f32_e64 s[24:25], v253, v210
	v_cmp_lt_f32_e64 s[26:27], v253, v211
	v_cmp_lt_f32_e64 s[30:31], v253, v212
	v_cmp_lt_f32_e64 s[34:35], v253, v213
	v_cndmask_b32_e64 v238, v242, v238, s[24:25]
	v_cndmask_b32_e64 v239, v243, v239, s[26:27]
	v_cndmask_b32_e64 v240, v244, v240, s[30:31]
	v_cndmask_b32_e64 v241, v245, v241, s[34:35]
	v_sqrt_f32_e32 v238, v238
	v_sqrt_f32_e32 v239, v239
	v_sqrt_f32_e32 v240, v240
	v_sqrt_f32_e32 v241, v241
	v_pk_mul_f32 v[92:93], v[238:239], v[206:207] op_sel:[0,0] op_sel_hi:[1,1]
	v_pk_mul_f32 v[94:95], v[240:241], v[208:209] op_sel:[0,0] op_sel_hi:[1,1]
	v_pk_add_f32 v[202:203], v[144:145], v[68:69] op_sel:[0,0] op_sel_hi:[1,1]
	v_pk_add_f32 v[204:205], v[146:147], v[70:71] op_sel:[0,0] op_sel_hi:[1,1]
	v_pk_add_f32 v[206:207], v[128:129], v[100:101] op_sel:[0,0] op_sel_hi:[1,1]
	v_pk_add_f32 v[208:209], v[130:131], v[102:103] op_sel:[0,0] op_sel_hi:[1,1]
	v_pk_mul_f32 v[202:203], v[202:203], v[246:247] op_sel:[0,0] op_sel_hi:[1,0]
	v_pk_mul_f32 v[204:205], v[204:205], v[246:247] op_sel:[0,0] op_sel_hi:[1,0]
	v_pk_mul_f32 v[206:207], v[206:207], v[246:247] op_sel:[0,0] op_sel_hi:[1,0]
; __device__ __forceinline__ float fast_exp(float x) { return __builtin_amdgcn_exp2f(x * 1.4426950408889634f); }
; __device__ __forceinline__ float fast_sigmoid(float x) { return __builtin_amdgcn_rcpf(1.0f + fast_exp(-x)); }
;     __device__ __forceinline__ void operator()(Acc& acc, const Unit& u, int wr, int wc, int fr_, int fq_, LAS unsigned char* le, int wid, int lane, int&) const {
;     ...
;                     const f32x4 ba = *(const f32x4*)(b_a + ch0 + n * 16), bi = *(const f32x4*)(b_i + ch0 + n * 16), sl = *(const f32x4*)(spl + ch0 + n * 16);
;                     const u32x2 xw = xpre[ai][m][n]; const float xv[4] = {bflo(xw.x), bfhi(xw.x), bflo(xw.y), bfhi(xw.y)};
;                     const f32x4 ra = acc[ai][0][m][n] + ba, ri = acc[ai][1][m][n] + bi;
; #pragma unroll
;                     for (int j = 0; j < 4; ++j) { const float r = fast_sigmoid(ra[j]), ig = fast_sigmoid(ri[j]);
;                         const float la = -8.0f * r * sl[j];
;                         const float a = fast_exp(la); const float x2 = 2.0f * la;
;                         const float ser = -x2 * (1.0f + x2 * (0.5f + x2 * (1.0f / 6.0f + x2 * (1.0f / 24.0f + x2 * (1.0f / 120.0f)))));
;                         const float om = (x2 > -0.3f) ? ser : (1.0f - a * a);
;                         const float uu = __builtin_amdgcn_sqrtf(om) * (ig * xv[j]);
;                         if (m == 0) { acc[ai][0][m][n][j] = a; acc[ai][1][m][n][j] = uu; }
;                         else { acc[ai][1][m][n][j] = a * acc[ai][1][m - 1][n][j] + uu; acc[ai][0][m][n][j] = acc[ai][0][m - 1][n][j] * a; } } } }
	v_pk_mul_f32 v[208:209], v[208:209], v[246:247] op_sel:[0,0] op_sel_hi:[1,0]
	v_exp_f32_e32 v202, v202
	v_exp_f32_e32 v203, v203
	v_exp_f32_e32 v204, v204
	v_exp_f32_e32 v205, v205
	v_exp_f32_e32 v206, v206
	v_exp_f32_e32 v207, v207
	v_exp_f32_e32 v208, v208
	v_exp_f32_e32 v209, v209
	v_pk_add_f32 v[202:203], v[202:203], v[248:249] op_sel:[0,0] op_sel_hi:[1,0]
	v_pk_add_f32 v[204:205], v[204:205], v[248:249] op_sel:[0,0] op_sel_hi:[1,0]
	v_pk_add_f32 v[206:207], v[206:207], v[248:249] op_sel:[0,0] op_sel_hi:[1,0]
	v_pk_add_f32 v[208:209], v[208:209], v[248:249] op_sel:[0,0] op_sel_hi:[1,0]
	v_rcp_f32_e32 v202, v202
	v_rcp_f32_e32 v203, v203
	v_rcp_f32_e32 v204, v204
	v_rcp_f32_e32 v205, v205
	v_rcp_f32_e32 v206, v206
	v_rcp_f32_e32 v207, v207
	v_rcp_f32_e32 v208, v208
	v_rcp_f32_e32 v209, v209
	v_lshlrev_b32_e32 v242, 16, v170
	v_and_b32_e32 v243, s22, v170
	v_lshlrev_b32_e32 v244, 16, v171
	v_and_b32_e32 v245, s22, v171
	v_pk_mul_f32 v[210:211], v[202:203], v[88:89] op_sel:[0,0] op_sel_hi:[1,1]
	v_pk_mul_f32 v[212:213], v[204:205], v[90:91] op_sel:[0,0] op_sel_hi:[1,1]
	v_pk_mul_f32 v[206:207], v[206:207], v[242:243] op_sel:[0,0] op_sel_hi:[1,1]
	v_pk_mul_f32 v[208:209], v[208:209], v[244:245] op_sel:[0,0] op_sel_hi:[1,1]
	v_pk_mul_f32 v[214:215], v[210:211], v[246:247] op_sel:[0,1] op_sel_hi:[1,1]
	v_pk_mul_f32 v[216:217], v[212:213], v[246:247] op_sel:[0,1] op_sel_hi:[1,1]
	v_pk_add_f32 v[210:211], v[210:211], v[210:211] op_sel:[0,0] op_sel_hi:[1,1]
	v_pk_add_f32 v[212:213], v[212:213], v[212:213] op_sel:[0,0] op_sel_hi:[1,1]
	v_exp_f32_e32 v214, v214
	v_exp_f32_e32 v215, v215
	v_exp_f32_e32 v216, v216
	v_exp_f32_e32 v217, v217
	v_pk_fma_f32 v[238:239], v[210:211], v[248:249], v[250:251] op_sel:[0,1,0] op_sel_hi:[1,1,0]
	v_pk_fma_f32 v[240:241], v[212:213], v[248:249], v[250:251] op_sel:[0,1,0] op_sel_hi:[1,1,0]
	v_pk_fma_f32 v[238:239], v[210:211], v[238:239], v[250:251] op_sel:[0,0,1] op_sel_hi:[1,1,1]
	v_pk_fma_f32 v[240:241], v[212:213], v[240:241], v[250:251] op_sel:[0,0,1] op_sel_hi:[1,1,1]
	v_pk_fma_f32 v[238:239], v[210:211], v[238:239], v[252:253] op_sel:[0,0,0] op_sel_hi:[1,1,0]
	v_pk_fma_f32 v[240:241], v[212:213], v[240:241], v[252:253] op_sel:[0,0,0] op_sel_hi:[1,1,0]
	v_pk_fma_f32 v[238:239], v[210:211], v[238:239], v[248:249] op_sel:[0,0,0] op_sel_hi:[1,1,0]
	v_pk_fma_f32 v[240:241], v[212:213], v[240:241], v[248:249] op_sel:[0,0,0] op_sel_hi:[1,1,0]
	v_pk_mul_f32 v[238:239], v[210:211], v[238:239] op_sel:[0,0] op_sel_hi:[1,1] neg_lo:[1,0] neg_hi:[1,0]
	v_pk_mul_f32 v[240:241], v[212:213], v[240:241] op_sel:[0,0] op_sel_hi:[1,1] neg_lo:[1,0] neg_hi:[1,0]
	v_pk_fma_f32 v[242:243], v[214:215], v[214:215], v[248:249] op_sel:[0,0,0] op_sel_hi:[1,1,0] neg_lo:[1,0,0] neg_hi:[1,0,0]
	v_pk_fma_f32 v[244:245], v[216:217], v[216:217], v[248:249] op_sel:[0,0,0] op_sel_hi:[1,1,0] neg_lo:[1,0,0] neg_hi:[1,0,0]
	v_cmp_lt_f32_e64 s[24:25], v253, v210
	v_cmp_lt_f32_e64 s[26:27], v253, v211
	v_cmp_lt_f32_e64 s[30:31], v253, v212
	v_cmp_lt_f32_e64 s[34:35], v253, v213
	v_cndmask_b32_e64 v238, v242, v238, s[24:25]
	v_cndmask_b32_e64 v239, v243, v239, s[26:27]
	v_cndmask_b32_e64 v240, v244, v240, s[30:31]
	v_cndmask_b32_e64 v241, v245, v241, s[34:35]
	v_sqrt_f32_e32 v238, v238
	v_sqrt_f32_e32 v239, v239
	v_sqrt_f32_e32 v240, v240
	v_sqrt_f32_e32 v241, v241
	v_pk_mul_f32 v[206:207], v[238:239], v[206:207] op_sel:[0,0] op_sel_hi:[1,1]
	v_pk_mul_f32 v[208:209], v[240:241], v[208:209] op_sel:[0,0] op_sel_hi:[1,1]
	v_pk_fma_f32 v[128:129], v[214:215], v[132:133], v[206:207] op_sel:[0,0,0] op_sel_hi:[1,1,1]
	v_pk_fma_f32 v[130:131], v[216:217], v[134:135], v[208:209] op_sel:[0,0,0] op_sel_hi:[1,1,1]
	v_pk_mul_f32 v[144:145], v[148:149], v[214:215] op_sel:[0,0] op_sel_hi:[1,1]
	v_pk_mul_f32 v[146:147], v[150:151], v[216:217] op_sel:[0,0] op_sel_hi:[1,1]
	v_pk_add_f32 v[202:203], v[112:113], v[72:73] op_sel:[0,0] op_sel_hi:[1,1]
	v_pk_add_f32 v[204:205], v[114:115], v[74:75] op_sel:[0,0] op_sel_hi:[1,1]
	v_pk_add_f32 v[206:207], v[84:85], v[104:105] op_sel:[0,0] op_sel_hi:[1,1]
	v_pk_add_f32 v[208:209], v[86:87], v[106:107] op_sel:[0,0] op_sel_hi:[1,1]
	v_pk_mul_f32 v[202:203], v[202:203], v[246:247] op_sel:[0,0] op_sel_hi:[1,0]
	v_pk_mul_f32 v[204:205], v[204:205], v[246:247] op_sel:[0,0] op_sel_hi:[1,0]
	v_pk_mul_f32 v[206:207], v[206:207], v[246:247] op_sel:[0,0] op_sel_hi:[1,0]
	v_pk_mul_f32 v[208:209], v[208:209], v[246:247] op_sel:[0,0] op_sel_hi:[1,0]
	v_exp_f32_e32 v202, v202
	v_exp_f32_e32 v203, v203
	v_exp_f32_e32 v204, v204
	v_exp_f32_e32 v205, v205
	v_exp_f32_e32 v206, v206
	v_exp_f32_e32 v207, v207
	v_exp_f32_e32 v208, v208
	v_exp_f32_e32 v209, v209
	v_pk_add_f32 v[202:203], v[202:203], v[248:249] op_sel:[0,0] op_sel_hi:[1,0]
	v_pk_add_f32 v[204:205], v[204:205], v[248:249] op_sel:[0,0] op_sel_hi:[1,0]
	v_pk_add_f32 v[206:207], v[206:207], v[248:249] op_sel:[0,0] op_sel_hi:[1,0]
	v_pk_add_f32 v[208:209], v[208:209], v[248:249] op_sel:[0,0] op_sel_hi:[1,0]
	v_rcp_f32_e32 v202, v202
	v_rcp_f32_e32 v203, v203
	v_rcp_f32_e32 v204, v204
	v_rcp_f32_e32 v205, v205
	v_rcp_f32_e32 v206, v206
	v_rcp_f32_e32 v207, v207
	v_rcp_f32_e32 v208, v208
	v_rcp_f32_e32 v209, v209
	v_lshlrev_b32_e32 v242, 16, v172
	v_and_b32_e32 v243, s22, v172
	v_lshlrev_b32_e32 v244, 16, v173
	v_and_b32_e32 v245, s22, v173
	v_pk_mul_f32 v[210:211], v[202:203], v[198:199] op_sel:[0,0] op_sel_hi:[1,1]
	v_pk_mul_f32 v[212:213], v[204:205], v[200:201] op_sel:[0,0] op_sel_hi:[1,1]
	v_pk_mul_f32 v[206:207], v[206:207], v[242:243] op_sel:[0,0] op_sel_hi:[1,1]
	v_pk_mul_f32 v[208:209], v[208:209], v[244:245] op_sel:[0,0] op_sel_hi:[1,1]
; __device__ __forceinline__ float fast_exp(float x) { return __builtin_amdgcn_exp2f(x * 1.4426950408889634f); }
; __device__ __forceinline__ float fast_sigmoid(float x) { return __builtin_amdgcn_rcpf(1.0f + fast_exp(-x)); }
;     __device__ __forceinline__ void operator()(Acc& acc, const Unit& u, int wr, int wc, int fr_, int fq_, LAS unsigned char* le, int wid, int lane, int&) const {
;     ...
;                     const f32x4 ba = *(const f32x4*)(b_a + ch0 + n * 16), bi = *(const f32x4*)(b_i + ch0 + n * 16), sl = *(const f32x4*)(spl + ch0 + n * 16);
;                     const u32x2 xw = xpre[ai][m][n]; const float xv[4] = {bflo(xw.x), bfhi(xw.x), bflo(xw.y), bfhi(xw.y)};
;                     const f32x4 ra = acc[ai][0][m][n] + ba, ri = acc[ai][1][m][n] + bi;
; #pragma unroll
;                     for (int j = 0; j < 4; ++j) { const float r = fast_sigmoid(ra[j]), ig = fast_sigmoid(ri[j]);
;                         const float la = -8.0f * r * sl[j];
;                         const float a = fast_exp(la); const float x2 = 2.0f * la;
;                         const float ser = -x2 * (1.0f + x2 * (0.5f + x2 * (1.0f / 6.0f + x2 * (1.0f / 24.0f + x2 * (1.0f / 120.0f)))));
;                         const float om = (x2 > -0.3f) ? ser : (1.0f - a * a);
;                         const float uu = __builtin_amdgcn_sqrtf(om) * (ig * xv[j]);
;                         if (m == 0) { acc[ai][0][m][n][j] = a; acc[ai][1][m][n][j] = uu; }
;                         else { acc[ai][1][m][n][j] = a * acc[ai][1][m - 1][n][j] + uu; acc[ai][0][m][n][j] = acc[ai][0][m - 1][n][j] * a; } } } }
	v_pk_mul_f32 v[214:215], v[210:211], v[246:247] op_sel:[0,1] op_sel_hi:[1,1]
	v_pk_mul_f32 v[216:217], v[212:213], v[246:247] op_sel:[0,1] op_sel_hi:[1,1]
	v_pk_add_f32 v[210:211], v[210:211], v[210:211] op_sel:[0,0] op_sel_hi:[1,1]
	v_pk_add_f32 v[212:213], v[212:213], v[212:213] op_sel:[0,0] op_sel_hi:[1,1]
	v_exp_f32_e32 v214, v214
	v_exp_f32_e32 v215, v215
	v_exp_f32_e32 v216, v216
	v_exp_f32_e32 v217, v217
	v_pk_fma_f32 v[238:239], v[210:211], v[248:249], v[250:251] op_sel:[0,1,0] op_sel_hi:[1,1,0]
	v_pk_fma_f32 v[240:241], v[212:213], v[248:249], v[250:251] op_sel:[0,1,0] op_sel_hi:[1,1,0]
	v_pk_fma_f32 v[238:239], v[210:211], v[238:239], v[250:251] op_sel:[0,0,1] op_sel_hi:[1,1,1]
	v_pk_fma_f32 v[240:241], v[212:213], v[240:241], v[250:251] op_sel:[0,0,1] op_sel_hi:[1,1,1]
	v_pk_fma_f32 v[238:239], v[210:211], v[238:239], v[252:253] op_sel:[0,0,0] op_sel_hi:[1,1,0]
	v_pk_fma_f32 v[240:241], v[212:213], v[240:241], v[252:253] op_sel:[0,0,0] op_sel_hi:[1,1,0]
	v_pk_fma_f32 v[238:239], v[210:211], v[238:239], v[248:249] op_sel:[0,0,0] op_sel_hi:[1,1,0]
	v_pk_fma_f32 v[240:241], v[212:213], v[240:241], v[248:249] op_sel:[0,0,0] op_sel_hi:[1,1,0]
	v_pk_mul_f32 v[238:239], v[210:211], v[238:239] op_sel:[0,0] op_sel_hi:[1,1] neg_lo:[1,0] neg_hi:[1,0]
	v_pk_mul_f32 v[240:241], v[212:213], v[240:241] op_sel:[0,0] op_sel_hi:[1,1] neg_lo:[1,0] neg_hi:[1,0]
	v_pk_fma_f32 v[242:243], v[214:215], v[214:215], v[248:249] op_sel:[0,0,0] op_sel_hi:[1,1,0] neg_lo:[1,0,0] neg_hi:[1,0,0]
	v_pk_fma_f32 v[244:245], v[216:217], v[216:217], v[248:249] op_sel:[0,0,0] op_sel_hi:[1,1,0] neg_lo:[1,0,0] neg_hi:[1,0,0]
	v_cmp_lt_f32_e64 s[24:25], v253, v210
	v_cmp_lt_f32_e64 s[26:27], v253, v211
	v_cmp_lt_f32_e64 s[30:31], v253, v212
	v_cmp_lt_f32_e64 s[34:35], v253, v213
	v_cndmask_b32_e64 v238, v242, v238, s[24:25]
	v_cndmask_b32_e64 v239, v243, v239, s[26:27]
	v_cndmask_b32_e64 v240, v244, v240, s[30:31]
	v_cndmask_b32_e64 v241, v245, v241, s[34:35]
	v_sqrt_f32_e32 v238, v238
	v_sqrt_f32_e32 v239, v239
	v_sqrt_f32_e32 v240, v240
	v_sqrt_f32_e32 v241, v241
	v_pk_mul_f32 v[206:207], v[238:239], v[206:207] op_sel:[0,0] op_sel_hi:[1,1]
	v_pk_mul_f32 v[208:209], v[240:241], v[208:209] op_sel:[0,0] op_sel_hi:[1,1]
	v_pk_fma_f32 v[84:85], v[214:215], v[92:93], v[206:207] op_sel:[0,0,0] op_sel_hi:[1,1,1]
	v_pk_fma_f32 v[86:87], v[216:217], v[94:95], v[208:209] op_sel:[0,0,0] op_sel_hi:[1,1,1]
	v_pk_mul_f32 v[112:113], v[116:117], v[214:215] op_sel:[0,0] op_sel_hi:[1,1]
	v_pk_mul_f32 v[114:115], v[118:119], v[216:217] op_sel:[0,0] op_sel_hi:[1,1]
	v_pk_add_f32 v[202:203], v[140:141], v[68:69] op_sel:[0,0] op_sel_hi:[1,1]
	v_pk_add_f32 v[204:205], v[142:143], v[70:71] op_sel:[0,0] op_sel_hi:[1,1]
	v_pk_add_f32 v[206:207], v[124:125], v[100:101] op_sel:[0,0] op_sel_hi:[1,1]
	v_pk_add_f32 v[208:209], v[126:127], v[102:103] op_sel:[0,0] op_sel_hi:[1,1]
	v_pk_mul_f32 v[202:203], v[202:203], v[246:247] op_sel:[0,0] op_sel_hi:[1,0]
	v_pk_mul_f32 v[204:205], v[204:205], v[246:247] op_sel:[0,0] op_sel_hi:[1,0]
	v_pk_mul_f32 v[206:207], v[206:207], v[246:247] op_sel:[0,0] op_sel_hi:[1,0]
	v_pk_mul_f32 v[208:209], v[208:209], v[246:247] op_sel:[0,0] op_sel_hi:[1,0]
	v_exp_f32_e32 v202, v202
	v_exp_f32_e32 v203, v203
	v_exp_f32_e32 v204, v204
	v_exp_f32_e32 v205, v205
	v_exp_f32_e32 v206, v206
	v_exp_f32_e32 v207, v207
	v_exp_f32_e32 v208, v208
	v_exp_f32_e32 v209, v209
	v_pk_add_f32 v[202:203], v[202:203], v[248:249] op_sel:[0,0] op_sel_hi:[1,0]
	v_pk_add_f32 v[204:205], v[204:205], v[248:249] op_sel:[0,0] op_sel_hi:[1,0]
	v_pk_add_f32 v[206:207], v[206:207], v[248:249] op_sel:[0,0] op_sel_hi:[1,0]
	v_pk_add_f32 v[208:209], v[208:209], v[248:249] op_sel:[0,0] op_sel_hi:[1,0]
	v_rcp_f32_e32 v202, v202
	v_rcp_f32_e32 v203, v203
	v_rcp_f32_e32 v204, v204
	v_rcp_f32_e32 v205, v205
	v_rcp_f32_e32 v206, v206
	v_rcp_f32_e32 v207, v207
	v_rcp_f32_e32 v208, v208
	v_rcp_f32_e32 v209, v209
	v_lshlrev_b32_e32 v242, 16, v174
	v_and_b32_e32 v243, s22, v174
	v_lshlrev_b32_e32 v244, 16, v175
	v_and_b32_e32 v245, s22, v175
	v_pk_mul_f32 v[210:211], v[202:203], v[88:89] op_sel:[0,0] op_sel_hi:[1,1]
	v_pk_mul_f32 v[212:213], v[204:205], v[90:91] op_sel:[0,0] op_sel_hi:[1,1]
	v_pk_mul_f32 v[206:207], v[206:207], v[242:243] op_sel:[0,0] op_sel_hi:[1,1]
	v_pk_mul_f32 v[208:209], v[208:209], v[244:245] op_sel:[0,0] op_sel_hi:[1,1]
	v_pk_mul_f32 v[214:215], v[210:211], v[246:247] op_sel:[0,1] op_sel_hi:[1,1]
	v_pk_mul_f32 v[216:217], v[212:213], v[246:247] op_sel:[0,1] op_sel_hi:[1,1]
	v_pk_add_f32 v[210:211], v[210:211], v[210:211] op_sel:[0,0] op_sel_hi:[1,1]
	v_pk_add_f32 v[212:213], v[212:213], v[212:213] op_sel:[0,0] op_sel_hi:[1,1]
	v_exp_f32_e32 v214, v214
	v_exp_f32_e32 v215, v215
	v_exp_f32_e32 v216, v216
	v_exp_f32_e32 v217, v217
	v_pk_fma_f32 v[238:239], v[210:211], v[248:249], v[250:251] op_sel:[0,1,0] op_sel_hi:[1,1,0]
	v_pk_fma_f32 v[240:241], v[212:213], v[248:249], v[250:251] op_sel:[0,1,0] op_sel_hi:[1,1,0]
	v_pk_fma_f32 v[238:239], v[210:211], v[238:239], v[250:251] op_sel:[0,0,1] op_sel_hi:[1,1,1]
	v_pk_fma_f32 v[240:241], v[212:213], v[240:241], v[250:251] op_sel:[0,0,1] op_sel_hi:[1,1,1]
	v_pk_fma_f32 v[238:239], v[210:211], v[238:239], v[252:253] op_sel:[0,0,0] op_sel_hi:[1,1,0]
	v_pk_fma_f32 v[240:241], v[212:213], v[240:241], v[252:253] op_sel:[0,0,0] op_sel_hi:[1,1,0]
	v_pk_fma_f32 v[238:239], v[210:211], v[238:239], v[248:249] op_sel:[0,0,0] op_sel_hi:[1,1,0]
	v_pk_fma_f32 v[240:241], v[212:213], v[240:241], v[248:249] op_sel:[0,0,0] op_sel_hi:[1,1,0]
	v_pk_mul_f32 v[238:239], v[210:211], v[238:239] op_sel:[0,0] op_sel_hi:[1,1] neg_lo:[1,0] neg_hi:[1,0]
; __device__ __forceinline__ float fast_exp(float x) { return __builtin_amdgcn_exp2f(x * 1.4426950408889634f); }
; __device__ __forceinline__ float fast_sigmoid(float x) { return __builtin_amdgcn_rcpf(1.0f + fast_exp(-x)); }
;     __device__ __forceinline__ void operator()(Acc& acc, const Unit& u, int wr, int wc, int fr_, int fq_, LAS unsigned char* le, int wid, int lane, int&) const {
;     ...
;                     const f32x4 ba = *(const f32x4*)(b_a + ch0 + n * 16), bi = *(const f32x4*)(b_i + ch0 + n * 16), sl = *(const f32x4*)(spl + ch0 + n * 16);
;                     const u32x2 xw = xpre[ai][m][n]; const float xv[4] = {bflo(xw.x), bfhi(xw.x), bflo(xw.y), bfhi(xw.y)};
;                     const f32x4 ra = acc[ai][0][m][n] + ba, ri = acc[ai][1][m][n] + bi;
; #pragma unroll
;                     for (int j = 0; j < 4; ++j) { const float r = fast_sigmoid(ra[j]), ig = fast_sigmoid(ri[j]);
;                         const float la = -8.0f * r * sl[j];
;                         const float a = fast_exp(la); const float x2 = 2.0f * la;
;                         const float ser = -x2 * (1.0f + x2 * (0.5f + x2 * (1.0f / 6.0f + x2 * (1.0f / 24.0f + x2 * (1.0f / 120.0f)))));
;                         const float om = (x2 > -0.3f) ? ser : (1.0f - a * a);
;                         const float uu = __builtin_amdgcn_sqrtf(om) * (ig * xv[j]);
;                         if (m == 0) { acc[ai][0][m][n][j] = a; acc[ai][1][m][n][j] = uu; }
;                         else { acc[ai][1][m][n][j] = a * acc[ai][1][m - 1][n][j] + uu; acc[ai][0][m][n][j] = acc[ai][0][m - 1][n][j] * a; } } } }
	v_pk_mul_f32 v[240:241], v[212:213], v[240:241] op_sel:[0,0] op_sel_hi:[1,1] neg_lo:[1,0] neg_hi:[1,0]
	v_pk_fma_f32 v[242:243], v[214:215], v[214:215], v[248:249] op_sel:[0,0,0] op_sel_hi:[1,1,0] neg_lo:[1,0,0] neg_hi:[1,0,0]
	v_pk_fma_f32 v[244:245], v[216:217], v[216:217], v[248:249] op_sel:[0,0,0] op_sel_hi:[1,1,0] neg_lo:[1,0,0] neg_hi:[1,0,0]
	v_cmp_lt_f32_e64 s[24:25], v253, v210
	v_cmp_lt_f32_e64 s[26:27], v253, v211
	v_cmp_lt_f32_e64 s[30:31], v253, v212
	v_cmp_lt_f32_e64 s[34:35], v253, v213
	v_cndmask_b32_e64 v238, v242, v238, s[24:25]
	v_cndmask_b32_e64 v239, v243, v239, s[26:27]
	v_cndmask_b32_e64 v240, v244, v240, s[30:31]
	v_cndmask_b32_e64 v241, v245, v241, s[34:35]
	v_sqrt_f32_e32 v238, v238
	v_sqrt_f32_e32 v239, v239
	v_sqrt_f32_e32 v240, v240
	v_sqrt_f32_e32 v241, v241
	v_pk_mul_f32 v[206:207], v[238:239], v[206:207] op_sel:[0,0] op_sel_hi:[1,1]
	v_pk_mul_f32 v[208:209], v[240:241], v[208:209] op_sel:[0,0] op_sel_hi:[1,1]
	v_pk_fma_f32 v[124:125], v[214:215], v[128:129], v[206:207] op_sel:[0,0,0] op_sel_hi:[1,1,1]
	v_pk_fma_f32 v[126:127], v[216:217], v[130:131], v[208:209] op_sel:[0,0,0] op_sel_hi:[1,1,1]
	v_pk_mul_f32 v[140:141], v[144:145], v[214:215] op_sel:[0,0] op_sel_hi:[1,1]
	v_pk_mul_f32 v[142:143], v[146:147], v[216:217] op_sel:[0,0] op_sel_hi:[1,1]
	v_pk_add_f32 v[202:203], v[108:109], v[72:73] op_sel:[0,0] op_sel_hi:[1,1]
	v_pk_add_f32 v[204:205], v[110:111], v[74:75] op_sel:[0,0] op_sel_hi:[1,1]
	v_pk_add_f32 v[206:207], v[80:81], v[104:105] op_sel:[0,0] op_sel_hi:[1,1]
	v_pk_add_f32 v[208:209], v[82:83], v[106:107] op_sel:[0,0] op_sel_hi:[1,1]
	v_pk_mul_f32 v[202:203], v[202:203], v[246:247] op_sel:[0,0] op_sel_hi:[1,0]
	v_pk_mul_f32 v[204:205], v[204:205], v[246:247] op_sel:[0,0] op_sel_hi:[1,0]
	v_pk_mul_f32 v[206:207], v[206:207], v[246:247] op_sel:[0,0] op_sel_hi:[1,0]
	v_pk_mul_f32 v[208:209], v[208:209], v[246:247] op_sel:[0,0] op_sel_hi:[1,0]
	v_exp_f32_e32 v202, v202
	v_exp_f32_e32 v203, v203
	v_exp_f32_e32 v204, v204
	v_exp_f32_e32 v205, v205
	v_exp_f32_e32 v206, v206
	v_exp_f32_e32 v207, v207
	v_exp_f32_e32 v208, v208
	v_exp_f32_e32 v209, v209
	v_pk_add_f32 v[202:203], v[202:203], v[248:249] op_sel:[0,0] op_sel_hi:[1,0]
	v_pk_add_f32 v[204:205], v[204:205], v[248:249] op_sel:[0,0] op_sel_hi:[1,0]
	v_pk_add_f32 v[206:207], v[206:207], v[248:249] op_sel:[0,0] op_sel_hi:[1,0]
	v_pk_add_f32 v[208:209], v[208:209], v[248:249] op_sel:[0,0] op_sel_hi:[1,0]
	v_rcp_f32_e32 v202, v202
	v_rcp_f32_e32 v203, v203
	v_rcp_f32_e32 v204, v204
	v_rcp_f32_e32 v205, v205
	v_rcp_f32_e32 v206, v206
	v_rcp_f32_e32 v207, v207
	v_rcp_f32_e32 v208, v208
	v_rcp_f32_e32 v209, v209
	v_lshlrev_b32_e32 v242, 16, v176
	v_and_b32_e32 v243, s22, v176
	v_lshlrev_b32_e32 v244, 16, v177
	v_and_b32_e32 v245, s22, v177
	v_pk_mul_f32 v[210:211], v[202:203], v[198:199] op_sel:[0,0] op_sel_hi:[1,1]
	v_pk_mul_f32 v[212:213], v[204:205], v[200:201] op_sel:[0,0] op_sel_hi:[1,1]
	v_pk_mul_f32 v[206:207], v[206:207], v[242:243] op_sel:[0,0] op_sel_hi:[1,1]
	v_pk_mul_f32 v[208:209], v[208:209], v[244:245] op_sel:[0,0] op_sel_hi:[1,1]
	v_pk_mul_f32 v[214:215], v[210:211], v[246:247] op_sel:[0,1] op_sel_hi:[1,1]
	v_pk_mul_f32 v[216:217], v[212:213], v[246:247] op_sel:[0,1] op_sel_hi:[1,1]
	v_pk_add_f32 v[210:211], v[210:211], v[210:211] op_sel:[0,0] op_sel_hi:[1,1]
	v_pk_add_f32 v[212:213], v[212:213], v[212:213] op_sel:[0,0] op_sel_hi:[1,1]
	v_exp_f32_e32 v214, v214
	v_exp_f32_e32 v215, v215
	v_exp_f32_e32 v216, v216
	v_exp_f32_e32 v217, v217
	v_pk_fma_f32 v[238:239], v[210:211], v[248:249], v[250:251] op_sel:[0,1,0] op_sel_hi:[1,1,0]
	v_pk_fma_f32 v[240:241], v[212:213], v[248:249], v[250:251] op_sel:[0,1,0] op_sel_hi:[1,1,0]
	v_pk_fma_f32 v[238:239], v[210:211], v[238:239], v[250:251] op_sel:[0,0,1] op_sel_hi:[1,1,1]
	v_pk_fma_f32 v[240:241], v[212:213], v[240:241], v[250:251] op_sel:[0,0,1] op_sel_hi:[1,1,1]
	v_pk_fma_f32 v[238:239], v[210:211], v[238:239], v[252:253] op_sel:[0,0,0] op_sel_hi:[1,1,0]
	v_pk_fma_f32 v[240:241], v[212:213], v[240:241], v[252:253] op_sel:[0,0,0] op_sel_hi:[1,1,0]
	v_pk_fma_f32 v[238:239], v[210:211], v[238:239], v[248:249] op_sel:[0,0,0] op_sel_hi:[1,1,0]
	v_pk_fma_f32 v[240:241], v[212:213], v[240:241], v[248:249] op_sel:[0,0,0] op_sel_hi:[1,1,0]
	v_pk_mul_f32 v[238:239], v[210:211], v[238:239] op_sel:[0,0] op_sel_hi:[1,1] neg_lo:[1,0] neg_hi:[1,0]
	v_pk_mul_f32 v[240:241], v[212:213], v[240:241] op_sel:[0,0] op_sel_hi:[1,1] neg_lo:[1,0] neg_hi:[1,0]
	v_pk_fma_f32 v[242:243], v[214:215], v[214:215], v[248:249] op_sel:[0,0,0] op_sel_hi:[1,1,0] neg_lo:[1,0,0] neg_hi:[1,0,0]
	v_pk_fma_f32 v[244:245], v[216:217], v[216:217], v[248:249] op_sel:[0,0,0] op_sel_hi:[1,1,0] neg_lo:[1,0,0] neg_hi:[1,0,0]
	v_cmp_lt_f32_e64 s[24:25], v253, v210
	v_cmp_lt_f32_e64 s[26:27], v253, v211
	v_cmp_lt_f32_e64 s[30:31], v253, v212
	v_cmp_lt_f32_e64 s[34:35], v253, v213
	v_cndmask_b32_e64 v238, v242, v238, s[24:25]
	v_cndmask_b32_e64 v239, v243, v239, s[26:27]
	v_cndmask_b32_e64 v240, v244, v240, s[30:31]
	v_cndmask_b32_e64 v241, v245, v241, s[34:35]
	v_sqrt_f32_e32 v238, v238
	v_sqrt_f32_e32 v239, v239
	v_sqrt_f32_e32 v240, v240
	v_sqrt_f32_e32 v241, v241
	v_pk_mul_f32 v[206:207], v[238:239], v[206:207] op_sel:[0,0] op_sel_hi:[1,1]
	v_pk_mul_f32 v[208:209], v[240:241], v[208:209] op_sel:[0,0] op_sel_hi:[1,1]
	v_pk_fma_f32 v[80:81], v[214:215], v[84:85], v[206:207] op_sel:[0,0,0] op_sel_hi:[1,1,1]
	v_pk_fma_f32 v[82:83], v[216:217], v[86:87], v[208:209] op_sel:[0,0,0] op_sel_hi:[1,1,1]
	v_pk_mul_f32 v[108:109], v[112:113], v[214:215] op_sel:[0,0] op_sel_hi:[1,1]
	v_pk_mul_f32 v[110:111], v[114:115], v[216:217] op_sel:[0,0] op_sel_hi:[1,1]
; __device__ __forceinline__ float fast_exp(float x) { return __builtin_amdgcn_exp2f(x * 1.4426950408889634f); }
; __device__ __forceinline__ float fast_sigmoid(float x) { return __builtin_amdgcn_rcpf(1.0f + fast_exp(-x)); }
;     __device__ __forceinline__ void operator()(Acc& acc, const Unit& u, int wr, int wc, int fr_, int fq_, LAS unsigned char* le, int wid, int lane, int&) const {
;     ...
;                     const f32x4 ba = *(const f32x4*)(b_a + ch0 + n * 16), bi = *(const f32x4*)(b_i + ch0 + n * 16), sl = *(const f32x4*)(spl + ch0 + n * 16);
;                     const u32x2 xw = xpre[ai][m][n]; const float xv[4] = {bflo(xw.x), bfhi(xw.x), bflo(xw.y), bfhi(xw.y)};
;                     const f32x4 ra = acc[ai][0][m][n] + ba, ri = acc[ai][1][m][n] + bi;
; #pragma unroll
;                     for (int j = 0; j < 4; ++j) { const float r = fast_sigmoid(ra[j]), ig = fast_sigmoid(ri[j]);
;                         const float la = -8.0f * r * sl[j];
;                         const float a = fast_exp(la); const float x2 = 2.0f * la;
;                         const float ser = -x2 * (1.0f + x2 * (0.5f + x2 * (1.0f / 6.0f + x2 * (1.0f / 24.0f + x2 * (1.0f / 120.0f)))));
;                         const float om = (x2 > -0.3f) ? ser : (1.0f - a * a);
;                         const float uu = __builtin_amdgcn_sqrtf(om) * (ig * xv[j]);
;                         if (m == 0) { acc[ai][0][m][n][j] = a; acc[ai][1][m][n][j] = uu; }
;                         else { acc[ai][1][m][n][j] = a * acc[ai][1][m - 1][n][j] + uu; acc[ai][0][m][n][j] = acc[ai][0][m - 1][n][j] * a; } } } }
	v_pk_add_f32 v[202:203], v[136:137], v[68:69] op_sel:[0,0] op_sel_hi:[1,1]
	v_pk_add_f32 v[204:205], v[138:139], v[70:71] op_sel:[0,0] op_sel_hi:[1,1]
	v_pk_add_f32 v[206:207], v[120:121], v[100:101] op_sel:[0,0] op_sel_hi:[1,1]
	v_pk_add_f32 v[208:209], v[122:123], v[102:103] op_sel:[0,0] op_sel_hi:[1,1]
	v_pk_mul_f32 v[202:203], v[202:203], v[246:247] op_sel:[0,0] op_sel_hi:[1,0]
	v_pk_mul_f32 v[204:205], v[204:205], v[246:247] op_sel:[0,0] op_sel_hi:[1,0]
	v_pk_mul_f32 v[206:207], v[206:207], v[246:247] op_sel:[0,0] op_sel_hi:[1,0]
	v_pk_mul_f32 v[208:209], v[208:209], v[246:247] op_sel:[0,0] op_sel_hi:[1,0]
	v_exp_f32_e32 v202, v202
	v_exp_f32_e32 v203, v203
	v_exp_f32_e32 v204, v204
	v_exp_f32_e32 v205, v205
	v_exp_f32_e32 v206, v206
	v_exp_f32_e32 v207, v207
	v_exp_f32_e32 v208, v208
	v_exp_f32_e32 v209, v209
	v_pk_add_f32 v[202:203], v[202:203], v[248:249] op_sel:[0,0] op_sel_hi:[1,0]
	v_pk_add_f32 v[204:205], v[204:205], v[248:249] op_sel:[0,0] op_sel_hi:[1,0]
	v_pk_add_f32 v[206:207], v[206:207], v[248:249] op_sel:[0,0] op_sel_hi:[1,0]
	v_pk_add_f32 v[208:209], v[208:209], v[248:249] op_sel:[0,0] op_sel_hi:[1,0]
	v_rcp_f32_e32 v202, v202
	v_rcp_f32_e32 v203, v203
	v_rcp_f32_e32 v204, v204
	v_rcp_f32_e32 v205, v205
	v_rcp_f32_e32 v206, v206
	v_rcp_f32_e32 v207, v207
	v_rcp_f32_e32 v208, v208
	v_rcp_f32_e32 v209, v209
	v_lshlrev_b32_e32 v242, 16, v178
	v_and_b32_e32 v243, s22, v178
	v_lshlrev_b32_e32 v244, 16, v179
	v_and_b32_e32 v245, s22, v179
	v_pk_mul_f32 v[210:211], v[202:203], v[88:89] op_sel:[0,0] op_sel_hi:[1,1]
	v_pk_mul_f32 v[212:213], v[204:205], v[90:91] op_sel:[0,0] op_sel_hi:[1,1]
	v_pk_mul_f32 v[206:207], v[206:207], v[242:243] op_sel:[0,0] op_sel_hi:[1,1]
	v_pk_mul_f32 v[208:209], v[208:209], v[244:245] op_sel:[0,0] op_sel_hi:[1,1]
	v_pk_mul_f32 v[214:215], v[210:211], v[246:247] op_sel:[0,1] op_sel_hi:[1,1]
	v_pk_mul_f32 v[216:217], v[212:213], v[246:247] op_sel:[0,1] op_sel_hi:[1,1]
	v_pk_add_f32 v[210:211], v[210:211], v[210:211] op_sel:[0,0] op_sel_hi:[1,1]
	v_pk_add_f32 v[212:213], v[212:213], v[212:213] op_sel:[0,0] op_sel_hi:[1,1]
	v_exp_f32_e32 v214, v214
	v_exp_f32_e32 v215, v215
	v_exp_f32_e32 v216, v216
	v_exp_f32_e32 v217, v217
	v_pk_fma_f32 v[238:239], v[210:211], v[248:249], v[250:251] op_sel:[0,1,0] op_sel_hi:[1,1,0]
	v_pk_fma_f32 v[240:241], v[212:213], v[248:249], v[250:251] op_sel:[0,1,0] op_sel_hi:[1,1,0]
	v_pk_fma_f32 v[238:239], v[210:211], v[238:239], v[250:251] op_sel:[0,0,1] op_sel_hi:[1,1,1]
	v_pk_fma_f32 v[240:241], v[212:213], v[240:241], v[250:251] op_sel:[0,0,1] op_sel_hi:[1,1,1]
	v_pk_fma_f32 v[238:239], v[210:211], v[238:239], v[252:253] op_sel:[0,0,0] op_sel_hi:[1,1,0]
	v_pk_fma_f32 v[240:241], v[212:213], v[240:241], v[252:253] op_sel:[0,0,0] op_sel_hi:[1,1,0]
	v_pk_fma_f32 v[238:239], v[210:211], v[238:239], v[248:249] op_sel:[0,0,0] op_sel_hi:[1,1,0]
	v_pk_fma_f32 v[240:241], v[212:213], v[240:241], v[248:249] op_sel:[0,0,0] op_sel_hi:[1,1,0]
	v_pk_mul_f32 v[238:239], v[210:211], v[238:239] op_sel:[0,0] op_sel_hi:[1,1] neg_lo:[1,0] neg_hi:[1,0]
	v_pk_mul_f32 v[240:241], v[212:213], v[240:241] op_sel:[0,0] op_sel_hi:[1,1] neg_lo:[1,0] neg_hi:[1,0]
	v_pk_fma_f32 v[242:243], v[214:215], v[214:215], v[248:249] op_sel:[0,0,0] op_sel_hi:[1,1,0] neg_lo:[1,0,0] neg_hi:[1,0,0]
	v_pk_fma_f32 v[244:245], v[216:217], v[216:217], v[248:249] op_sel:[0,0,0] op_sel_hi:[1,1,0] neg_lo:[1,0,0] neg_hi:[1,0,0]
	v_cmp_lt_f32_e64 s[24:25], v253, v210
	v_cmp_lt_f32_e64 s[26:27], v253, v211
	v_cmp_lt_f32_e64 s[30:31], v253, v212
	v_cmp_lt_f32_e64 s[34:35], v253, v213
	v_cndmask_b32_e64 v238, v242, v238, s[24:25]
	v_cndmask_b32_e64 v239, v243, v239, s[26:27]
	v_cndmask_b32_e64 v240, v244, v240, s[30:31]
	v_cndmask_b32_e64 v241, v245, v241, s[34:35]
	v_sqrt_f32_e32 v238, v238
	v_sqrt_f32_e32 v239, v239
	v_sqrt_f32_e32 v240, v240
	v_sqrt_f32_e32 v241, v241
	v_pk_mul_f32 v[206:207], v[238:239], v[206:207] op_sel:[0,0] op_sel_hi:[1,1]
	v_pk_mul_f32 v[208:209], v[240:241], v[208:209] op_sel:[0,0] op_sel_hi:[1,1]
	v_pk_fma_f32 v[120:121], v[214:215], v[124:125], v[206:207] op_sel:[0,0,0] op_sel_hi:[1,1,1]
	v_pk_fma_f32 v[122:123], v[216:217], v[126:127], v[208:209] op_sel:[0,0,0] op_sel_hi:[1,1,1]
	v_pk_mul_f32 v[136:137], v[140:141], v[214:215] op_sel:[0,0] op_sel_hi:[1,1]
	v_pk_mul_f32 v[138:139], v[142:143], v[216:217] op_sel:[0,0] op_sel_hi:[1,1]
	v_pk_add_f32 v[202:203], v[96:97], v[72:73] op_sel:[0,0] op_sel_hi:[1,1]
	v_pk_add_f32 v[204:205], v[98:99], v[74:75] op_sel:[0,0] op_sel_hi:[1,1]
	v_pk_add_f32 v[206:207], v[76:77], v[104:105] op_sel:[0,0] op_sel_hi:[1,1]
	v_pk_add_f32 v[208:209], v[78:79], v[106:107] op_sel:[0,0] op_sel_hi:[1,1]
	v_pk_mul_f32 v[202:203], v[202:203], v[246:247] op_sel:[0,0] op_sel_hi:[1,0]
	v_pk_mul_f32 v[204:205], v[204:205], v[246:247] op_sel:[0,0] op_sel_hi:[1,0]
	v_pk_mul_f32 v[206:207], v[206:207], v[246:247] op_sel:[0,0] op_sel_hi:[1,0]
	v_pk_mul_f32 v[208:209], v[208:209], v[246:247] op_sel:[0,0] op_sel_hi:[1,0]
	v_exp_f32_e32 v202, v202
	v_exp_f32_e32 v203, v203
	v_exp_f32_e32 v204, v204
	v_exp_f32_e32 v205, v205
	v_exp_f32_e32 v206, v206
	v_exp_f32_e32 v207, v207
	v_exp_f32_e32 v208, v208
	v_exp_f32_e32 v209, v209
	v_pk_add_f32 v[202:203], v[202:203], v[248:249] op_sel:[0,0] op_sel_hi:[1,0]
	v_pk_add_f32 v[204:205], v[204:205], v[248:249] op_sel:[0,0] op_sel_hi:[1,0]
	v_pk_add_f32 v[206:207], v[206:207], v[248:249] op_sel:[0,0] op_sel_hi:[1,0]
	v_pk_add_f32 v[208:209], v[208:209], v[248:249] op_sel:[0,0] op_sel_hi:[1,0]
	v_rcp_f32_e32 v202, v202
	v_rcp_f32_e32 v203, v203
	v_rcp_f32_e32 v204, v204
	v_rcp_f32_e32 v205, v205
	v_rcp_f32_e32 v206, v206
	v_rcp_f32_e32 v207, v207
; __device__ __forceinline__ float fast_exp(float x) { return __builtin_amdgcn_exp2f(x * 1.4426950408889634f); }
; __device__ __forceinline__ float fast_sigmoid(float x) { return __builtin_amdgcn_rcpf(1.0f + fast_exp(-x)); }
;     __device__ __forceinline__ void operator()(Acc& acc, const Unit& u, int wr, int wc, int fr_, int fq_, LAS unsigned char* le, int wid, int lane, int&) const {
;     ...
;                     const f32x4 ba = *(const f32x4*)(b_a + ch0 + n * 16), bi = *(const f32x4*)(b_i + ch0 + n * 16), sl = *(const f32x4*)(spl + ch0 + n * 16);
;                     const u32x2 xw = xpre[ai][m][n]; const float xv[4] = {bflo(xw.x), bfhi(xw.x), bflo(xw.y), bfhi(xw.y)};
;                     const f32x4 ra = acc[ai][0][m][n] + ba, ri = acc[ai][1][m][n] + bi;
; #pragma unroll
;                     for (int j = 0; j < 4; ++j) { const float r = fast_sigmoid(ra[j]), ig = fast_sigmoid(ri[j]);
;                         const float la = -8.0f * r * sl[j];
;                         const float a = fast_exp(la); const float x2 = 2.0f * la;
;                         const float ser = -x2 * (1.0f + x2 * (0.5f + x2 * (1.0f / 6.0f + x2 * (1.0f / 24.0f + x2 * (1.0f / 120.0f)))));
;                         const float om = (x2 > -0.3f) ? ser : (1.0f - a * a);
;                         const float uu = __builtin_amdgcn_sqrtf(om) * (ig * xv[j]);
;                         if (m == 0) { acc[ai][0][m][n][j] = a; acc[ai][1][m][n][j] = uu; }
;                         else { acc[ai][1][m][n][j] = a * acc[ai][1][m - 1][n][j] + uu; acc[ai][0][m][n][j] = acc[ai][0][m - 1][n][j] * a; } } } }
	v_rcp_f32_e32 v208, v208
	v_rcp_f32_e32 v209, v209
	v_lshlrev_b32_e32 v242, 16, v180
	v_and_b32_e32 v243, s22, v180
	v_lshlrev_b32_e32 v244, 16, v181
	v_and_b32_e32 v245, s22, v181
	v_pk_mul_f32 v[210:211], v[202:203], v[198:199] op_sel:[0,0] op_sel_hi:[1,1]
	v_pk_mul_f32 v[212:213], v[204:205], v[200:201] op_sel:[0,0] op_sel_hi:[1,1]
	v_pk_mul_f32 v[206:207], v[206:207], v[242:243] op_sel:[0,0] op_sel_hi:[1,1]
	v_pk_mul_f32 v[208:209], v[208:209], v[244:245] op_sel:[0,0] op_sel_hi:[1,1]
	v_pk_mul_f32 v[214:215], v[210:211], v[246:247] op_sel:[0,1] op_sel_hi:[1,1]
	v_pk_mul_f32 v[216:217], v[212:213], v[246:247] op_sel:[0,1] op_sel_hi:[1,1]
	v_pk_add_f32 v[210:211], v[210:211], v[210:211] op_sel:[0,0] op_sel_hi:[1,1]
	v_pk_add_f32 v[212:213], v[212:213], v[212:213] op_sel:[0,0] op_sel_hi:[1,1]
	v_exp_f32_e32 v214, v214
	v_exp_f32_e32 v215, v215
	v_exp_f32_e32 v216, v216
	v_exp_f32_e32 v217, v217
	v_pk_fma_f32 v[238:239], v[210:211], v[248:249], v[250:251] op_sel:[0,1,0] op_sel_hi:[1,1,0]
	v_pk_fma_f32 v[240:241], v[212:213], v[248:249], v[250:251] op_sel:[0,1,0] op_sel_hi:[1,1,0]
	v_pk_fma_f32 v[238:239], v[210:211], v[238:239], v[250:251] op_sel:[0,0,1] op_sel_hi:[1,1,1]
	v_pk_fma_f32 v[240:241], v[212:213], v[240:241], v[250:251] op_sel:[0,0,1] op_sel_hi:[1,1,1]
	v_pk_fma_f32 v[238:239], v[210:211], v[238:239], v[252:253] op_sel:[0,0,0] op_sel_hi:[1,1,0]
	v_pk_fma_f32 v[240:241], v[212:213], v[240:241], v[252:253] op_sel:[0,0,0] op_sel_hi:[1,1,0]
	v_pk_fma_f32 v[238:239], v[210:211], v[238:239], v[248:249] op_sel:[0,0,0] op_sel_hi:[1,1,0]
	v_pk_fma_f32 v[240:241], v[212:213], v[240:241], v[248:249] op_sel:[0,0,0] op_sel_hi:[1,1,0]
	v_pk_mul_f32 v[238:239], v[210:211], v[238:239] op_sel:[0,0] op_sel_hi:[1,1] neg_lo:[1,0] neg_hi:[1,0]
	v_pk_mul_f32 v[240:241], v[212:213], v[240:241] op_sel:[0,0] op_sel_hi:[1,1] neg_lo:[1,0] neg_hi:[1,0]
	v_pk_fma_f32 v[242:243], v[214:215], v[214:215], v[248:249] op_sel:[0,0,0] op_sel_hi:[1,1,0] neg_lo:[1,0,0] neg_hi:[1,0,0]
	v_pk_fma_f32 v[244:245], v[216:217], v[216:217], v[248:249] op_sel:[0,0,0] op_sel_hi:[1,1,0] neg_lo:[1,0,0] neg_hi:[1,0,0]
	v_cmp_lt_f32_e64 s[24:25], v253, v210
	v_cmp_lt_f32_e64 s[26:27], v253, v211
	v_cmp_lt_f32_e64 s[30:31], v253, v212
	v_cmp_lt_f32_e64 s[34:35], v253, v213
	v_cndmask_b32_e64 v238, v242, v238, s[24:25]
	v_cndmask_b32_e64 v239, v243, v239, s[26:27]
	v_cndmask_b32_e64 v240, v244, v240, s[30:31]
	v_cndmask_b32_e64 v241, v245, v241, s[34:35]
	v_sqrt_f32_e32 v238, v238
	v_sqrt_f32_e32 v239, v239
	v_sqrt_f32_e32 v240, v240
	v_sqrt_f32_e32 v241, v241
	v_pk_mul_f32 v[206:207], v[238:239], v[206:207] op_sel:[0,0] op_sel_hi:[1,1]
	v_pk_mul_f32 v[208:209], v[240:241], v[208:209] op_sel:[0,0] op_sel_hi:[1,1]
	v_pk_fma_f32 v[76:77], v[214:215], v[80:81], v[206:207] op_sel:[0,0,0] op_sel_hi:[1,1,1]
	v_pk_fma_f32 v[78:79], v[216:217], v[82:83], v[208:209] op_sel:[0,0,0] op_sel_hi:[1,1,1]
	v_pk_mul_f32 v[96:97], v[108:109], v[214:215] op_sel:[0,0] op_sel_hi:[1,1]
	v_pk_mul_f32 v[98:99], v[110:111], v[216:217] op_sel:[0,0] op_sel_hi:[1,1]
	v_pk_add_f32 v[202:203], v[64:65], v[68:69] op_sel:[0,0] op_sel_hi:[1,1]
	v_pk_add_f32 v[204:205], v[66:67], v[70:71] op_sel:[0,0] op_sel_hi:[1,1]
	v_pk_add_f32 v[206:207], v[44:45], v[100:101] op_sel:[0,0] op_sel_hi:[1,1]
	v_pk_add_f32 v[208:209], v[46:47], v[102:103] op_sel:[0,0] op_sel_hi:[1,1]
	v_pk_mul_f32 v[202:203], v[202:203], v[246:247] op_sel:[0,0] op_sel_hi:[1,0]
	v_pk_mul_f32 v[204:205], v[204:205], v[246:247] op_sel:[0,0] op_sel_hi:[1,0]
	v_pk_mul_f32 v[206:207], v[206:207], v[246:247] op_sel:[0,0] op_sel_hi:[1,0]
	v_pk_mul_f32 v[208:209], v[208:209], v[246:247] op_sel:[0,0] op_sel_hi:[1,0]
	v_exp_f32_e32 v202, v202
	v_exp_f32_e32 v203, v203
	v_exp_f32_e32 v204, v204
	v_exp_f32_e32 v205, v205
	v_exp_f32_e32 v206, v206
	v_exp_f32_e32 v207, v207
	v_exp_f32_e32 v208, v208
	v_exp_f32_e32 v209, v209
	v_pk_add_f32 v[202:203], v[202:203], v[248:249] op_sel:[0,0] op_sel_hi:[1,0]
	v_pk_add_f32 v[204:205], v[204:205], v[248:249] op_sel:[0,0] op_sel_hi:[1,0]
	v_pk_add_f32 v[206:207], v[206:207], v[248:249] op_sel:[0,0] op_sel_hi:[1,0]
	v_pk_add_f32 v[208:209], v[208:209], v[248:249] op_sel:[0,0] op_sel_hi:[1,0]
	v_rcp_f32_e32 v202, v202
	v_rcp_f32_e32 v203, v203
	v_rcp_f32_e32 v204, v204
	v_rcp_f32_e32 v205, v205
	v_rcp_f32_e32 v206, v206
	v_rcp_f32_e32 v207, v207
	v_rcp_f32_e32 v208, v208
	v_rcp_f32_e32 v209, v209
	v_lshlrev_b32_e32 v242, 16, v182
	v_and_b32_e32 v243, s22, v182
	v_lshlrev_b32_e32 v244, 16, v183
	v_and_b32_e32 v245, s22, v183
	v_pk_mul_f32 v[210:211], v[202:203], v[88:89] op_sel:[0,0] op_sel_hi:[1,1]
	v_pk_mul_f32 v[212:213], v[204:205], v[90:91] op_sel:[0,0] op_sel_hi:[1,1]
	v_pk_mul_f32 v[206:207], v[206:207], v[242:243] op_sel:[0,0] op_sel_hi:[1,1]
	v_pk_mul_f32 v[208:209], v[208:209], v[244:245] op_sel:[0,0] op_sel_hi:[1,1]
	v_pk_mul_f32 v[214:215], v[210:211], v[246:247] op_sel:[0,1] op_sel_hi:[1,1]
	v_pk_mul_f32 v[216:217], v[212:213], v[246:247] op_sel:[0,1] op_sel_hi:[1,1]
	v_pk_add_f32 v[210:211], v[210:211], v[210:211] op_sel:[0,0] op_sel_hi:[1,1]
	v_pk_add_f32 v[212:213], v[212:213], v[212:213] op_sel:[0,0] op_sel_hi:[1,1]
	v_exp_f32_e32 v64, v214
	v_exp_f32_e32 v65, v215
	v_exp_f32_e32 v66, v216
	v_exp_f32_e32 v67, v217
	v_pk_fma_f32 v[238:239], v[210:211], v[248:249], v[250:251] op_sel:[0,1,0] op_sel_hi:[1,1,0]
	v_pk_fma_f32 v[240:241], v[212:213], v[248:249], v[250:251] op_sel:[0,1,0] op_sel_hi:[1,1,0]
	v_pk_fma_f32 v[238:239], v[210:211], v[238:239], v[250:251] op_sel:[0,0,1] op_sel_hi:[1,1,1]
	v_pk_fma_f32 v[240:241], v[212:213], v[240:241], v[250:251] op_sel:[0,0,1] op_sel_hi:[1,1,1]
; __device__ __forceinline__ float fast_exp(float x) { return __builtin_amdgcn_exp2f(x * 1.4426950408889634f); }
; __device__ __forceinline__ float fast_sigmoid(float x) { return __builtin_amdgcn_rcpf(1.0f + fast_exp(-x)); }
;     __device__ __forceinline__ void operator()(Acc& acc, const Unit& u, int wr, int wc, int fr_, int fq_, LAS unsigned char* le, int wid, int lane, int&) const {
;     ...
;                     const f32x4 ba = *(const f32x4*)(b_a + ch0 + n * 16), bi = *(const f32x4*)(b_i + ch0 + n * 16), sl = *(const f32x4*)(spl + ch0 + n * 16);
;                     const u32x2 xw = xpre[ai][m][n]; const float xv[4] = {bflo(xw.x), bfhi(xw.x), bflo(xw.y), bfhi(xw.y)};
;                     const f32x4 ra = acc[ai][0][m][n] + ba, ri = acc[ai][1][m][n] + bi;
; #pragma unroll
;                     for (int j = 0; j < 4; ++j) { const float r = fast_sigmoid(ra[j]), ig = fast_sigmoid(ri[j]);
;                         const float la = -8.0f * r * sl[j];
;                         const float a = fast_exp(la); const float x2 = 2.0f * la;
;                         const float ser = -x2 * (1.0f + x2 * (0.5f + x2 * (1.0f / 6.0f + x2 * (1.0f / 24.0f + x2 * (1.0f / 120.0f)))));
;                         const float om = (x2 > -0.3f) ? ser : (1.0f - a * a);
;                         const float uu = __builtin_amdgcn_sqrtf(om) * (ig * xv[j]);
;                         if (m == 0) { acc[ai][0][m][n][j] = a; acc[ai][1][m][n][j] = uu; }
;                         else { acc[ai][1][m][n][j] = a * acc[ai][1][m - 1][n][j] + uu; acc[ai][0][m][n][j] = acc[ai][0][m - 1][n][j] * a; } } } }
	v_pk_fma_f32 v[238:239], v[210:211], v[238:239], v[252:253] op_sel:[0,0,0] op_sel_hi:[1,1,0]
	v_pk_fma_f32 v[240:241], v[212:213], v[240:241], v[252:253] op_sel:[0,0,0] op_sel_hi:[1,1,0]
	v_pk_fma_f32 v[238:239], v[210:211], v[238:239], v[248:249] op_sel:[0,0,0] op_sel_hi:[1,1,0]
	v_pk_fma_f32 v[240:241], v[212:213], v[240:241], v[248:249] op_sel:[0,0,0] op_sel_hi:[1,1,0]
	v_pk_mul_f32 v[238:239], v[210:211], v[238:239] op_sel:[0,0] op_sel_hi:[1,1] neg_lo:[1,0] neg_hi:[1,0]
	v_pk_mul_f32 v[240:241], v[212:213], v[240:241] op_sel:[0,0] op_sel_hi:[1,1] neg_lo:[1,0] neg_hi:[1,0]
	v_pk_fma_f32 v[242:243], v[64:65], v[64:65], v[248:249] op_sel:[0,0,0] op_sel_hi:[1,1,0] neg_lo:[1,0,0] neg_hi:[1,0,0]
	v_pk_fma_f32 v[244:245], v[66:67], v[66:67], v[248:249] op_sel:[0,0,0] op_sel_hi:[1,1,0] neg_lo:[1,0,0] neg_hi:[1,0,0]
	v_cmp_lt_f32_e64 s[24:25], v253, v210
	v_cmp_lt_f32_e64 s[26:27], v253, v211
	v_cmp_lt_f32_e64 s[30:31], v253, v212
	v_cmp_lt_f32_e64 s[34:35], v253, v213
	v_cndmask_b32_e64 v238, v242, v238, s[24:25]
	v_cndmask_b32_e64 v239, v243, v239, s[26:27]
	v_cndmask_b32_e64 v240, v244, v240, s[30:31]
	v_cndmask_b32_e64 v241, v245, v241, s[34:35]
	v_sqrt_f32_e32 v238, v238
	v_sqrt_f32_e32 v239, v239
	v_sqrt_f32_e32 v240, v240
	v_sqrt_f32_e32 v241, v241
	v_pk_mul_f32 v[44:45], v[238:239], v[206:207] op_sel:[0,0] op_sel_hi:[1,1]
	v_pk_mul_f32 v[46:47], v[240:241], v[208:209] op_sel:[0,0] op_sel_hi:[1,1]
	v_pk_add_f32 v[202:203], v[28:29], v[72:73] op_sel:[0,0] op_sel_hi:[1,1]
	v_pk_add_f32 v[204:205], v[30:31], v[74:75] op_sel:[0,0] op_sel_hi:[1,1]
	v_pk_add_f32 v[206:207], v[12:13], v[104:105] op_sel:[0,0] op_sel_hi:[1,1]
	v_pk_add_f32 v[208:209], v[14:15], v[106:107] op_sel:[0,0] op_sel_hi:[1,1]
	v_pk_mul_f32 v[202:203], v[202:203], v[246:247] op_sel:[0,0] op_sel_hi:[1,0]
	v_pk_mul_f32 v[204:205], v[204:205], v[246:247] op_sel:[0,0] op_sel_hi:[1,0]
	v_pk_mul_f32 v[206:207], v[206:207], v[246:247] op_sel:[0,0] op_sel_hi:[1,0]
	v_pk_mul_f32 v[208:209], v[208:209], v[246:247] op_sel:[0,0] op_sel_hi:[1,0]
	v_exp_f32_e32 v202, v202
	v_exp_f32_e32 v203, v203
	v_exp_f32_e32 v204, v204
	v_exp_f32_e32 v205, v205
	v_exp_f32_e32 v206, v206
	v_exp_f32_e32 v207, v207
	v_exp_f32_e32 v208, v208
	v_exp_f32_e32 v209, v209
	v_pk_add_f32 v[202:203], v[202:203], v[248:249] op_sel:[0,0] op_sel_hi:[1,0]
	v_pk_add_f32 v[204:205], v[204:205], v[248:249] op_sel:[0,0] op_sel_hi:[1,0]
	v_pk_add_f32 v[206:207], v[206:207], v[248:249] op_sel:[0,0] op_sel_hi:[1,0]
	v_pk_add_f32 v[208:209], v[208:209], v[248:249] op_sel:[0,0] op_sel_hi:[1,0]
	v_rcp_f32_e32 v202, v202
	v_rcp_f32_e32 v203, v203
	v_rcp_f32_e32 v204, v204
	v_rcp_f32_e32 v205, v205
	v_rcp_f32_e32 v206, v206
	v_rcp_f32_e32 v207, v207
	v_rcp_f32_e32 v208, v208
	v_rcp_f32_e32 v209, v209
	v_lshlrev_b32_e32 v242, 16, v184
	v_and_b32_e32 v243, s22, v184
	v_lshlrev_b32_e32 v244, 16, v185
	v_and_b32_e32 v245, s22, v185
	v_pk_mul_f32 v[210:211], v[202:203], v[198:199] op_sel:[0,0] op_sel_hi:[1,1]
	v_pk_mul_f32 v[212:213], v[204:205], v[200:201] op_sel:[0,0] op_sel_hi:[1,1]
	v_pk_mul_f32 v[206:207], v[206:207], v[242:243] op_sel:[0,0] op_sel_hi:[1,1]
	v_pk_mul_f32 v[208:209], v[208:209], v[244:245] op_sel:[0,0] op_sel_hi:[1,1]
	v_pk_mul_f32 v[214:215], v[210:211], v[246:247] op_sel:[0,1] op_sel_hi:[1,1]
	v_pk_mul_f32 v[216:217], v[212:213], v[246:247] op_sel:[0,1] op_sel_hi:[1,1]
	v_pk_add_f32 v[210:211], v[210:211], v[210:211] op_sel:[0,0] op_sel_hi:[1,1]
	v_pk_add_f32 v[212:213], v[212:213], v[212:213] op_sel:[0,0] op_sel_hi:[1,1]
	v_exp_f32_e32 v28, v214
	v_exp_f32_e32 v29, v215
	v_exp_f32_e32 v30, v216
	v_exp_f32_e32 v31, v217
	v_pk_fma_f32 v[238:239], v[210:211], v[248:249], v[250:251] op_sel:[0,1,0] op_sel_hi:[1,1,0]
	v_pk_fma_f32 v[240:241], v[212:213], v[248:249], v[250:251] op_sel:[0,1,0] op_sel_hi:[1,1,0]
	v_pk_fma_f32 v[238:239], v[210:211], v[238:239], v[250:251] op_sel:[0,0,1] op_sel_hi:[1,1,1]
	v_pk_fma_f32 v[240:241], v[212:213], v[240:241], v[250:251] op_sel:[0,0,1] op_sel_hi:[1,1,1]
	v_pk_fma_f32 v[238:239], v[210:211], v[238:239], v[252:253] op_sel:[0,0,0] op_sel_hi:[1,1,0]
	v_pk_fma_f32 v[240:241], v[212:213], v[240:241], v[252:253] op_sel:[0,0,0] op_sel_hi:[1,1,0]
	v_pk_fma_f32 v[238:239], v[210:211], v[238:239], v[248:249] op_sel:[0,0,0] op_sel_hi:[1,1,0]
	v_pk_fma_f32 v[240:241], v[212:213], v[240:241], v[248:249] op_sel:[0,0,0] op_sel_hi:[1,1,0]
	v_pk_mul_f32 v[238:239], v[210:211], v[238:239] op_sel:[0,0] op_sel_hi:[1,1] neg_lo:[1,0] neg_hi:[1,0]
	v_pk_mul_f32 v[240:241], v[212:213], v[240:241] op_sel:[0,0] op_sel_hi:[1,1] neg_lo:[1,0] neg_hi:[1,0]
	v_pk_fma_f32 v[242:243], v[28:29], v[28:29], v[248:249] op_sel:[0,0,0] op_sel_hi:[1,1,0] neg_lo:[1,0,0] neg_hi:[1,0,0]
	v_pk_fma_f32 v[244:245], v[30:31], v[30:31], v[248:249] op_sel:[0,0,0] op_sel_hi:[1,1,0] neg_lo:[1,0,0] neg_hi:[1,0,0]
	v_cmp_lt_f32_e64 s[24:25], v253, v210
	v_cmp_lt_f32_e64 s[26:27], v253, v211
	v_cmp_lt_f32_e64 s[30:31], v253, v212
	v_cmp_lt_f32_e64 s[34:35], v253, v213
	v_cndmask_b32_e64 v238, v242, v238, s[24:25]
	v_cndmask_b32_e64 v239, v243, v239, s[26:27]
	v_cndmask_b32_e64 v240, v244, v240, s[30:31]
	v_cndmask_b32_e64 v241, v245, v241, s[34:35]
	v_sqrt_f32_e32 v238, v238
	v_sqrt_f32_e32 v239, v239
	v_sqrt_f32_e32 v240, v240
	v_sqrt_f32_e32 v241, v241
	v_pk_mul_f32 v[12:13], v[238:239], v[206:207] op_sel:[0,0] op_sel_hi:[1,1]
	v_pk_mul_f32 v[14:15], v[240:241], v[208:209] op_sel:[0,0] op_sel_hi:[1,1]
	v_pk_add_f32 v[202:203], v[60:61], v[68:69] op_sel:[0,0] op_sel_hi:[1,1]
	v_pk_add_f32 v[204:205], v[62:63], v[70:71] op_sel:[0,0] op_sel_hi:[1,1]
	v_pk_add_f32 v[206:207], v[40:41], v[100:101] op_sel:[0,0] op_sel_hi:[1,1]
; __device__ __forceinline__ float fast_exp(float x) { return __builtin_amdgcn_exp2f(x * 1.4426950408889634f); }
; __device__ __forceinline__ float fast_sigmoid(float x) { return __builtin_amdgcn_rcpf(1.0f + fast_exp(-x)); }
;     __device__ __forceinline__ void operator()(Acc& acc, const Unit& u, int wr, int wc, int fr_, int fq_, LAS unsigned char* le, int wid, int lane, int&) const {
;     ...
;                     const f32x4 ba = *(const f32x4*)(b_a + ch0 + n * 16), bi = *(const f32x4*)(b_i + ch0 + n * 16), sl = *(const f32x4*)(spl + ch0 + n * 16);
;                     const u32x2 xw = xpre[ai][m][n]; const float xv[4] = {bflo(xw.x), bfhi(xw.x), bflo(xw.y), bfhi(xw.y)};
;                     const f32x4 ra = acc[ai][0][m][n] + ba, ri = acc[ai][1][m][n] + bi;
; #pragma unroll
;                     for (int j = 0; j < 4; ++j) { const float r = fast_sigmoid(ra[j]), ig = fast_sigmoid(ri[j]);
;                         const float la = -8.0f * r * sl[j];
;                         const float a = fast_exp(la); const float x2 = 2.0f * la;
;                         const float ser = -x2 * (1.0f + x2 * (0.5f + x2 * (1.0f / 6.0f + x2 * (1.0f / 24.0f + x2 * (1.0f / 120.0f)))));
;                         const float om = (x2 > -0.3f) ? ser : (1.0f - a * a);
;                         const float uu = __builtin_amdgcn_sqrtf(om) * (ig * xv[j]);
;                         if (m == 0) { acc[ai][0][m][n][j] = a; acc[ai][1][m][n][j] = uu; }
;                         else { acc[ai][1][m][n][j] = a * acc[ai][1][m - 1][n][j] + uu; acc[ai][0][m][n][j] = acc[ai][0][m - 1][n][j] * a; } } } }
	v_pk_add_f32 v[208:209], v[42:43], v[102:103] op_sel:[0,0] op_sel_hi:[1,1]
	v_pk_mul_f32 v[202:203], v[202:203], v[246:247] op_sel:[0,0] op_sel_hi:[1,0]
	v_pk_mul_f32 v[204:205], v[204:205], v[246:247] op_sel:[0,0] op_sel_hi:[1,0]
	v_pk_mul_f32 v[206:207], v[206:207], v[246:247] op_sel:[0,0] op_sel_hi:[1,0]
	v_pk_mul_f32 v[208:209], v[208:209], v[246:247] op_sel:[0,0] op_sel_hi:[1,0]
	v_exp_f32_e32 v202, v202
	v_exp_f32_e32 v203, v203
	v_exp_f32_e32 v204, v204
	v_exp_f32_e32 v205, v205
	v_exp_f32_e32 v206, v206
	v_exp_f32_e32 v207, v207
	v_exp_f32_e32 v208, v208
	v_exp_f32_e32 v209, v209
	v_pk_add_f32 v[202:203], v[202:203], v[248:249] op_sel:[0,0] op_sel_hi:[1,0]
	v_pk_add_f32 v[204:205], v[204:205], v[248:249] op_sel:[0,0] op_sel_hi:[1,0]
	v_pk_add_f32 v[206:207], v[206:207], v[248:249] op_sel:[0,0] op_sel_hi:[1,0]
	v_pk_add_f32 v[208:209], v[208:209], v[248:249] op_sel:[0,0] op_sel_hi:[1,0]
	v_rcp_f32_e32 v202, v202
	v_rcp_f32_e32 v203, v203
	v_rcp_f32_e32 v204, v204
	v_rcp_f32_e32 v205, v205
	v_rcp_f32_e32 v206, v206
	v_rcp_f32_e32 v207, v207
	v_rcp_f32_e32 v208, v208
	v_rcp_f32_e32 v209, v209
	v_lshlrev_b32_e32 v242, 16, v186
	v_and_b32_e32 v243, s22, v186
	v_lshlrev_b32_e32 v244, 16, v187
	v_and_b32_e32 v245, s22, v187
	v_pk_mul_f32 v[210:211], v[202:203], v[88:89] op_sel:[0,0] op_sel_hi:[1,1]
	v_pk_mul_f32 v[212:213], v[204:205], v[90:91] op_sel:[0,0] op_sel_hi:[1,1]
	v_pk_mul_f32 v[206:207], v[206:207], v[242:243] op_sel:[0,0] op_sel_hi:[1,1]
	v_pk_mul_f32 v[208:209], v[208:209], v[244:245] op_sel:[0,0] op_sel_hi:[1,1]
	v_pk_mul_f32 v[214:215], v[210:211], v[246:247] op_sel:[0,1] op_sel_hi:[1,1]
	v_pk_mul_f32 v[216:217], v[212:213], v[246:247] op_sel:[0,1] op_sel_hi:[1,1]
	v_pk_add_f32 v[210:211], v[210:211], v[210:211] op_sel:[0,0] op_sel_hi:[1,1]
	v_pk_add_f32 v[212:213], v[212:213], v[212:213] op_sel:[0,0] op_sel_hi:[1,1]
	v_exp_f32_e32 v214, v214
	v_exp_f32_e32 v215, v215
	v_exp_f32_e32 v216, v216
	v_exp_f32_e32 v217, v217
	v_pk_fma_f32 v[238:239], v[210:211], v[248:249], v[250:251] op_sel:[0,1,0] op_sel_hi:[1,1,0]
	v_pk_fma_f32 v[240:241], v[212:213], v[248:249], v[250:251] op_sel:[0,1,0] op_sel_hi:[1,1,0]
	v_pk_fma_f32 v[238:239], v[210:211], v[238:239], v[250:251] op_sel:[0,0,1] op_sel_hi:[1,1,1]
	v_pk_fma_f32 v[240:241], v[212:213], v[240:241], v[250:251] op_sel:[0,0,1] op_sel_hi:[1,1,1]
	v_pk_fma_f32 v[238:239], v[210:211], v[238:239], v[252:253] op_sel:[0,0,0] op_sel_hi:[1,1,0]
	v_pk_fma_f32 v[240:241], v[212:213], v[240:241], v[252:253] op_sel:[0,0,0] op_sel_hi:[1,1,0]
	v_pk_fma_f32 v[238:239], v[210:211], v[238:239], v[248:249] op_sel:[0,0,0] op_sel_hi:[1,1,0]
	v_pk_fma_f32 v[240:241], v[212:213], v[240:241], v[248:249] op_sel:[0,0,0] op_sel_hi:[1,1,0]
	v_pk_mul_f32 v[238:239], v[210:211], v[238:239] op_sel:[0,0] op_sel_hi:[1,1] neg_lo:[1,0] neg_hi:[1,0]
	v_pk_mul_f32 v[240:241], v[212:213], v[240:241] op_sel:[0,0] op_sel_hi:[1,1] neg_lo:[1,0] neg_hi:[1,0]
	v_pk_fma_f32 v[242:243], v[214:215], v[214:215], v[248:249] op_sel:[0,0,0] op_sel_hi:[1,1,0] neg_lo:[1,0,0] neg_hi:[1,0,0]
	v_pk_fma_f32 v[244:245], v[216:217], v[216:217], v[248:249] op_sel:[0,0,0] op_sel_hi:[1,1,0] neg_lo:[1,0,0] neg_hi:[1,0,0]
	v_cmp_lt_f32_e64 s[24:25], v253, v210
	v_cmp_lt_f32_e64 s[26:27], v253, v211
	v_cmp_lt_f32_e64 s[30:31], v253, v212
	v_cmp_lt_f32_e64 s[34:35], v253, v213
	v_cndmask_b32_e64 v238, v242, v238, s[24:25]
	v_cndmask_b32_e64 v239, v243, v239, s[26:27]
	v_cndmask_b32_e64 v240, v244, v240, s[30:31]
	v_cndmask_b32_e64 v241, v245, v241, s[34:35]
	v_sqrt_f32_e32 v238, v238
	v_sqrt_f32_e32 v239, v239
	v_sqrt_f32_e32 v240, v240
	v_sqrt_f32_e32 v241, v241
	v_pk_mul_f32 v[206:207], v[238:239], v[206:207] op_sel:[0,0] op_sel_hi:[1,1]
	v_pk_mul_f32 v[208:209], v[240:241], v[208:209] op_sel:[0,0] op_sel_hi:[1,1]
	v_pk_fma_f32 v[40:41], v[214:215], v[44:45], v[206:207] op_sel:[0,0,0] op_sel_hi:[1,1,1]
	v_pk_fma_f32 v[42:43], v[216:217], v[46:47], v[208:209] op_sel:[0,0,0] op_sel_hi:[1,1,1]
	v_pk_mul_f32 v[60:61], v[64:65], v[214:215] op_sel:[0,0] op_sel_hi:[1,1]
	v_pk_mul_f32 v[62:63], v[66:67], v[216:217] op_sel:[0,0] op_sel_hi:[1,1]
	v_pk_add_f32 v[202:203], v[24:25], v[72:73] op_sel:[0,0] op_sel_hi:[1,1]
	v_pk_add_f32 v[204:205], v[26:27], v[74:75] op_sel:[0,0] op_sel_hi:[1,1]
	v_pk_add_f32 v[206:207], v[8:9], v[104:105] op_sel:[0,0] op_sel_hi:[1,1]
	v_pk_add_f32 v[208:209], v[10:11], v[106:107] op_sel:[0,0] op_sel_hi:[1,1]
	v_pk_mul_f32 v[202:203], v[202:203], v[246:247] op_sel:[0,0] op_sel_hi:[1,0]
	v_pk_mul_f32 v[204:205], v[204:205], v[246:247] op_sel:[0,0] op_sel_hi:[1,0]
	v_pk_mul_f32 v[206:207], v[206:207], v[246:247] op_sel:[0,0] op_sel_hi:[1,0]
	v_pk_mul_f32 v[208:209], v[208:209], v[246:247] op_sel:[0,0] op_sel_hi:[1,0]
	v_exp_f32_e32 v202, v202
	v_exp_f32_e32 v203, v203
	v_exp_f32_e32 v204, v204
	v_exp_f32_e32 v205, v205
	v_exp_f32_e32 v206, v206
	v_exp_f32_e32 v207, v207
	v_exp_f32_e32 v208, v208
	v_exp_f32_e32 v209, v209
	v_pk_add_f32 v[202:203], v[202:203], v[248:249] op_sel:[0,0] op_sel_hi:[1,0]
	v_pk_add_f32 v[204:205], v[204:205], v[248:249] op_sel:[0,0] op_sel_hi:[1,0]
	v_pk_add_f32 v[206:207], v[206:207], v[248:249] op_sel:[0,0] op_sel_hi:[1,0]
	v_pk_add_f32 v[208:209], v[208:209], v[248:249] op_sel:[0,0] op_sel_hi:[1,0]
	v_rcp_f32_e32 v202, v202
	v_rcp_f32_e32 v203, v203
	v_rcp_f32_e32 v204, v204
	v_rcp_f32_e32 v205, v205
	v_rcp_f32_e32 v206, v206
	v_rcp_f32_e32 v207, v207
	v_rcp_f32_e32 v208, v208
	v_rcp_f32_e32 v209, v209
	v_lshlrev_b32_e32 v242, 16, v188
	v_and_b32_e32 v243, s22, v188
	v_lshlrev_b32_e32 v244, 16, v189
	v_and_b32_e32 v245, s22, v189
	v_pk_mul_f32 v[210:211], v[202:203], v[198:199] op_sel:[0,0] op_sel_hi:[1,1]
; __device__ __forceinline__ float fast_exp(float x) { return __builtin_amdgcn_exp2f(x * 1.4426950408889634f); }
; __device__ __forceinline__ float fast_sigmoid(float x) { return __builtin_amdgcn_rcpf(1.0f + fast_exp(-x)); }
;     __device__ __forceinline__ void operator()(Acc& acc, const Unit& u, int wr, int wc, int fr_, int fq_, LAS unsigned char* le, int wid, int lane, int&) const {
;     ...
;                     const f32x4 ba = *(const f32x4*)(b_a + ch0 + n * 16), bi = *(const f32x4*)(b_i + ch0 + n * 16), sl = *(const f32x4*)(spl + ch0 + n * 16);
;                     const u32x2 xw = xpre[ai][m][n]; const float xv[4] = {bflo(xw.x), bfhi(xw.x), bflo(xw.y), bfhi(xw.y)};
;                     const f32x4 ra = acc[ai][0][m][n] + ba, ri = acc[ai][1][m][n] + bi;
; #pragma unroll
;                     for (int j = 0; j < 4; ++j) { const float r = fast_sigmoid(ra[j]), ig = fast_sigmoid(ri[j]);
;                         const float la = -8.0f * r * sl[j];
;                         const float a = fast_exp(la); const float x2 = 2.0f * la;
;                         const float ser = -x2 * (1.0f + x2 * (0.5f + x2 * (1.0f / 6.0f + x2 * (1.0f / 24.0f + x2 * (1.0f / 120.0f)))));
;                         const float om = (x2 > -0.3f) ? ser : (1.0f - a * a);
;                         const float uu = __builtin_amdgcn_sqrtf(om) * (ig * xv[j]);
;                         if (m == 0) { acc[ai][0][m][n][j] = a; acc[ai][1][m][n][j] = uu; }
;                         else { acc[ai][1][m][n][j] = a * acc[ai][1][m - 1][n][j] + uu; acc[ai][0][m][n][j] = acc[ai][0][m - 1][n][j] * a; } } } }
	v_pk_mul_f32 v[212:213], v[204:205], v[200:201] op_sel:[0,0] op_sel_hi:[1,1]
	v_pk_mul_f32 v[206:207], v[206:207], v[242:243] op_sel:[0,0] op_sel_hi:[1,1]
	v_pk_mul_f32 v[208:209], v[208:209], v[244:245] op_sel:[0,0] op_sel_hi:[1,1]
	v_pk_mul_f32 v[214:215], v[210:211], v[246:247] op_sel:[0,1] op_sel_hi:[1,1]
	v_pk_mul_f32 v[216:217], v[212:213], v[246:247] op_sel:[0,1] op_sel_hi:[1,1]
	v_pk_add_f32 v[210:211], v[210:211], v[210:211] op_sel:[0,0] op_sel_hi:[1,1]
	v_pk_add_f32 v[212:213], v[212:213], v[212:213] op_sel:[0,0] op_sel_hi:[1,1]
	v_exp_f32_e32 v214, v214
	v_exp_f32_e32 v215, v215
	v_exp_f32_e32 v216, v216
	v_exp_f32_e32 v217, v217
	v_pk_fma_f32 v[238:239], v[210:211], v[248:249], v[250:251] op_sel:[0,1,0] op_sel_hi:[1,1,0]
	v_pk_fma_f32 v[240:241], v[212:213], v[248:249], v[250:251] op_sel:[0,1,0] op_sel_hi:[1,1,0]
	v_pk_fma_f32 v[238:239], v[210:211], v[238:239], v[250:251] op_sel:[0,0,1] op_sel_hi:[1,1,1]
	v_pk_fma_f32 v[240:241], v[212:213], v[240:241], v[250:251] op_sel:[0,0,1] op_sel_hi:[1,1,1]
	v_pk_fma_f32 v[238:239], v[210:211], v[238:239], v[252:253] op_sel:[0,0,0] op_sel_hi:[1,1,0]
	v_pk_fma_f32 v[240:241], v[212:213], v[240:241], v[252:253] op_sel:[0,0,0] op_sel_hi:[1,1,0]
	v_pk_fma_f32 v[238:239], v[210:211], v[238:239], v[248:249] op_sel:[0,0,0] op_sel_hi:[1,1,0]
	v_pk_fma_f32 v[240:241], v[212:213], v[240:241], v[248:249] op_sel:[0,0,0] op_sel_hi:[1,1,0]
	v_pk_mul_f32 v[238:239], v[210:211], v[238:239] op_sel:[0,0] op_sel_hi:[1,1] neg_lo:[1,0] neg_hi:[1,0]
	v_pk_mul_f32 v[240:241], v[212:213], v[240:241] op_sel:[0,0] op_sel_hi:[1,1] neg_lo:[1,0] neg_hi:[1,0]
	v_pk_fma_f32 v[242:243], v[214:215], v[214:215], v[248:249] op_sel:[0,0,0] op_sel_hi:[1,1,0] neg_lo:[1,0,0] neg_hi:[1,0,0]
	v_pk_fma_f32 v[244:245], v[216:217], v[216:217], v[248:249] op_sel:[0,0,0] op_sel_hi:[1,1,0] neg_lo:[1,0,0] neg_hi:[1,0,0]
	v_cmp_lt_f32_e64 s[24:25], v253, v210
	v_cmp_lt_f32_e64 s[26:27], v253, v211
	v_cmp_lt_f32_e64 s[30:31], v253, v212
	v_cmp_lt_f32_e64 s[34:35], v253, v213
	v_cndmask_b32_e64 v238, v242, v238, s[24:25]
	v_cndmask_b32_e64 v239, v243, v239, s[26:27]
	v_cndmask_b32_e64 v240, v244, v240, s[30:31]
	v_cndmask_b32_e64 v241, v245, v241, s[34:35]
	v_sqrt_f32_e32 v238, v238
	v_sqrt_f32_e32 v239, v239
	v_sqrt_f32_e32 v240, v240
	v_sqrt_f32_e32 v241, v241
	v_pk_mul_f32 v[206:207], v[238:239], v[206:207] op_sel:[0,0] op_sel_hi:[1,1]
	v_pk_mul_f32 v[208:209], v[240:241], v[208:209] op_sel:[0,0] op_sel_hi:[1,1]
	v_pk_fma_f32 v[8:9], v[214:215], v[12:13], v[206:207] op_sel:[0,0,0] op_sel_hi:[1,1,1]
	v_pk_fma_f32 v[10:11], v[216:217], v[14:15], v[208:209] op_sel:[0,0,0] op_sel_hi:[1,1,1]
	v_pk_mul_f32 v[24:25], v[28:29], v[214:215] op_sel:[0,0] op_sel_hi:[1,1]
	v_pk_mul_f32 v[26:27], v[30:31], v[216:217] op_sel:[0,0] op_sel_hi:[1,1]
	v_pk_add_f32 v[202:203], v[52:53], v[68:69] op_sel:[0,0] op_sel_hi:[1,1]
	v_pk_add_f32 v[204:205], v[54:55], v[70:71] op_sel:[0,0] op_sel_hi:[1,1]
	v_pk_add_f32 v[206:207], v[36:37], v[100:101] op_sel:[0,0] op_sel_hi:[1,1]
	v_pk_add_f32 v[208:209], v[38:39], v[102:103] op_sel:[0,0] op_sel_hi:[1,1]
	v_pk_mul_f32 v[202:203], v[202:203], v[246:247] op_sel:[0,0] op_sel_hi:[1,0]
	v_pk_mul_f32 v[204:205], v[204:205], v[246:247] op_sel:[0,0] op_sel_hi:[1,0]
	v_pk_mul_f32 v[206:207], v[206:207], v[246:247] op_sel:[0,0] op_sel_hi:[1,0]
	v_pk_mul_f32 v[208:209], v[208:209], v[246:247] op_sel:[0,0] op_sel_hi:[1,0]
	v_exp_f32_e32 v202, v202
	v_exp_f32_e32 v203, v203
	v_exp_f32_e32 v204, v204
	v_exp_f32_e32 v205, v205
	v_exp_f32_e32 v206, v206
	v_exp_f32_e32 v207, v207
	v_exp_f32_e32 v208, v208
	v_exp_f32_e32 v209, v209
	v_pk_add_f32 v[202:203], v[202:203], v[248:249] op_sel:[0,0] op_sel_hi:[1,0]
	v_pk_add_f32 v[204:205], v[204:205], v[248:249] op_sel:[0,0] op_sel_hi:[1,0]
	v_pk_add_f32 v[206:207], v[206:207], v[248:249] op_sel:[0,0] op_sel_hi:[1,0]
	v_pk_add_f32 v[208:209], v[208:209], v[248:249] op_sel:[0,0] op_sel_hi:[1,0]
	v_rcp_f32_e32 v202, v202
	v_rcp_f32_e32 v203, v203
	v_rcp_f32_e32 v204, v204
	v_rcp_f32_e32 v205, v205
	v_rcp_f32_e32 v206, v206
	v_rcp_f32_e32 v207, v207
	v_rcp_f32_e32 v208, v208
	v_rcp_f32_e32 v209, v209
	v_lshlrev_b32_e32 v242, 16, v190
	v_and_b32_e32 v243, s22, v190
	v_lshlrev_b32_e32 v244, 16, v191
	v_and_b32_e32 v245, s22, v191
	v_pk_mul_f32 v[210:211], v[202:203], v[88:89] op_sel:[0,0] op_sel_hi:[1,1]
	v_pk_mul_f32 v[212:213], v[204:205], v[90:91] op_sel:[0,0] op_sel_hi:[1,1]
	v_pk_mul_f32 v[206:207], v[206:207], v[242:243] op_sel:[0,0] op_sel_hi:[1,1]
	v_pk_mul_f32 v[208:209], v[208:209], v[244:245] op_sel:[0,0] op_sel_hi:[1,1]
	v_pk_mul_f32 v[214:215], v[210:211], v[246:247] op_sel:[0,1] op_sel_hi:[1,1]
	v_pk_mul_f32 v[216:217], v[212:213], v[246:247] op_sel:[0,1] op_sel_hi:[1,1]
	v_pk_add_f32 v[210:211], v[210:211], v[210:211] op_sel:[0,0] op_sel_hi:[1,1]
	v_pk_add_f32 v[212:213], v[212:213], v[212:213] op_sel:[0,0] op_sel_hi:[1,1]
	v_exp_f32_e32 v214, v214
	v_exp_f32_e32 v215, v215
	v_exp_f32_e32 v216, v216
	v_exp_f32_e32 v217, v217
	v_pk_fma_f32 v[238:239], v[210:211], v[248:249], v[250:251] op_sel:[0,1,0] op_sel_hi:[1,1,0]
	v_pk_fma_f32 v[240:241], v[212:213], v[248:249], v[250:251] op_sel:[0,1,0] op_sel_hi:[1,1,0]
	v_pk_fma_f32 v[238:239], v[210:211], v[238:239], v[250:251] op_sel:[0,0,1] op_sel_hi:[1,1,1]
	v_pk_fma_f32 v[240:241], v[212:213], v[240:241], v[250:251] op_sel:[0,0,1] op_sel_hi:[1,1,1]
	v_pk_fma_f32 v[238:239], v[210:211], v[238:239], v[252:253] op_sel:[0,0,0] op_sel_hi:[1,1,0]
	v_pk_fma_f32 v[240:241], v[212:213], v[240:241], v[252:253] op_sel:[0,0,0] op_sel_hi:[1,1,0]
	v_pk_fma_f32 v[238:239], v[210:211], v[238:239], v[248:249] op_sel:[0,0,0] op_sel_hi:[1,1,0]
; __device__ __forceinline__ float fast_exp(float x) { return __builtin_amdgcn_exp2f(x * 1.4426950408889634f); }
; __device__ __forceinline__ float fast_sigmoid(float x) { return __builtin_amdgcn_rcpf(1.0f + fast_exp(-x)); }
;     __device__ __forceinline__ void operator()(Acc& acc, const Unit& u, int wr, int wc, int fr_, int fq_, LAS unsigned char* le, int wid, int lane, int&) const {
;     ...
;                     const f32x4 ba = *(const f32x4*)(b_a + ch0 + n * 16), bi = *(const f32x4*)(b_i + ch0 + n * 16), sl = *(const f32x4*)(spl + ch0 + n * 16);
;                     const u32x2 xw = xpre[ai][m][n]; const float xv[4] = {bflo(xw.x), bfhi(xw.x), bflo(xw.y), bfhi(xw.y)};
;                     const f32x4 ra = acc[ai][0][m][n] + ba, ri = acc[ai][1][m][n] + bi;
; #pragma unroll
;                     for (int j = 0; j < 4; ++j) { const float r = fast_sigmoid(ra[j]), ig = fast_sigmoid(ri[j]);
;                         const float la = -8.0f * r * sl[j];
;                         const float a = fast_exp(la); const float x2 = 2.0f * la;
;                         const float ser = -x2 * (1.0f + x2 * (0.5f + x2 * (1.0f / 6.0f + x2 * (1.0f / 24.0f + x2 * (1.0f / 120.0f)))));
;                         const float om = (x2 > -0.3f) ? ser : (1.0f - a * a);
;                         const float uu = __builtin_amdgcn_sqrtf(om) * (ig * xv[j]);
;                         if (m == 0) { acc[ai][0][m][n][j] = a; acc[ai][1][m][n][j] = uu; }
;                         else { acc[ai][1][m][n][j] = a * acc[ai][1][m - 1][n][j] + uu; acc[ai][0][m][n][j] = acc[ai][0][m - 1][n][j] * a; } } } }
	v_pk_fma_f32 v[240:241], v[212:213], v[240:241], v[248:249] op_sel:[0,0,0] op_sel_hi:[1,1,0]
	v_pk_mul_f32 v[238:239], v[210:211], v[238:239] op_sel:[0,0] op_sel_hi:[1,1] neg_lo:[1,0] neg_hi:[1,0]
	v_pk_mul_f32 v[240:241], v[212:213], v[240:241] op_sel:[0,0] op_sel_hi:[1,1] neg_lo:[1,0] neg_hi:[1,0]
	v_pk_fma_f32 v[242:243], v[214:215], v[214:215], v[248:249] op_sel:[0,0,0] op_sel_hi:[1,1,0] neg_lo:[1,0,0] neg_hi:[1,0,0]
	v_pk_fma_f32 v[244:245], v[216:217], v[216:217], v[248:249] op_sel:[0,0,0] op_sel_hi:[1,1,0] neg_lo:[1,0,0] neg_hi:[1,0,0]
	v_cmp_lt_f32_e64 s[24:25], v253, v210
	v_cmp_lt_f32_e64 s[26:27], v253, v211
	v_cmp_lt_f32_e64 s[30:31], v253, v212
	v_cmp_lt_f32_e64 s[34:35], v253, v213
	v_cndmask_b32_e64 v238, v242, v238, s[24:25]
	v_cndmask_b32_e64 v239, v243, v239, s[26:27]
	v_cndmask_b32_e64 v240, v244, v240, s[30:31]
	v_cndmask_b32_e64 v241, v245, v241, s[34:35]
	v_sqrt_f32_e32 v238, v238
	v_sqrt_f32_e32 v239, v239
	v_sqrt_f32_e32 v240, v240
	v_sqrt_f32_e32 v241, v241
	v_pk_mul_f32 v[206:207], v[238:239], v[206:207] op_sel:[0,0] op_sel_hi:[1,1]
	v_pk_mul_f32 v[208:209], v[240:241], v[208:209] op_sel:[0,0] op_sel_hi:[1,1]
	v_pk_fma_f32 v[36:37], v[214:215], v[40:41], v[206:207] op_sel:[0,0,0] op_sel_hi:[1,1,1]
	v_pk_fma_f32 v[38:39], v[216:217], v[42:43], v[208:209] op_sel:[0,0,0] op_sel_hi:[1,1,1]
	v_pk_mul_f32 v[52:53], v[60:61], v[214:215] op_sel:[0,0] op_sel_hi:[1,1]
	v_pk_mul_f32 v[54:55], v[62:63], v[216:217] op_sel:[0,0] op_sel_hi:[1,1]
	v_pk_add_f32 v[202:203], v[20:21], v[72:73] op_sel:[0,0] op_sel_hi:[1,1]
	v_pk_add_f32 v[204:205], v[22:23], v[74:75] op_sel:[0,0] op_sel_hi:[1,1]
	v_pk_add_f32 v[206:207], v[4:5], v[104:105] op_sel:[0,0] op_sel_hi:[1,1]
	v_pk_add_f32 v[208:209], v[6:7], v[106:107] op_sel:[0,0] op_sel_hi:[1,1]
	v_pk_mul_f32 v[202:203], v[202:203], v[246:247] op_sel:[0,0] op_sel_hi:[1,0]
	v_pk_mul_f32 v[204:205], v[204:205], v[246:247] op_sel:[0,0] op_sel_hi:[1,0]
	v_pk_mul_f32 v[206:207], v[206:207], v[246:247] op_sel:[0,0] op_sel_hi:[1,0]
	v_pk_mul_f32 v[208:209], v[208:209], v[246:247] op_sel:[0,0] op_sel_hi:[1,0]
	v_exp_f32_e32 v202, v202
	v_exp_f32_e32 v203, v203
	v_exp_f32_e32 v204, v204
	v_exp_f32_e32 v205, v205
	v_exp_f32_e32 v206, v206
	v_exp_f32_e32 v207, v207
	v_exp_f32_e32 v208, v208
	v_exp_f32_e32 v209, v209
	v_pk_add_f32 v[202:203], v[202:203], v[248:249] op_sel:[0,0] op_sel_hi:[1,0]
	v_pk_add_f32 v[204:205], v[204:205], v[248:249] op_sel:[0,0] op_sel_hi:[1,0]
	v_pk_add_f32 v[206:207], v[206:207], v[248:249] op_sel:[0,0] op_sel_hi:[1,0]
	v_pk_add_f32 v[208:209], v[208:209], v[248:249] op_sel:[0,0] op_sel_hi:[1,0]
	v_rcp_f32_e32 v202, v202
	v_rcp_f32_e32 v203, v203
	v_rcp_f32_e32 v204, v204
	v_rcp_f32_e32 v205, v205
	v_rcp_f32_e32 v206, v206
	v_rcp_f32_e32 v207, v207
	v_rcp_f32_e32 v208, v208
	v_rcp_f32_e32 v209, v209
	v_lshlrev_b32_e32 v242, 16, v192
	v_and_b32_e32 v243, s22, v192
	v_lshlrev_b32_e32 v244, 16, v193
	v_and_b32_e32 v245, s22, v193
	v_pk_mul_f32 v[210:211], v[202:203], v[198:199] op_sel:[0,0] op_sel_hi:[1,1]
	v_pk_mul_f32 v[212:213], v[204:205], v[200:201] op_sel:[0,0] op_sel_hi:[1,1]
	v_pk_mul_f32 v[206:207], v[206:207], v[242:243] op_sel:[0,0] op_sel_hi:[1,1]
	v_pk_mul_f32 v[208:209], v[208:209], v[244:245] op_sel:[0,0] op_sel_hi:[1,1]
	v_pk_mul_f32 v[214:215], v[210:211], v[246:247] op_sel:[0,1] op_sel_hi:[1,1]
	v_pk_mul_f32 v[216:217], v[212:213], v[246:247] op_sel:[0,1] op_sel_hi:[1,1]
	v_pk_add_f32 v[210:211], v[210:211], v[210:211] op_sel:[0,0] op_sel_hi:[1,1]
	v_pk_add_f32 v[212:213], v[212:213], v[212:213] op_sel:[0,0] op_sel_hi:[1,1]
	v_exp_f32_e32 v214, v214
	v_exp_f32_e32 v215, v215
	v_exp_f32_e32 v216, v216
	v_exp_f32_e32 v217, v217
	v_pk_fma_f32 v[238:239], v[210:211], v[248:249], v[250:251] op_sel:[0,1,0] op_sel_hi:[1,1,0]
	v_pk_fma_f32 v[240:241], v[212:213], v[248:249], v[250:251] op_sel:[0,1,0] op_sel_hi:[1,1,0]
	v_pk_fma_f32 v[238:239], v[210:211], v[238:239], v[250:251] op_sel:[0,0,1] op_sel_hi:[1,1,1]
	v_pk_fma_f32 v[240:241], v[212:213], v[240:241], v[250:251] op_sel:[0,0,1] op_sel_hi:[1,1,1]
	v_pk_fma_f32 v[238:239], v[210:211], v[238:239], v[252:253] op_sel:[0,0,0] op_sel_hi:[1,1,0]
	v_pk_fma_f32 v[240:241], v[212:213], v[240:241], v[252:253] op_sel:[0,0,0] op_sel_hi:[1,1,0]
	v_pk_fma_f32 v[238:239], v[210:211], v[238:239], v[248:249] op_sel:[0,0,0] op_sel_hi:[1,1,0]
	v_pk_fma_f32 v[240:241], v[212:213], v[240:241], v[248:249] op_sel:[0,0,0] op_sel_hi:[1,1,0]
	v_pk_mul_f32 v[238:239], v[210:211], v[238:239] op_sel:[0,0] op_sel_hi:[1,1] neg_lo:[1,0] neg_hi:[1,0]
	v_pk_mul_f32 v[240:241], v[212:213], v[240:241] op_sel:[0,0] op_sel_hi:[1,1] neg_lo:[1,0] neg_hi:[1,0]
	v_pk_fma_f32 v[242:243], v[214:215], v[214:215], v[248:249] op_sel:[0,0,0] op_sel_hi:[1,1,0] neg_lo:[1,0,0] neg_hi:[1,0,0]
	v_pk_fma_f32 v[244:245], v[216:217], v[216:217], v[248:249] op_sel:[0,0,0] op_sel_hi:[1,1,0] neg_lo:[1,0,0] neg_hi:[1,0,0]
	v_cmp_lt_f32_e64 s[24:25], v253, v210
	v_cmp_lt_f32_e64 s[26:27], v253, v211
	v_cmp_lt_f32_e64 s[30:31], v253, v212
	v_cmp_lt_f32_e64 s[34:35], v253, v213
	v_cndmask_b32_e64 v238, v242, v238, s[24:25]
	v_cndmask_b32_e64 v239, v243, v239, s[26:27]
	v_cndmask_b32_e64 v240, v244, v240, s[30:31]
	v_cndmask_b32_e64 v241, v245, v241, s[34:35]
	v_sqrt_f32_e32 v238, v238
	v_sqrt_f32_e32 v239, v239
	v_sqrt_f32_e32 v240, v240
	v_sqrt_f32_e32 v241, v241
	v_pk_mul_f32 v[206:207], v[238:239], v[206:207] op_sel:[0,0] op_sel_hi:[1,1]
	v_pk_mul_f32 v[208:209], v[240:241], v[208:209] op_sel:[0,0] op_sel_hi:[1,1]
	v_pk_fma_f32 v[4:5], v[214:215], v[8:9], v[206:207] op_sel:[0,0,0] op_sel_hi:[1,1,1]
	v_pk_fma_f32 v[6:7], v[216:217], v[10:11], v[208:209] op_sel:[0,0,0] op_sel_hi:[1,1,1]
; __device__ __forceinline__ float fast_exp(float x) { return __builtin_amdgcn_exp2f(x * 1.4426950408889634f); }
; __device__ __forceinline__ float fast_sigmoid(float x) { return __builtin_amdgcn_rcpf(1.0f + fast_exp(-x)); }
;     __device__ __forceinline__ void operator()(Acc& acc, const Unit& u, int wr, int wc, int fr_, int fq_, LAS unsigned char* le, int wid, int lane, int&) const {
;     ...
;                     const f32x4 ba = *(const f32x4*)(b_a + ch0 + n * 16), bi = *(const f32x4*)(b_i + ch0 + n * 16), sl = *(const f32x4*)(spl + ch0 + n * 16);
;                     const u32x2 xw = xpre[ai][m][n]; const float xv[4] = {bflo(xw.x), bfhi(xw.x), bflo(xw.y), bfhi(xw.y)};
;                     const f32x4 ra = acc[ai][0][m][n] + ba, ri = acc[ai][1][m][n] + bi;
; #pragma unroll
;                     for (int j = 0; j < 4; ++j) { const float r = fast_sigmoid(ra[j]), ig = fast_sigmoid(ri[j]);
;                         const float la = -8.0f * r * sl[j];
;                         const float a = fast_exp(la); const float x2 = 2.0f * la;
;                         const float ser = -x2 * (1.0f + x2 * (0.5f + x2 * (1.0f / 6.0f + x2 * (1.0f / 24.0f + x2 * (1.0f / 120.0f)))));
;                         const float om = (x2 > -0.3f) ? ser : (1.0f - a * a);
;                         const float uu = __builtin_amdgcn_sqrtf(om) * (ig * xv[j]);
;                         if (m == 0) { acc[ai][0][m][n][j] = a; acc[ai][1][m][n][j] = uu; }
;                         else { acc[ai][1][m][n][j] = a * acc[ai][1][m - 1][n][j] + uu; acc[ai][0][m][n][j] = acc[ai][0][m - 1][n][j] * a; } } } }
	v_pk_mul_f32 v[20:21], v[24:25], v[214:215] op_sel:[0,0] op_sel_hi:[1,1]
	v_pk_mul_f32 v[22:23], v[26:27], v[216:217] op_sel:[0,0] op_sel_hi:[1,1]
	v_pk_add_f32 v[202:203], v[48:49], v[68:69] op_sel:[0,0] op_sel_hi:[1,1]
	v_pk_add_f32 v[204:205], v[50:51], v[70:71] op_sel:[0,0] op_sel_hi:[1,1]
	v_pk_add_f32 v[206:207], v[32:33], v[100:101] op_sel:[0,0] op_sel_hi:[1,1]
	v_pk_add_f32 v[208:209], v[34:35], v[102:103] op_sel:[0,0] op_sel_hi:[1,1]
	v_pk_mul_f32 v[202:203], v[202:203], v[246:247] op_sel:[0,0] op_sel_hi:[1,0]
	v_pk_mul_f32 v[204:205], v[204:205], v[246:247] op_sel:[0,0] op_sel_hi:[1,0]
	v_pk_mul_f32 v[206:207], v[206:207], v[246:247] op_sel:[0,0] op_sel_hi:[1,0]
	v_pk_mul_f32 v[208:209], v[208:209], v[246:247] op_sel:[0,0] op_sel_hi:[1,0]
	v_exp_f32_e32 v202, v202
	v_exp_f32_e32 v203, v203
	v_exp_f32_e32 v204, v204
	v_exp_f32_e32 v205, v205
	v_exp_f32_e32 v206, v206
	v_exp_f32_e32 v207, v207
	v_exp_f32_e32 v208, v208
	v_exp_f32_e32 v209, v209
	v_pk_add_f32 v[202:203], v[202:203], v[248:249] op_sel:[0,0] op_sel_hi:[1,0]
	v_pk_add_f32 v[204:205], v[204:205], v[248:249] op_sel:[0,0] op_sel_hi:[1,0]
	v_pk_add_f32 v[206:207], v[206:207], v[248:249] op_sel:[0,0] op_sel_hi:[1,0]
	v_pk_add_f32 v[208:209], v[208:209], v[248:249] op_sel:[0,0] op_sel_hi:[1,0]
	v_rcp_f32_e32 v202, v202
	v_rcp_f32_e32 v203, v203
	v_rcp_f32_e32 v204, v204
	v_rcp_f32_e32 v205, v205
	v_rcp_f32_e32 v206, v206
	v_rcp_f32_e32 v207, v207
	v_rcp_f32_e32 v208, v208
	v_rcp_f32_e32 v209, v209
	v_lshlrev_b32_e32 v242, 16, v194
	v_and_b32_e32 v243, s22, v194
	v_lshlrev_b32_e32 v244, 16, v195
	v_and_b32_e32 v245, s22, v195
	v_pk_mul_f32 v[210:211], v[202:203], v[88:89] op_sel:[0,0] op_sel_hi:[1,1]
	v_pk_mul_f32 v[212:213], v[204:205], v[90:91] op_sel:[0,0] op_sel_hi:[1,1]
	v_pk_mul_f32 v[206:207], v[206:207], v[242:243] op_sel:[0,0] op_sel_hi:[1,1]
	v_pk_mul_f32 v[208:209], v[208:209], v[244:245] op_sel:[0,0] op_sel_hi:[1,1]
	v_pk_mul_f32 v[214:215], v[210:211], v[246:247] op_sel:[0,1] op_sel_hi:[1,1]
	v_pk_mul_f32 v[216:217], v[212:213], v[246:247] op_sel:[0,1] op_sel_hi:[1,1]
	v_pk_add_f32 v[210:211], v[210:211], v[210:211] op_sel:[0,0] op_sel_hi:[1,1]
	v_pk_add_f32 v[212:213], v[212:213], v[212:213] op_sel:[0,0] op_sel_hi:[1,1]
	v_exp_f32_e32 v214, v214
	v_exp_f32_e32 v215, v215
	v_exp_f32_e32 v216, v216
	v_exp_f32_e32 v217, v217
	v_pk_fma_f32 v[238:239], v[210:211], v[248:249], v[250:251] op_sel:[0,1,0] op_sel_hi:[1,1,0]
	v_pk_fma_f32 v[240:241], v[212:213], v[248:249], v[250:251] op_sel:[0,1,0] op_sel_hi:[1,1,0]
	v_pk_fma_f32 v[238:239], v[210:211], v[238:239], v[250:251] op_sel:[0,0,1] op_sel_hi:[1,1,1]
	v_pk_fma_f32 v[240:241], v[212:213], v[240:241], v[250:251] op_sel:[0,0,1] op_sel_hi:[1,1,1]
	v_pk_fma_f32 v[238:239], v[210:211], v[238:239], v[252:253] op_sel:[0,0,0] op_sel_hi:[1,1,0]
	v_pk_fma_f32 v[240:241], v[212:213], v[240:241], v[252:253] op_sel:[0,0,0] op_sel_hi:[1,1,0]
	v_pk_fma_f32 v[238:239], v[210:211], v[238:239], v[248:249] op_sel:[0,0,0] op_sel_hi:[1,1,0]
	v_pk_fma_f32 v[240:241], v[212:213], v[240:241], v[248:249] op_sel:[0,0,0] op_sel_hi:[1,1,0]
	v_pk_mul_f32 v[238:239], v[210:211], v[238:239] op_sel:[0,0] op_sel_hi:[1,1] neg_lo:[1,0] neg_hi:[1,0]
	v_pk_mul_f32 v[240:241], v[212:213], v[240:241] op_sel:[0,0] op_sel_hi:[1,1] neg_lo:[1,0] neg_hi:[1,0]
	v_pk_fma_f32 v[242:243], v[214:215], v[214:215], v[248:249] op_sel:[0,0,0] op_sel_hi:[1,1,0] neg_lo:[1,0,0] neg_hi:[1,0,0]
	v_pk_fma_f32 v[244:245], v[216:217], v[216:217], v[248:249] op_sel:[0,0,0] op_sel_hi:[1,1,0] neg_lo:[1,0,0] neg_hi:[1,0,0]
	v_cmp_lt_f32_e64 s[24:25], v253, v210
	v_cmp_lt_f32_e64 s[26:27], v253, v211
	v_cmp_lt_f32_e64 s[30:31], v253, v212
	v_cmp_lt_f32_e64 s[34:35], v253, v213
	v_cndmask_b32_e64 v238, v242, v238, s[24:25]
	v_cndmask_b32_e64 v239, v243, v239, s[26:27]
	v_cndmask_b32_e64 v240, v244, v240, s[30:31]
	v_cndmask_b32_e64 v241, v245, v241, s[34:35]
	v_sqrt_f32_e32 v238, v238
	v_sqrt_f32_e32 v239, v239
	v_sqrt_f32_e32 v240, v240
	v_sqrt_f32_e32 v241, v241
	v_pk_mul_f32 v[206:207], v[238:239], v[206:207] op_sel:[0,0] op_sel_hi:[1,1]
	v_pk_mul_f32 v[208:209], v[240:241], v[208:209] op_sel:[0,0] op_sel_hi:[1,1]
	v_pk_fma_f32 v[32:33], v[214:215], v[36:37], v[206:207] op_sel:[0,0,0] op_sel_hi:[1,1,1]
	v_pk_fma_f32 v[34:35], v[216:217], v[38:39], v[208:209] op_sel:[0,0,0] op_sel_hi:[1,1,1]
	v_pk_mul_f32 v[48:49], v[52:53], v[214:215] op_sel:[0,0] op_sel_hi:[1,1]
	v_pk_mul_f32 v[50:51], v[54:55], v[216:217] op_sel:[0,0] op_sel_hi:[1,1]
	v_pk_add_f32 v[202:203], v[16:17], v[72:73] op_sel:[0,0] op_sel_hi:[1,1]
	v_pk_add_f32 v[204:205], v[18:19], v[74:75] op_sel:[0,0] op_sel_hi:[1,1]
	v_pk_add_f32 v[206:207], v[0:1], v[104:105] op_sel:[0,0] op_sel_hi:[1,1]
	v_pk_add_f32 v[208:209], v[2:3], v[106:107] op_sel:[0,0] op_sel_hi:[1,1]
	v_pk_mul_f32 v[202:203], v[202:203], v[246:247] op_sel:[0,0] op_sel_hi:[1,0]
	v_pk_mul_f32 v[204:205], v[204:205], v[246:247] op_sel:[0,0] op_sel_hi:[1,0]
	v_pk_mul_f32 v[206:207], v[206:207], v[246:247] op_sel:[0,0] op_sel_hi:[1,0]
	v_pk_mul_f32 v[208:209], v[208:209], v[246:247] op_sel:[0,0] op_sel_hi:[1,0]
	v_exp_f32_e32 v202, v202
	v_exp_f32_e32 v203, v203
	v_exp_f32_e32 v204, v204
	v_exp_f32_e32 v205, v205
	v_exp_f32_e32 v206, v206
	v_exp_f32_e32 v207, v207
	v_exp_f32_e32 v208, v208
	v_exp_f32_e32 v209, v209
	v_pk_add_f32 v[202:203], v[202:203], v[248:249] op_sel:[0,0] op_sel_hi:[1,0]
	v_pk_add_f32 v[204:205], v[204:205], v[248:249] op_sel:[0,0] op_sel_hi:[1,0]
	v_pk_add_f32 v[206:207], v[206:207], v[248:249] op_sel:[0,0] op_sel_hi:[1,0]
	v_pk_add_f32 v[208:209], v[208:209], v[248:249] op_sel:[0,0] op_sel_hi:[1,0]
	v_rcp_f32_e32 v202, v202
; #define LAS __attribute__((address_space(3)))
; __device__ __forceinline__ float fast_exp(float x) { return __builtin_amdgcn_exp2f(x * 1.4426950408889634f); }
;     __device__ __forceinline__ void operator()(Acc& acc, const Unit& u, int wr, int wc, int fr_, int fq_, LAS unsigned char* le, int wid, int lane, int&) const {
;     ...
;                     for (int j = 0; j < 4; ++j) { const float r = fast_sigmoid(ra[j]), ig = fast_sigmoid(ri[j]);
;                         const float la = -8.0f * r * sl[j];
;                         const float a = fast_exp(la); const float x2 = 2.0f * la;
;                         const float ser = -x2 * (1.0f + x2 * (0.5f + x2 * (1.0f / 6.0f + x2 * (1.0f / 24.0f + x2 * (1.0f / 120.0f)))));
;                         const float om = (x2 > -0.3f) ? ser : (1.0f - a * a);
;                         const float uu = __builtin_amdgcn_sqrtf(om) * (ig * xv[j]);
;                         if (m == 0) { acc[ai][0][m][n][j] = a; acc[ai][1][m][n][j] = uu; }
;                         else { acc[ai][1][m][n][j] = a * acc[ai][1][m - 1][n][j] + uu; acc[ai][0][m][n][j] = acc[ai][0][m - 1][n][j] * a; } } } }
; #pragma unroll
;             for (int n = 0; n < 2; ++n)
; #pragma unroll
;                 for (int j = 0; j < 4; ++j) { float A = acc[ai][0][3][n][j], H = acc[ai][1][3][n][j];
;                     { const float Ap = DPP_SHR_ID(A, 1.0f, 0x111), Hp = DPP_SHR_ID(H, 0.0f, 0x111); H = A * Hp + H; A = Ap * A; }
;                     { const float Ap = DPP_SHR_ID(A, 1.0f, 0x112), Hp = DPP_SHR_ID(H, 0.0f, 0x112); H = A * Hp + H; A = Ap * A; }
;                     { const float Ap = DPP_SHR_ID(A, 1.0f, 0x114), Hp = DPP_SHR_ID(H, 0.0f, 0x114); H = A * Hp + H; A = Ap * A; }
;                     { const float Ap = DPP_SHR_ID(A, 1.0f, 0x118), Hp = DPP_SHR_ID(H, 0.0f, 0x118); H = A * Hp + H; A = Ap * A; }
;                     EA[ai][n][j] = DPP_SHR_ID(A, 1.0f, 0x111); EH[ai][n][j] = DPP_SHR_ID(H, 0.0f, 0x111);
;                     if (fr == 15) { LAS float* xp = X + (((ai * 2 + wr) * 128) + wc * 32 + n * 16 + fq * 4 + j) * 2; xp[0] = A; xp[1] = H; } }
;         }
;         u32x2 gpre[2][4][2];
; #pragma unroll
;         for (int m = 0; m < 4; ++m)
; #pragma unroll
;             for (int n = 0; n < 2; ++n) gpre[0][m][n] = *(const u32x2*)(gg + roff + (size_t)m * DM + n * 16);
	v_rcp_f32_e32 v203, v203
	v_rcp_f32_e32 v204, v204
	v_rcp_f32_e32 v205, v205
	v_rcp_f32_e32 v206, v206
	v_rcp_f32_e32 v207, v207
	v_rcp_f32_e32 v208, v208
	v_rcp_f32_e32 v209, v209
	v_lshlrev_b32_e32 v242, 16, v196
	v_and_b32_e32 v243, s22, v196
	v_lshlrev_b32_e32 v244, 16, v197
	v_and_b32_e32 v245, s22, v197
	v_pk_mul_f32 v[210:211], v[202:203], v[198:199] op_sel:[0,0] op_sel_hi:[1,1]
	v_pk_mul_f32 v[212:213], v[204:205], v[200:201] op_sel:[0,0] op_sel_hi:[1,1]
	v_pk_mul_f32 v[206:207], v[206:207], v[242:243] op_sel:[0,0] op_sel_hi:[1,1]
	v_pk_mul_f32 v[208:209], v[208:209], v[244:245] op_sel:[0,0] op_sel_hi:[1,1]
	v_pk_mul_f32 v[214:215], v[210:211], v[246:247] op_sel:[0,1] op_sel_hi:[1,1]
	v_pk_mul_f32 v[216:217], v[212:213], v[246:247] op_sel:[0,1] op_sel_hi:[1,1]
	v_pk_add_f32 v[210:211], v[210:211], v[210:211] op_sel:[0,0] op_sel_hi:[1,1]
	v_pk_add_f32 v[212:213], v[212:213], v[212:213] op_sel:[0,0] op_sel_hi:[1,1]
	v_exp_f32_e32 v214, v214
	v_exp_f32_e32 v215, v215
	v_exp_f32_e32 v216, v216
	v_exp_f32_e32 v217, v217
	v_pk_fma_f32 v[238:239], v[210:211], v[248:249], v[250:251] op_sel:[0,1,0] op_sel_hi:[1,1,0]
	v_pk_fma_f32 v[240:241], v[212:213], v[248:249], v[250:251] op_sel:[0,1,0] op_sel_hi:[1,1,0]
	v_pk_fma_f32 v[238:239], v[210:211], v[238:239], v[250:251] op_sel:[0,0,1] op_sel_hi:[1,1,1]
	v_pk_fma_f32 v[240:241], v[212:213], v[240:241], v[250:251] op_sel:[0,0,1] op_sel_hi:[1,1,1]
	v_pk_fma_f32 v[238:239], v[210:211], v[238:239], v[252:253] op_sel:[0,0,0] op_sel_hi:[1,1,0]
	v_pk_fma_f32 v[240:241], v[212:213], v[240:241], v[252:253] op_sel:[0,0,0] op_sel_hi:[1,1,0]
	v_pk_fma_f32 v[238:239], v[210:211], v[238:239], v[248:249] op_sel:[0,0,0] op_sel_hi:[1,1,0]
	v_pk_fma_f32 v[240:241], v[212:213], v[240:241], v[248:249] op_sel:[0,0,0] op_sel_hi:[1,1,0]
	v_pk_mul_f32 v[238:239], v[210:211], v[238:239] op_sel:[0,0] op_sel_hi:[1,1] neg_lo:[1,0] neg_hi:[1,0]
	v_pk_mul_f32 v[240:241], v[212:213], v[240:241] op_sel:[0,0] op_sel_hi:[1,1] neg_lo:[1,0] neg_hi:[1,0]
	v_pk_fma_f32 v[242:243], v[214:215], v[214:215], v[248:249] op_sel:[0,0,0] op_sel_hi:[1,1,0] neg_lo:[1,0,0] neg_hi:[1,0,0]
	v_pk_fma_f32 v[244:245], v[216:217], v[216:217], v[248:249] op_sel:[0,0,0] op_sel_hi:[1,1,0] neg_lo:[1,0,0] neg_hi:[1,0,0]
	v_cmp_lt_f32_e64 s[24:25], v253, v210
	v_cmp_lt_f32_e64 s[26:27], v253, v211
	v_cmp_lt_f32_e64 s[30:31], v253, v212
	v_cmp_lt_f32_e64 s[34:35], v253, v213
	v_cndmask_b32_e64 v238, v242, v238, s[24:25]
	v_cndmask_b32_e64 v239, v243, v239, s[26:27]
	v_cndmask_b32_e64 v240, v244, v240, s[30:31]
	v_cndmask_b32_e64 v241, v245, v241, s[34:35]
	v_sqrt_f32_e32 v238, v238
	v_sqrt_f32_e32 v239, v239
	v_sqrt_f32_e32 v240, v240
	v_sqrt_f32_e32 v241, v241
	v_pk_mul_f32 v[206:207], v[238:239], v[206:207] op_sel:[0,0] op_sel_hi:[1,1]
	v_pk_mul_f32 v[208:209], v[240:241], v[208:209] op_sel:[0,0] op_sel_hi:[1,1]
	v_pk_fma_f32 v[0:1], v[214:215], v[4:5], v[206:207] op_sel:[0,0,0] op_sel_hi:[1,1,1]
	v_pk_fma_f32 v[2:3], v[216:217], v[6:7], v[208:209] op_sel:[0,0,0] op_sel_hi:[1,1,1]
	v_pk_mul_f32 v[16:17], v[20:21], v[214:215] op_sel:[0,0] op_sel_hi:[1,1]
	v_pk_mul_f32 v[18:19], v[22:23], v[216:217] op_sel:[0,0] op_sel_hi:[1,1]
	global_load_dwordx2 v[166:167], v229, s[46:47] offset:0
	global_load_dwordx2 v[168:169], v229, s[46:47] offset:32
	global_load_dwordx2 v[170:171], v230, s[46:47] offset:0
	global_load_dwordx2 v[172:173], v230, s[46:47] offset:32
	global_load_dwordx2 v[174:175], v231, s[46:47] offset:0
	global_load_dwordx2 v[176:177], v231, s[46:47] offset:32
	global_load_dwordx2 v[178:179], v232, s[46:47] offset:0
	global_load_dwordx2 v[180:181], v232, s[46:47] offset:32
	global_load_dwordx2 v[182:183], v233, s[46:47] offset:0
	global_load_dwordx2 v[184:185], v233, s[46:47] offset:32
	global_load_dwordx2 v[186:187], v234, s[46:47] offset:0
	global_load_dwordx2 v[188:189], v234, s[46:47] offset:32
	global_load_dwordx2 v[190:191], v235, s[46:47] offset:0
	global_load_dwordx2 v[192:193], v235, s[46:47] offset:32
	global_load_dwordx2 v[194:195], v236, s[46:47] offset:0
	global_load_dwordx2 v[196:197], v236, s[46:47] offset:32
	v_cmp_eq_u32_e64 s[30:31], 15, v227
	s_lshl_b32 s8, s9, 7
	s_lshl_b32 s12, s10, 5
	s_add_i32 s8, s8, s12
	v_lshl_add_u32 v218, v224, 2, s8
	v_lshlrev_b32_e32 v218, 3, v218
	v_add_u32_e32 v218, 0x20000, v218
	v_mov_b32_e32 v202, v136
	v_mov_b32_e32 v203, v120
	v_mov_b32_e32 v204, v137
	v_mov_b32_e32 v205, v121
	v_mov_b32_e32 v206, v138
	v_mov_b32_e32 v207, v122
	v_mov_b32_e32 v208, v139
	v_mov_b32_e32 v209, v123
	v_mov_b32_e32 v210, v96
	v_mov_b32_e32 v211, v76
	v_mov_b32_e32 v212, v97
	v_mov_b32_e32 v213, v77
	v_mov_b32_e32 v214, v98
	v_mov_b32_e32 v215, v78
	v_mov_b32_e32 v216, v99
	v_mov_b32_e32 v217, v79
	v_fmac_f32_dpp v203, v203, v202 row_shr:1 row_mask:0xf bank_mask:0xf
	v_fmac_f32_dpp v205, v205, v204 row_shr:1 row_mask:0xf bank_mask:0xf
	v_fmac_f32_dpp v207, v207, v206 row_shr:1 row_mask:0xf bank_mask:0xf
	v_fmac_f32_dpp v209, v209, v208 row_shr:1 row_mask:0xf bank_mask:0xf
	v_fmac_f32_dpp v211, v211, v210 row_shr:1 row_mask:0xf bank_mask:0xf
	v_fmac_f32_dpp v213, v213, v212 row_shr:1 row_mask:0xf bank_mask:0xf
	v_fmac_f32_dpp v215, v215, v214 row_shr:1 row_mask:0xf bank_mask:0xf
	v_fmac_f32_dpp v217, v217, v216 row_shr:1 row_mask:0xf bank_mask:0xf
	v_mul_f32_dpp v202, v202, v202 row_shr:1 row_mask:0xf bank_mask:0xf
	v_mul_f32_dpp v204, v204, v204 row_shr:1 row_mask:0xf bank_mask:0xf
	v_mul_f32_dpp v206, v206, v206 row_shr:1 row_mask:0xf bank_mask:0xf
	v_mul_f32_dpp v208, v208, v208 row_shr:1 row_mask:0xf bank_mask:0xf
	v_mul_f32_dpp v210, v210, v210 row_shr:1 row_mask:0xf bank_mask:0xf
; #define LAS __attribute__((address_space(3)))
; #define DPP_SHR_ID(x, idv, ctrl) __builtin_bit_cast(float, __builtin_amdgcn_update_dpp(__builtin_bit_cast(int, (float)(idv)), __builtin_bit_cast(int, (x)), (ctrl), 0xf, 0xf, false))
;     __device__ __forceinline__ void operator()(Acc& acc, const Unit& u, int wr, int wc, int fr_, int fq_, LAS unsigned char* le, int wid, int lane, int&) const {
;     ...
;             for (int n = 0; n < 2; ++n)
; #pragma unroll
;                 for (int j = 0; j < 4; ++j) { float A = acc[ai][0][3][n][j], H = acc[ai][1][3][n][j];
;                     { const float Ap = DPP_SHR_ID(A, 1.0f, 0x111), Hp = DPP_SHR_ID(H, 0.0f, 0x111); H = A * Hp + H; A = Ap * A; }
;                     { const float Ap = DPP_SHR_ID(A, 1.0f, 0x112), Hp = DPP_SHR_ID(H, 0.0f, 0x112); H = A * Hp + H; A = Ap * A; }
;                     { const float Ap = DPP_SHR_ID(A, 1.0f, 0x114), Hp = DPP_SHR_ID(H, 0.0f, 0x114); H = A * Hp + H; A = Ap * A; }
;                     { const float Ap = DPP_SHR_ID(A, 1.0f, 0x118), Hp = DPP_SHR_ID(H, 0.0f, 0x118); H = A * Hp + H; A = Ap * A; }
;                     EA[ai][n][j] = DPP_SHR_ID(A, 1.0f, 0x111); EH[ai][n][j] = DPP_SHR_ID(H, 0.0f, 0x111);
;                     if (fr == 15) { LAS float* xp = X + (((ai * 2 + wr) * 128) + wc * 32 + n * 16 + fq * 4 + j) * 2; xp[0] = A; xp[1] = H; } }
;     ...
;                 for (int j = 0; j < 4; ++j) { const int c = wc * 32 + n * 16 + fq * 4 + j; float s = C0[c];
;                     if (ai == 1) { const f32x2 b0 = *(const LAS f32x2*)(X + (0 * 128 + c) * 2), b1 = *(const LAS f32x2*)(X + (1 * 128 + c) * 2); s = b0.x * s + b0.y; s = b1.x * s + b1.y; }
;                     if (wr == 1) { const f32x2 b2 = *(const LAS f32x2*)(X + ((ai * 2) * 128 + c) * 2); s = b2.x * s + b2.y; }
;                     cl[n][j] = EA[ai][n][j] * s + EH[ai][n][j]; }
; #pragma unroll
;             for (int m = 0; m < 4; ++m) {
; #pragma unroll
;                 for (int n = 0; n < 2; ++n) { const u32x2 gw = gpre[ai][m][n]; const float gv[4] = {bflo(gw.x), bfhi(gw.x), bflo(gw.y), bfhi(gw.y)}; float y[4];
; #pragma unroll
;                     for (int j = 0; j < 4; ++j) y[j] = (acc[ai][0][m][n][j] * cl[n][j] + acc[ai][1][m][n][j]) * gv[j];
	v_mul_f32_dpp v212, v212, v212 row_shr:1 row_mask:0xf bank_mask:0xf
	v_mul_f32_dpp v214, v214, v214 row_shr:1 row_mask:0xf bank_mask:0xf
	v_mul_f32_dpp v216, v216, v216 row_shr:1 row_mask:0xf bank_mask:0xf
	v_fmac_f32_dpp v203, v203, v202 row_shr:2 row_mask:0xf bank_mask:0xf
	v_fmac_f32_dpp v205, v205, v204 row_shr:2 row_mask:0xf bank_mask:0xf
	v_fmac_f32_dpp v207, v207, v206 row_shr:2 row_mask:0xf bank_mask:0xf
	v_fmac_f32_dpp v209, v209, v208 row_shr:2 row_mask:0xf bank_mask:0xf
	v_fmac_f32_dpp v211, v211, v210 row_shr:2 row_mask:0xf bank_mask:0xf
	v_fmac_f32_dpp v213, v213, v212 row_shr:2 row_mask:0xf bank_mask:0xf
	v_fmac_f32_dpp v215, v215, v214 row_shr:2 row_mask:0xf bank_mask:0xf
	v_fmac_f32_dpp v217, v217, v216 row_shr:2 row_mask:0xf bank_mask:0xf
	v_mul_f32_dpp v202, v202, v202 row_shr:2 row_mask:0xf bank_mask:0xf
	v_mul_f32_dpp v204, v204, v204 row_shr:2 row_mask:0xf bank_mask:0xf
	v_mul_f32_dpp v206, v206, v206 row_shr:2 row_mask:0xf bank_mask:0xf
	v_mul_f32_dpp v208, v208, v208 row_shr:2 row_mask:0xf bank_mask:0xf
	v_mul_f32_dpp v210, v210, v210 row_shr:2 row_mask:0xf bank_mask:0xf
	v_mul_f32_dpp v212, v212, v212 row_shr:2 row_mask:0xf bank_mask:0xf
	v_mul_f32_dpp v214, v214, v214 row_shr:2 row_mask:0xf bank_mask:0xf
	v_mul_f32_dpp v216, v216, v216 row_shr:2 row_mask:0xf bank_mask:0xf
	v_fmac_f32_dpp v203, v203, v202 row_shr:4 row_mask:0xf bank_mask:0xf
	v_fmac_f32_dpp v205, v205, v204 row_shr:4 row_mask:0xf bank_mask:0xf
	v_fmac_f32_dpp v207, v207, v206 row_shr:4 row_mask:0xf bank_mask:0xf
	v_fmac_f32_dpp v209, v209, v208 row_shr:4 row_mask:0xf bank_mask:0xf
	v_fmac_f32_dpp v211, v211, v210 row_shr:4 row_mask:0xf bank_mask:0xf
	v_fmac_f32_dpp v213, v213, v212 row_shr:4 row_mask:0xf bank_mask:0xf
	v_fmac_f32_dpp v215, v215, v214 row_shr:4 row_mask:0xf bank_mask:0xf
	v_fmac_f32_dpp v217, v217, v216 row_shr:4 row_mask:0xf bank_mask:0xf
	v_mul_f32_dpp v202, v202, v202 row_shr:4 row_mask:0xf bank_mask:0xf
	v_mul_f32_dpp v204, v204, v204 row_shr:4 row_mask:0xf bank_mask:0xf
	v_mul_f32_dpp v206, v206, v206 row_shr:4 row_mask:0xf bank_mask:0xf
	v_mul_f32_dpp v208, v208, v208 row_shr:4 row_mask:0xf bank_mask:0xf
	v_mul_f32_dpp v210, v210, v210 row_shr:4 row_mask:0xf bank_mask:0xf
	v_mul_f32_dpp v212, v212, v212 row_shr:4 row_mask:0xf bank_mask:0xf
	v_mul_f32_dpp v214, v214, v214 row_shr:4 row_mask:0xf bank_mask:0xf
	v_mul_f32_dpp v216, v216, v216 row_shr:4 row_mask:0xf bank_mask:0xf
	v_fmac_f32_dpp v203, v203, v202 row_shr:8 row_mask:0xf bank_mask:0xf
	v_fmac_f32_dpp v205, v205, v204 row_shr:8 row_mask:0xf bank_mask:0xf
	v_fmac_f32_dpp v207, v207, v206 row_shr:8 row_mask:0xf bank_mask:0xf
	v_fmac_f32_dpp v209, v209, v208 row_shr:8 row_mask:0xf bank_mask:0xf
	v_fmac_f32_dpp v211, v211, v210 row_shr:8 row_mask:0xf bank_mask:0xf
	v_fmac_f32_dpp v213, v213, v212 row_shr:8 row_mask:0xf bank_mask:0xf
	v_fmac_f32_dpp v215, v215, v214 row_shr:8 row_mask:0xf bank_mask:0xf
	v_fmac_f32_dpp v217, v217, v216 row_shr:8 row_mask:0xf bank_mask:0xf
	v_mul_f32_dpp v202, v202, v202 row_shr:8 row_mask:0xf bank_mask:0xf
	v_mul_f32_dpp v204, v204, v204 row_shr:8 row_mask:0xf bank_mask:0xf
	v_mul_f32_dpp v206, v206, v206 row_shr:8 row_mask:0xf bank_mask:0xf
	v_mul_f32_dpp v208, v208, v208 row_shr:8 row_mask:0xf bank_mask:0xf
	v_mul_f32_dpp v210, v210, v210 row_shr:8 row_mask:0xf bank_mask:0xf
	v_mul_f32_dpp v212, v212, v212 row_shr:8 row_mask:0xf bank_mask:0xf
	v_mul_f32_dpp v214, v214, v214 row_shr:8 row_mask:0xf bank_mask:0xf
	v_mul_f32_dpp v216, v216, v216 row_shr:8 row_mask:0xf bank_mask:0xf
	v_mov_b32_e32 v238, 1.0
	v_mov_b32_e32 v239, 0
	v_mov_b32_e32 v240, 1.0
	v_mov_b32_e32 v241, 0
	v_mov_b32_e32 v242, 1.0
	v_mov_b32_e32 v243, 0
	v_mov_b32_e32 v244, 1.0
	v_mov_b32_e32 v245, 0
	v_mov_b32_e32 v246, 1.0
	v_mov_b32_e32 v247, 0
	v_mov_b32_e32 v248, 1.0
	v_mov_b32_e32 v249, 0
	v_mov_b32_e32 v250, 1.0
	v_mov_b32_e32 v251, 0
	v_mov_b32_e32 v252, 1.0
	v_mov_b32_e32 v253, 0
	v_mov_b32_dpp v238, v202 row_shr:1 row_mask:0xf bank_mask:0xf
	v_mov_b32_dpp v239, v203 row_shr:1 row_mask:0xf bank_mask:0xf
	v_mov_b32_dpp v240, v204 row_shr:1 row_mask:0xf bank_mask:0xf
	v_mov_b32_dpp v241, v205 row_shr:1 row_mask:0xf bank_mask:0xf
	v_mov_b32_dpp v242, v206 row_shr:1 row_mask:0xf bank_mask:0xf
	v_mov_b32_dpp v243, v207 row_shr:1 row_mask:0xf bank_mask:0xf
	v_mov_b32_dpp v244, v208 row_shr:1 row_mask:0xf bank_mask:0xf
	v_mov_b32_dpp v245, v209 row_shr:1 row_mask:0xf bank_mask:0xf
	v_mov_b32_dpp v246, v210 row_shr:1 row_mask:0xf bank_mask:0xf
	v_mov_b32_dpp v247, v211 row_shr:1 row_mask:0xf bank_mask:0xf
	v_mov_b32_dpp v248, v212 row_shr:1 row_mask:0xf bank_mask:0xf
	v_mov_b32_dpp v249, v213 row_shr:1 row_mask:0xf bank_mask:0xf
	v_mov_b32_dpp v250, v214 row_shr:1 row_mask:0xf bank_mask:0xf
	v_mov_b32_dpp v251, v215 row_shr:1 row_mask:0xf bank_mask:0xf
	v_mov_b32_dpp v252, v216 row_shr:1 row_mask:0xf bank_mask:0xf
	v_mov_b32_dpp v253, v217 row_shr:1 row_mask:0xf bank_mask:0xf
	s_and_saveexec_b64 s[34:35], s[30:31]
	ds_write_b64 v218, v[202:203] offset:0
	ds_write_b64 v218, v[204:205] offset:8
	ds_write_b64 v218, v[206:207] offset:16
	ds_write_b64 v218, v[208:209] offset:24
	ds_write_b64 v218, v[210:211] offset:128
	ds_write_b64 v218, v[212:213] offset:136
	ds_write_b64 v218, v[214:215] offset:144
	ds_write_b64 v218, v[216:217] offset:152
	s_mov_b64 exec, s[34:35]
	v_fmac_f32_e32 v132, v148, v239
	v_fmac_f32_e32 v133, v149, v241
	v_fmac_f32_e32 v134, v150, v243
	v_fmac_f32_e32 v135, v151, v245
	v_mul_f32_e32 v148, v148, v238
	v_mul_f32_e32 v149, v149, v240
	v_mul_f32_e32 v150, v150, v242
	v_mul_f32_e32 v151, v151, v244
	v_fmac_f32_e32 v92, v116, v247
	v_fmac_f32_e32 v93, v117, v249
; #define LAS __attribute__((address_space(3)))
; #define DPP_SHR_ID(x, idv, ctrl) __builtin_bit_cast(float, __builtin_amdgcn_update_dpp(__builtin_bit_cast(int, (float)(idv)), __builtin_bit_cast(int, (x)), (ctrl), 0xf, 0xf, false))
;     __device__ __forceinline__ void operator()(Acc& acc, const Unit& u, int wr, int wc, int fr_, int fq_, LAS unsigned char* le, int wid, int lane, int&) const {
;     ...
;             for (int n = 0; n < 2; ++n)
; #pragma unroll
;                 for (int j = 0; j < 4; ++j) { float A = acc[ai][0][3][n][j], H = acc[ai][1][3][n][j];
;                     { const float Ap = DPP_SHR_ID(A, 1.0f, 0x111), Hp = DPP_SHR_ID(H, 0.0f, 0x111); H = A * Hp + H; A = Ap * A; }
;                     { const float Ap = DPP_SHR_ID(A, 1.0f, 0x112), Hp = DPP_SHR_ID(H, 0.0f, 0x112); H = A * Hp + H; A = Ap * A; }
;                     { const float Ap = DPP_SHR_ID(A, 1.0f, 0x114), Hp = DPP_SHR_ID(H, 0.0f, 0x114); H = A * Hp + H; A = Ap * A; }
;                     { const float Ap = DPP_SHR_ID(A, 1.0f, 0x118), Hp = DPP_SHR_ID(H, 0.0f, 0x118); H = A * Hp + H; A = Ap * A; }
;                     EA[ai][n][j] = DPP_SHR_ID(A, 1.0f, 0x111); EH[ai][n][j] = DPP_SHR_ID(H, 0.0f, 0x111);
;                     if (fr == 15) { LAS float* xp = X + (((ai * 2 + wr) * 128) + wc * 32 + n * 16 + fq * 4 + j) * 2; xp[0] = A; xp[1] = H; } }
;     ...
;                 for (int j = 0; j < 4; ++j) { const int c = wc * 32 + n * 16 + fq * 4 + j; float s = C0[c];
;                     if (ai == 1) { const f32x2 b0 = *(const LAS f32x2*)(X + (0 * 128 + c) * 2), b1 = *(const LAS f32x2*)(X + (1 * 128 + c) * 2); s = b0.x * s + b0.y; s = b1.x * s + b1.y; }
;                     if (wr == 1) { const f32x2 b2 = *(const LAS f32x2*)(X + ((ai * 2) * 128 + c) * 2); s = b2.x * s + b2.y; }
;                     cl[n][j] = EA[ai][n][j] * s + EH[ai][n][j]; }
; #pragma unroll
;             for (int m = 0; m < 4; ++m) {
; #pragma unroll
;                 for (int n = 0; n < 2; ++n) { const u32x2 gw = gpre[ai][m][n]; const float gv[4] = {bflo(gw.x), bfhi(gw.x), bflo(gw.y), bfhi(gw.y)}; float y[4];
; #pragma unroll
;                     for (int j = 0; j < 4; ++j) y[j] = (acc[ai][0][m][n][j] * cl[n][j] + acc[ai][1][m][n][j]) * gv[j];
	v_fmac_f32_e32 v94, v118, v251
	v_fmac_f32_e32 v95, v119, v253
	v_mul_f32_e32 v116, v116, v246
	v_mul_f32_e32 v117, v117, v248
	v_mul_f32_e32 v118, v118, v250
	v_mul_f32_e32 v119, v119, v252
	v_fmac_f32_e32 v128, v144, v239
	v_fmac_f32_e32 v129, v145, v241
	v_fmac_f32_e32 v130, v146, v243
	v_fmac_f32_e32 v131, v147, v245
	v_mul_f32_e32 v144, v144, v238
	v_mul_f32_e32 v145, v145, v240
	v_mul_f32_e32 v146, v146, v242
	v_mul_f32_e32 v147, v147, v244
	v_fmac_f32_e32 v84, v112, v247
	v_fmac_f32_e32 v85, v113, v249
	v_fmac_f32_e32 v86, v114, v251
	v_fmac_f32_e32 v87, v115, v253
	v_mul_f32_e32 v112, v112, v246
	v_mul_f32_e32 v113, v113, v248
	v_mul_f32_e32 v114, v114, v250
	v_mul_f32_e32 v115, v115, v252
	v_fmac_f32_e32 v124, v140, v239
	v_fmac_f32_e32 v125, v141, v241
	v_fmac_f32_e32 v126, v142, v243
	v_fmac_f32_e32 v127, v143, v245
	v_mul_f32_e32 v140, v140, v238
	v_mul_f32_e32 v141, v141, v240
	v_mul_f32_e32 v142, v142, v242
	v_mul_f32_e32 v143, v143, v244
	v_fmac_f32_e32 v80, v108, v247
	v_fmac_f32_e32 v81, v109, v249
	v_fmac_f32_e32 v82, v110, v251
	v_fmac_f32_e32 v83, v111, v253
	v_mul_f32_e32 v108, v108, v246
	v_mul_f32_e32 v109, v109, v248
	v_mul_f32_e32 v110, v110, v250
	v_mul_f32_e32 v111, v111, v252
	v_fmac_f32_e32 v120, v136, v239
	v_fmac_f32_e32 v121, v137, v241
	v_fmac_f32_e32 v122, v138, v243
	v_fmac_f32_e32 v123, v139, v245
	v_mul_f32_e32 v136, v136, v238
	v_mul_f32_e32 v137, v137, v240
	v_mul_f32_e32 v138, v138, v242
	v_mul_f32_e32 v139, v139, v244
	v_fmac_f32_e32 v76, v96, v247
	v_fmac_f32_e32 v77, v97, v249
	v_fmac_f32_e32 v78, v98, v251
	v_fmac_f32_e32 v79, v99, v253
	v_mul_f32_e32 v96, v96, v246
	v_mul_f32_e32 v97, v97, v248
	v_mul_f32_e32 v98, v98, v250
	v_mul_f32_e32 v99, v99, v252
	v_mov_b32_e32 v202, v48
	v_mov_b32_e32 v203, v32
	v_mov_b32_e32 v204, v49
	v_mov_b32_e32 v205, v33
	v_mov_b32_e32 v206, v50
	v_mov_b32_e32 v207, v34
	v_mov_b32_e32 v208, v51
	v_mov_b32_e32 v209, v35
	v_mov_b32_e32 v210, v16
	v_mov_b32_e32 v211, v0
	v_mov_b32_e32 v212, v17
	v_mov_b32_e32 v213, v1
	v_mov_b32_e32 v214, v18
	v_mov_b32_e32 v215, v2
	v_mov_b32_e32 v216, v19
	v_mov_b32_e32 v217, v3
	v_fmac_f32_dpp v203, v203, v202 row_shr:1 row_mask:0xf bank_mask:0xf
	v_fmac_f32_dpp v205, v205, v204 row_shr:1 row_mask:0xf bank_mask:0xf
	v_fmac_f32_dpp v207, v207, v206 row_shr:1 row_mask:0xf bank_mask:0xf
	v_fmac_f32_dpp v209, v209, v208 row_shr:1 row_mask:0xf bank_mask:0xf
	v_fmac_f32_dpp v211, v211, v210 row_shr:1 row_mask:0xf bank_mask:0xf
	v_fmac_f32_dpp v213, v213, v212 row_shr:1 row_mask:0xf bank_mask:0xf
	v_fmac_f32_dpp v215, v215, v214 row_shr:1 row_mask:0xf bank_mask:0xf
	v_fmac_f32_dpp v217, v217, v216 row_shr:1 row_mask:0xf bank_mask:0xf
	v_mul_f32_dpp v202, v202, v202 row_shr:1 row_mask:0xf bank_mask:0xf
	v_mul_f32_dpp v204, v204, v204 row_shr:1 row_mask:0xf bank_mask:0xf
	v_mul_f32_dpp v206, v206, v206 row_shr:1 row_mask:0xf bank_mask:0xf
	v_mul_f32_dpp v208, v208, v208 row_shr:1 row_mask:0xf bank_mask:0xf
	v_mul_f32_dpp v210, v210, v210 row_shr:1 row_mask:0xf bank_mask:0xf
	v_mul_f32_dpp v212, v212, v212 row_shr:1 row_mask:0xf bank_mask:0xf
	v_mul_f32_dpp v214, v214, v214 row_shr:1 row_mask:0xf bank_mask:0xf
	v_mul_f32_dpp v216, v216, v216 row_shr:1 row_mask:0xf bank_mask:0xf
	v_fmac_f32_dpp v203, v203, v202 row_shr:2 row_mask:0xf bank_mask:0xf
	v_fmac_f32_dpp v205, v205, v204 row_shr:2 row_mask:0xf bank_mask:0xf
	v_fmac_f32_dpp v207, v207, v206 row_shr:2 row_mask:0xf bank_mask:0xf
	v_fmac_f32_dpp v209, v209, v208 row_shr:2 row_mask:0xf bank_mask:0xf
	v_fmac_f32_dpp v211, v211, v210 row_shr:2 row_mask:0xf bank_mask:0xf
	v_fmac_f32_dpp v213, v213, v212 row_shr:2 row_mask:0xf bank_mask:0xf
	v_fmac_f32_dpp v215, v215, v214 row_shr:2 row_mask:0xf bank_mask:0xf
	v_fmac_f32_dpp v217, v217, v216 row_shr:2 row_mask:0xf bank_mask:0xf
	v_mul_f32_dpp v202, v202, v202 row_shr:2 row_mask:0xf bank_mask:0xf
	v_mul_f32_dpp v204, v204, v204 row_shr:2 row_mask:0xf bank_mask:0xf
	v_mul_f32_dpp v206, v206, v206 row_shr:2 row_mask:0xf bank_mask:0xf
	v_mul_f32_dpp v208, v208, v208 row_shr:2 row_mask:0xf bank_mask:0xf
	v_mul_f32_dpp v210, v210, v210 row_shr:2 row_mask:0xf bank_mask:0xf
	v_mul_f32_dpp v212, v212, v212 row_shr:2 row_mask:0xf bank_mask:0xf
	v_mul_f32_dpp v214, v214, v214 row_shr:2 row_mask:0xf bank_mask:0xf
	v_mul_f32_dpp v216, v216, v216 row_shr:2 row_mask:0xf bank_mask:0xf
	v_fmac_f32_dpp v203, v203, v202 row_shr:4 row_mask:0xf bank_mask:0xf
	v_fmac_f32_dpp v205, v205, v204 row_shr:4 row_mask:0xf bank_mask:0xf
	v_fmac_f32_dpp v207, v207, v206 row_shr:4 row_mask:0xf bank_mask:0xf
	v_fmac_f32_dpp v209, v209, v208 row_shr:4 row_mask:0xf bank_mask:0xf
	v_fmac_f32_dpp v211, v211, v210 row_shr:4 row_mask:0xf bank_mask:0xf
	v_fmac_f32_dpp v213, v213, v212 row_shr:4 row_mask:0xf bank_mask:0xf
	v_fmac_f32_dpp v215, v215, v214 row_shr:4 row_mask:0xf bank_mask:0xf
	v_fmac_f32_dpp v217, v217, v216 row_shr:4 row_mask:0xf bank_mask:0xf
	v_mul_f32_dpp v202, v202, v202 row_shr:4 row_mask:0xf bank_mask:0xf
	v_mul_f32_dpp v204, v204, v204 row_shr:4 row_mask:0xf bank_mask:0xf
	v_mul_f32_dpp v206, v206, v206 row_shr:4 row_mask:0xf bank_mask:0xf
	v_mul_f32_dpp v208, v208, v208 row_shr:4 row_mask:0xf bank_mask:0xf
	v_mul_f32_dpp v210, v210, v210 row_shr:4 row_mask:0xf bank_mask:0xf
	v_mul_f32_dpp v212, v212, v212 row_shr:4 row_mask:0xf bank_mask:0xf
	v_mul_f32_dpp v214, v214, v214 row_shr:4 row_mask:0xf bank_mask:0xf
	v_mul_f32_dpp v216, v216, v216 row_shr:4 row_mask:0xf bank_mask:0xf
	v_fmac_f32_dpp v203, v203, v202 row_shr:8 row_mask:0xf bank_mask:0xf
	v_fmac_f32_dpp v205, v205, v204 row_shr:8 row_mask:0xf bank_mask:0xf
	v_fmac_f32_dpp v207, v207, v206 row_shr:8 row_mask:0xf bank_mask:0xf
; #define LAS __attribute__((address_space(3)))
; #define EPI_BAR() do { asm volatile("s_waitcnt lgkmcnt(0)" ::: "memory"); __builtin_amdgcn_s_barrier(); asm volatile("" ::: "memory"); } while (0)
; #define DPP_SHR_ID(x, idv, ctrl) __builtin_bit_cast(float, __builtin_amdgcn_update_dpp(__builtin_bit_cast(int, (float)(idv)), __builtin_bit_cast(int, (x)), (ctrl), 0xf, 0xf, false))
;     __device__ __forceinline__ void operator()(Acc& acc, const Unit& u, int wr, int wc, int fr_, int fq_, LAS unsigned char* le, int wid, int lane, int&) const {
;     ...
;             for (int n = 0; n < 2; ++n)
; #pragma unroll
;                 for (int j = 0; j < 4; ++j) { float A = acc[ai][0][3][n][j], H = acc[ai][1][3][n][j];
;                     { const float Ap = DPP_SHR_ID(A, 1.0f, 0x111), Hp = DPP_SHR_ID(H, 0.0f, 0x111); H = A * Hp + H; A = Ap * A; }
;                     { const float Ap = DPP_SHR_ID(A, 1.0f, 0x112), Hp = DPP_SHR_ID(H, 0.0f, 0x112); H = A * Hp + H; A = Ap * A; }
;                     { const float Ap = DPP_SHR_ID(A, 1.0f, 0x114), Hp = DPP_SHR_ID(H, 0.0f, 0x114); H = A * Hp + H; A = Ap * A; }
;                     { const float Ap = DPP_SHR_ID(A, 1.0f, 0x118), Hp = DPP_SHR_ID(H, 0.0f, 0x118); H = A * Hp + H; A = Ap * A; }
;                     EA[ai][n][j] = DPP_SHR_ID(A, 1.0f, 0x111); EH[ai][n][j] = DPP_SHR_ID(H, 0.0f, 0x111);
;                     if (fr == 15) { LAS float* xp = X + (((ai * 2 + wr) * 128) + wc * 32 + n * 16 + fq * 4 + j) * 2; xp[0] = A; xp[1] = H; } }
;         }
;         u32x2 gpre[2][4][2];
; #pragma unroll
;         for (int m = 0; m < 4; ++m)
; #pragma unroll
;             for (int n = 0; n < 2; ++n) gpre[0][m][n] = *(const u32x2*)(gg + roff + (size_t)m * DM + n * 16);
;         EPI_BAR();
;         if (tid < 128) { float TA = 1.f, TH = 0.f;
; #pragma unroll
;             for (int blk = 0; blk < 4; ++blk) { const f32x2 ah = *(const LAS f32x2*)(X + (blk * 128 + tid) * 2); TH = ah.x * TH + ah.y; TA = TA * ah.x; }
;             __hip_atomic_store((unsigned long long*)(agg + ((size_t)u.pm * DM + chb + tid) * 2), __builtin_bit_cast(unsigned long long, (f32x2){TA, TH}), __ATOMIC_RELAXED, __HIP_MEMORY_SCOPE_AGENT);
;             asm volatile("s_waitcnt vmcnt(0)" ::: "memory"); }
	v_fmac_f32_dpp v209, v209, v208 row_shr:8 row_mask:0xf bank_mask:0xf
	v_fmac_f32_dpp v211, v211, v210 row_shr:8 row_mask:0xf bank_mask:0xf
	v_fmac_f32_dpp v213, v213, v212 row_shr:8 row_mask:0xf bank_mask:0xf
	v_fmac_f32_dpp v215, v215, v214 row_shr:8 row_mask:0xf bank_mask:0xf
	v_fmac_f32_dpp v217, v217, v216 row_shr:8 row_mask:0xf bank_mask:0xf
	v_mul_f32_dpp v202, v202, v202 row_shr:8 row_mask:0xf bank_mask:0xf
	v_mul_f32_dpp v204, v204, v204 row_shr:8 row_mask:0xf bank_mask:0xf
	v_mul_f32_dpp v206, v206, v206 row_shr:8 row_mask:0xf bank_mask:0xf
	v_mul_f32_dpp v208, v208, v208 row_shr:8 row_mask:0xf bank_mask:0xf
	v_mul_f32_dpp v210, v210, v210 row_shr:8 row_mask:0xf bank_mask:0xf
	v_mul_f32_dpp v212, v212, v212 row_shr:8 row_mask:0xf bank_mask:0xf
	v_mul_f32_dpp v214, v214, v214 row_shr:8 row_mask:0xf bank_mask:0xf
	v_mul_f32_dpp v216, v216, v216 row_shr:8 row_mask:0xf bank_mask:0xf
	v_mov_b32_e32 v238, 1.0
	v_mov_b32_e32 v239, 0
	v_mov_b32_e32 v240, 1.0
	v_mov_b32_e32 v241, 0
	v_mov_b32_e32 v242, 1.0
	v_mov_b32_e32 v243, 0
	v_mov_b32_e32 v244, 1.0
	v_mov_b32_e32 v245, 0
	v_mov_b32_e32 v246, 1.0
	v_mov_b32_e32 v247, 0
	v_mov_b32_e32 v248, 1.0
	v_mov_b32_e32 v249, 0
	v_mov_b32_e32 v250, 1.0
	v_mov_b32_e32 v251, 0
	v_mov_b32_e32 v252, 1.0
	v_mov_b32_e32 v253, 0
	v_mov_b32_dpp v238, v202 row_shr:1 row_mask:0xf bank_mask:0xf
	v_mov_b32_dpp v239, v203 row_shr:1 row_mask:0xf bank_mask:0xf
	v_mov_b32_dpp v240, v204 row_shr:1 row_mask:0xf bank_mask:0xf
	v_mov_b32_dpp v241, v205 row_shr:1 row_mask:0xf bank_mask:0xf
	v_mov_b32_dpp v242, v206 row_shr:1 row_mask:0xf bank_mask:0xf
	v_mov_b32_dpp v243, v207 row_shr:1 row_mask:0xf bank_mask:0xf
	v_mov_b32_dpp v244, v208 row_shr:1 row_mask:0xf bank_mask:0xf
	v_mov_b32_dpp v245, v209 row_shr:1 row_mask:0xf bank_mask:0xf
	v_mov_b32_dpp v246, v210 row_shr:1 row_mask:0xf bank_mask:0xf
	v_mov_b32_dpp v247, v211 row_shr:1 row_mask:0xf bank_mask:0xf
	v_mov_b32_dpp v248, v212 row_shr:1 row_mask:0xf bank_mask:0xf
	v_mov_b32_dpp v249, v213 row_shr:1 row_mask:0xf bank_mask:0xf
	v_mov_b32_dpp v250, v214 row_shr:1 row_mask:0xf bank_mask:0xf
	v_mov_b32_dpp v251, v215 row_shr:1 row_mask:0xf bank_mask:0xf
	v_mov_b32_dpp v252, v216 row_shr:1 row_mask:0xf bank_mask:0xf
	v_mov_b32_dpp v253, v217 row_shr:1 row_mask:0xf bank_mask:0xf
	s_and_saveexec_b64 s[34:35], s[30:31]
	ds_write_b64 v218, v[202:203] offset:2048
	ds_write_b64 v218, v[204:205] offset:2056
	ds_write_b64 v218, v[206:207] offset:2064
	ds_write_b64 v218, v[208:209] offset:2072
	ds_write_b64 v218, v[210:211] offset:2176
	ds_write_b64 v218, v[212:213] offset:2184
	ds_write_b64 v218, v[214:215] offset:2192
	ds_write_b64 v218, v[216:217] offset:2200
	s_mov_b64 exec, s[34:35]
	v_fmac_f32_e32 v44, v64, v239
	v_fmac_f32_e32 v45, v65, v241
	v_fmac_f32_e32 v46, v66, v243
	v_fmac_f32_e32 v47, v67, v245
	v_mul_f32_e32 v64, v64, v238
	v_mul_f32_e32 v65, v65, v240
	v_mul_f32_e32 v66, v66, v242
	v_mul_f32_e32 v67, v67, v244
	v_fmac_f32_e32 v12, v28, v247
	v_fmac_f32_e32 v13, v29, v249
	v_fmac_f32_e32 v14, v30, v251
	v_fmac_f32_e32 v15, v31, v253
	v_mul_f32_e32 v28, v28, v246
	v_mul_f32_e32 v29, v29, v248
	v_mul_f32_e32 v30, v30, v250
	v_mul_f32_e32 v31, v31, v252
	v_fmac_f32_e32 v40, v60, v239
	v_fmac_f32_e32 v41, v61, v241
	v_fmac_f32_e32 v42, v62, v243
	v_fmac_f32_e32 v43, v63, v245
	v_mul_f32_e32 v60, v60, v238
	v_mul_f32_e32 v61, v61, v240
	v_mul_f32_e32 v62, v62, v242
	v_mul_f32_e32 v63, v63, v244
	v_fmac_f32_e32 v8, v24, v247
	v_fmac_f32_e32 v9, v25, v249
	v_fmac_f32_e32 v10, v26, v251
	v_fmac_f32_e32 v11, v27, v253
	v_mul_f32_e32 v24, v24, v246
	v_mul_f32_e32 v25, v25, v248
	v_mul_f32_e32 v26, v26, v250
	v_mul_f32_e32 v27, v27, v252
	v_fmac_f32_e32 v36, v52, v239
	v_fmac_f32_e32 v37, v53, v241
	v_fmac_f32_e32 v38, v54, v243
	v_fmac_f32_e32 v39, v55, v245
	v_mul_f32_e32 v52, v52, v238
	v_mul_f32_e32 v53, v53, v240
	v_mul_f32_e32 v54, v54, v242
	v_mul_f32_e32 v55, v55, v244
	v_fmac_f32_e32 v4, v20, v247
	v_fmac_f32_e32 v5, v21, v249
	v_fmac_f32_e32 v6, v22, v251
	v_fmac_f32_e32 v7, v23, v253
	v_mul_f32_e32 v20, v20, v246
	v_mul_f32_e32 v21, v21, v248
	v_mul_f32_e32 v22, v22, v250
	v_mul_f32_e32 v23, v23, v252
	v_fmac_f32_e32 v32, v48, v239
	v_fmac_f32_e32 v33, v49, v241
	v_fmac_f32_e32 v34, v50, v243
	v_fmac_f32_e32 v35, v51, v245
	v_mul_f32_e32 v48, v48, v238
	v_mul_f32_e32 v49, v49, v240
	v_mul_f32_e32 v50, v50, v242
	v_mul_f32_e32 v51, v51, v244
	v_fmac_f32_e32 v0, v16, v247
	v_fmac_f32_e32 v1, v17, v249
	v_fmac_f32_e32 v2, v18, v251
	v_fmac_f32_e32 v3, v19, v253
	v_mul_f32_e32 v16, v16, v246
	v_mul_f32_e32 v17, v17, v248
	v_mul_f32_e32 v18, v18, v250
	v_mul_f32_e32 v19, v19, v252
	s_waitcnt lgkmcnt(0)
	s_barrier
	s_cmp_lt_u32 s91, 0x80
	s_cbranch_scc0 .Lp9_lb_skip1
	v_lshlrev_b32_e32 v202, 3, v228
	v_add_u32_e32 v202, 0x20000, v202
	ds_read_b64 v[204:205], v202 offset:0
	ds_read_b64 v[206:207], v202 offset:1024
	ds_read_b64 v[208:209], v202 offset:2048
	ds_read_b64 v[210:211], v202 offset:3072
	s_lshl_b32 s8, s18, 11
	s_add_i32 s8, s8, s11
	v_add_u32_e32 v203, s8, v228
	v_lshlrev_b32_e32 v203, 3, v203
	s_waitcnt lgkmcnt(0)
	v_mov_b32_e32 v212, v204
	v_mov_b32_e32 v213, v205
	v_fma_f32 v213, v206, v213, v207
	v_mul_f32_e32 v212, v212, v206
	v_fma_f32 v213, v208, v213, v209
	v_mul_f32_e32 v212, v212, v208
	v_fma_f32 v213, v210, v213, v211
	v_mul_f32_e32 v212, v212, v210
	global_store_dwordx2 v203, v[212:213], s[50:51] sc1
	s_waitcnt vmcnt(0)
; #define LAS __attribute__((address_space(3)))
; #define EPI_BAR() do { asm volatile("s_waitcnt lgkmcnt(0)" ::: "memory"); __builtin_amdgcn_s_barrier(); asm volatile("" ::: "memory"); } while (0)
;     __device__ __forceinline__ void operator()(Acc& acc, const Unit& u, int wr, int wc, int fr_, int fq_, LAS unsigned char* le, int wid, int lane, int&) const {
;     ...
;         EPI_BAR();
;         if (tid == 0) __hip_atomic_store(flags + u.pm * 16 + u.pn, 1u, __ATOMIC_RELAXED, __HIP_MEMORY_SCOPE_AGENT);
;         if (tid < 128) { const int pm0 = u.pm & ~15, np = u.pm & 15; float h0 = 0.f;
;             { const int q = lane & 15; unsigned sp = 0;
;                 for (;;) { const unsigned f = (q < np) ? __hip_atomic_load(flags + (pm0 + q) * 16 + u.pn, __ATOMIC_RELAXED, __HIP_MEMORY_SCOPE_AGENT) : 1u;
;                     if (__builtin_amdgcn_ballot_w64(f == 0u) == 0ull) break;
;                     __builtin_amdgcn_s_sleep(1); if (++sp > (1u << 14)) break; } }
;             asm volatile("" ::: "memory");
;             f32x2 ahs[15];
; #pragma unroll
;             for (int q = 0; q < 15; ++q) { const int qq = q < np ? q : 0;
;                 ahs[q] = __builtin_bit_cast(f32x2, __hip_atomic_load((unsigned long long*)(agg + ((size_t)(pm0 + qq) * DM + chb + tid) * 2), __ATOMIC_RELAXED, __HIP_MEMORY_SCOPE_AGENT)); }
; #pragma unroll
;             for (int q = 0; q < 15; ++q) if (q < np) h0 = ahs[q].x * h0 + ahs[q].y;
;             C0[tid] = h0; }
;         EPI_BAR();
; #pragma unroll
;         for (int ai = 0; ai < 2; ++ai) { float cl[2][4];
;             if (ai == 0) {
; #pragma unroll
;                 for (int m = 0; m < 4; ++m)
; #pragma unroll
;                     for (int n = 0; n < 2; ++n) gpre[1][m][n] = *(const u32x2*)(gg + roff + (size_t)(128 + m) * DM + n * 16); }
; #pragma unroll
;             for (int n = 0; n < 2; ++n)
; #pragma unroll
;                 for (int j = 0; j < 4; ++j) { const int c = wc * 32 + n * 16 + fq * 4 + j; float s = C0[c];
;                     if (ai == 1) { const f32x2 b0 = *(const LAS f32x2*)(X + (0 * 128 + c) * 2), b1 = *(const LAS f32x2*)(X + (1 * 128 + c) * 2); s = b0.x * s + b0.y; s = b1.x * s + b1.y; }
;                     if (wr == 1) { const f32x2 b2 = *(const LAS f32x2*)(X + ((ai * 2) * 128 + c) * 2); s = b2.x * s + b2.y; }
;                     cl[n][j] = EA[ai][n][j] * s + EH[ai][n][j]; }
.Lp9_lb_skip1:
	s_waitcnt lgkmcnt(0)
	s_barrier
	s_cmp_lt_u32 s91, 0x80
	s_cbranch_scc0 .Lp9_lb_skip2
	s_lshl_b32 s8, s18, 4
	s_add_i32 s8, s8, s16
	s_lshl_b32 s8, s8, 2
	v_mov_b32_e32 v204, s8
	v_mov_b32_e32 v205, 1
	v_cmp_eq_u32_e32 vcc, 0, v228
	s_and_saveexec_b64 s[34:35], vcc
	global_store_dword v204, v205, s[52:53] sc1
	s_mov_b64 exec, s[34:35]
	s_and_b32 s12, s18, 15
	s_and_b32 s13, s18, -16
	v_add_u32_e32 v206, s13, v227
	v_lshl_add_u32 v206, v206, 4, s16
	v_lshlrev_b32_e32 v206, 2, v206
	v_cmp_gt_u32_e64 s[26:27], s12, v227
	s_mov_b32 s24, 0
.Lp9_poll:
	v_mov_b32_e32 v207, 1
	s_and_saveexec_b64 s[34:35], s[26:27]
	s_cbranch_execz .Lp9_poll_none
	global_load_dword v207, v206, s[52:53] sc1
	s_waitcnt vmcnt(0)
.Lp9_poll_none:
	s_mov_b64 exec, s[34:35]
	v_cmp_eq_u32_e64 s[36:37], 0, v207
	s_cmp_eq_u64 s[36:37], 0
	s_cbranch_scc1 .Lp9_polled
	s_sleep 1
	s_add_i32 s24, s24, 1
	s_cmp_lt_u32 s24, 0x4001
	s_cbranch_scc1 .Lp9_poll
.Lp9_polled:
	s_lshl_b32 s8, s13, 11
	s_add_i32 s8, s8, s11
	v_add_u32_e32 v250, s8, v228
	v_lshlrev_b32_e32 v250, 3, v250
	s_cmp_lt_u32 0, s12
	s_cselect_b32 s25, 0, 0
	v_add_u32_e32 v251, s25, v250
	global_load_dwordx2 v[202:203], v251, s[50:51] sc1
	s_cmp_lt_u32 1, s12
	s_cselect_b32 s25, 16384, 0
	v_add_u32_e32 v251, s25, v250
	global_load_dwordx2 v[204:205], v251, s[50:51] sc1
	s_cmp_lt_u32 2, s12
	s_cselect_b32 s25, 32768, 0
	v_add_u32_e32 v251, s25, v250
	global_load_dwordx2 v[206:207], v251, s[50:51] sc1
	s_cmp_lt_u32 3, s12
	s_cselect_b32 s25, 49152, 0
	v_add_u32_e32 v251, s25, v250
	global_load_dwordx2 v[208:209], v251, s[50:51] sc1
	s_cmp_lt_u32 4, s12
	s_cselect_b32 s25, 65536, 0
	v_add_u32_e32 v251, s25, v250
	global_load_dwordx2 v[210:211], v251, s[50:51] sc1
	s_cmp_lt_u32 5, s12
	s_cselect_b32 s25, 81920, 0
	v_add_u32_e32 v251, s25, v250
	global_load_dwordx2 v[212:213], v251, s[50:51] sc1
	s_cmp_lt_u32 6, s12
	s_cselect_b32 s25, 98304, 0
	v_add_u32_e32 v251, s25, v250
	global_load_dwordx2 v[214:215], v251, s[50:51] sc1
	s_cmp_lt_u32 7, s12
	s_cselect_b32 s25, 114688, 0
	v_add_u32_e32 v251, s25, v250
	global_load_dwordx2 v[216:217], v251, s[50:51] sc1
	s_cmp_lt_u32 8, s12
	s_cselect_b32 s25, 131072, 0
	v_add_u32_e32 v251, s25, v250
	global_load_dwordx2 v[218:219], v251, s[50:51] sc1
	s_cmp_lt_u32 9, s12
	s_cselect_b32 s25, 147456, 0
	v_add_u32_e32 v251, s25, v250
	global_load_dwordx2 v[238:239], v251, s[50:51] sc1
	s_cmp_lt_u32 10, s12
	s_cselect_b32 s25, 163840, 0
	v_add_u32_e32 v251, s25, v250
	global_load_dwordx2 v[240:241], v251, s[50:51] sc1
	s_cmp_lt_u32 11, s12
	s_cselect_b32 s25, 180224, 0
	v_add_u32_e32 v251, s25, v250
	global_load_dwordx2 v[242:243], v251, s[50:51] sc1
	s_cmp_lt_u32 12, s12
	s_cselect_b32 s25, 196608, 0
	v_add_u32_e32 v251, s25, v250
	global_load_dwordx2 v[244:245], v251, s[50:51] sc1
	s_cmp_lt_u32 13, s12
	s_cselect_b32 s25, 212992, 0
	v_add_u32_e32 v251, s25, v250
	global_load_dwordx2 v[246:247], v251, s[50:51] sc1
	s_cmp_lt_u32 14, s12
	s_cselect_b32 s25, 229376, 0
	v_add_u32_e32 v251, s25, v250
	global_load_dwordx2 v[248:249], v251, s[50:51] sc1
	v_mov_b32_e32 v252, 0
	s_waitcnt vmcnt(0)
	s_cmp_lt_u32 0, s12
	s_cbranch_scc0 .Lp9_folded
	v_fma_f32 v252, v202, v252, v203
	s_cmp_lt_u32 1, s12
	s_cbranch_scc0 .Lp9_folded
	v_fma_f32 v252, v204, v252, v205
	s_cmp_lt_u32 2, s12
	s_cbranch_scc0 .Lp9_folded
	v_fma_f32 v252, v206, v252, v207
	s_cmp_lt_u32 3, s12
	s_cbranch_scc0 .Lp9_folded
	v_fma_f32 v252, v208, v252, v209
	s_cmp_lt_u32 4, s12
	s_cbranch_scc0 .Lp9_folded
	v_fma_f32 v252, v210, v252, v211
	s_cmp_lt_u32 5, s12
	s_cbranch_scc0 .Lp9_folded
	v_fma_f32 v252, v212, v252, v213
	s_cmp_lt_u32 6, s12
	s_cbranch_scc0 .Lp9_folded
	v_fma_f32 v252, v214, v252, v215
	s_cmp_lt_u32 7, s12
	s_cbranch_scc0 .Lp9_folded
	v_fma_f32 v252, v216, v252, v217
	s_cmp_lt_u32 8, s12
	s_cbranch_scc0 .Lp9_folded
	v_fma_f32 v252, v218, v252, v219
	s_cmp_lt_u32 9, s12
	s_cbranch_scc0 .Lp9_folded
	v_fma_f32 v252, v238, v252, v239
	s_cmp_lt_u32 10, s12
	s_cbranch_scc0 .Lp9_folded
	v_fma_f32 v252, v240, v252, v241
	s_cmp_lt_u32 11, s12
	s_cbranch_scc0 .Lp9_folded
	v_fma_f32 v252, v242, v252, v243
	s_cmp_lt_u32 12, s12
	s_cbranch_scc0 .Lp9_folded
	v_fma_f32 v252, v244, v252, v245
	s_cmp_lt_u32 13, s12
	s_cbranch_scc0 .Lp9_folded
	v_fma_f32 v252, v246, v252, v247
	s_cmp_lt_u32 14, s12
	s_cbranch_scc0 .Lp9_folded
	v_fma_f32 v252, v248, v252, v249
.Lp9_folded:
	v_lshlrev_b32_e32 v253, 2, v228
	v_add_u32_e32 v253, 0x21000, v253
	ds_write_b32 v253, v252
.Lp9_lb_skip2:
	s_waitcnt lgkmcnt(0)
	s_barrier
	s_waitcnt vmcnt(0)
	s_lshl_b32 s8, s10, 5
	v_lshl_add_u32 v202, v224, 2, s8
	v_lshlrev_b32_e32 v203, 3, v202
	v_add_u32_e32 v203, 0x20000, v203
	v_lshlrev_b32_e32 v202, 2, v202
	v_add_u32_e32 v202, 0x21000, v202
	ds_read_b128 v[204:207], v202
	ds_read_b128 v[208:211], v202 offset:64
	s_waitcnt lgkmcnt(0)
	s_cmp_eq_u32 s9, 0
	s_cbranch_scc1 .Lp9_fin0
	ds_read_b128 v[212:215], v203 offset:0
	ds_read_b128 v[216:219], v203 offset:16
	s_waitcnt lgkmcnt(0)
	v_fma_f32 v204, v212, v204, v213
	v_fma_f32 v205, v214, v205, v215
	v_fma_f32 v206, v216, v206, v217
	v_fma_f32 v207, v218, v207, v219
	ds_read_b128 v[212:215], v203 offset:128
	ds_read_b128 v[216:219], v203 offset:144
	s_waitcnt lgkmcnt(0)
	v_fma_f32 v208, v212, v208, v213
	v_fma_f32 v209, v214, v209, v215
	v_fma_f32 v210, v216, v210, v217
	v_fma_f32 v211, v218, v211, v219
; #define LAS __attribute__((address_space(3)))
; __device__ __forceinline__ unsigned cvt_pk_bf16(float lo, float hi) { unsigned r; asm volatile("v_cvt_pk_bf16_f32 %0, %1, %2" : "=v"(r) : "v"(lo), "v"(hi)); return r; }
;     __device__ __forceinline__ void operator()(Acc& acc, const Unit& u, int wr, int wc, int fr_, int fq_, LAS unsigned char* le, int wid, int lane, int&) const {
;     ...
;         for (int ai = 0; ai < 2; ++ai) { float cl[2][4];
;             if (ai == 0) {
; #pragma unroll
;                 for (int m = 0; m < 4; ++m)
; #pragma unroll
;                     for (int n = 0; n < 2; ++n) gpre[1][m][n] = *(const u32x2*)(gg + roff + (size_t)(128 + m) * DM + n * 16); }
; #pragma unroll
;             for (int n = 0; n < 2; ++n)
; #pragma unroll
;                 for (int j = 0; j < 4; ++j) { const int c = wc * 32 + n * 16 + fq * 4 + j; float s = C0[c];
;                     if (ai == 1) { const f32x2 b0 = *(const LAS f32x2*)(X + (0 * 128 + c) * 2), b1 = *(const LAS f32x2*)(X + (1 * 128 + c) * 2); s = b0.x * s + b0.y; s = b1.x * s + b1.y; }
;                     if (wr == 1) { const f32x2 b2 = *(const LAS f32x2*)(X + ((ai * 2) * 128 + c) * 2); s = b2.x * s + b2.y; }
;                     cl[n][j] = EA[ai][n][j] * s + EH[ai][n][j]; }
; #pragma unroll
;             for (int m = 0; m < 4; ++m) {
; #pragma unroll
;                 for (int n = 0; n < 2; ++n) { const u32x2 gw = gpre[ai][m][n]; const float gv[4] = {bflo(gw.x), bfhi(gw.x), bflo(gw.y), bfhi(gw.y)}; float y[4];
; #pragma unroll
;                     for (int j = 0; j < 4; ++j) y[j] = (acc[ai][0][m][n][j] * cl[n][j] + acc[ai][1][m][n][j]) * gv[j];
;                     u32x2 w; w.x = cvt_pk_bf16(y[0], y[1]); w.y = cvt_pk_bf16(y[2], y[3]);
;                     *(u32x2*)(yb + roff + n * 16) = w; }
;                 roff += (size_t)(m == 3 ? 125 : 1) * DM; asm volatile("" : "+v"(roff) :: "memory"); } }
.Lp9_fin0:
	v_lshlrev_b32_e32 v238, 16, v166
	v_and_b32_e32 v239, s22, v166
	v_lshlrev_b32_e32 v240, 16, v167
	v_and_b32_e32 v241, s22, v167
	v_pk_fma_f32 v[242:243], v[148:149], v[204:205], v[132:133] op_sel:[0,0,0] op_sel_hi:[1,1,1]
	v_pk_fma_f32 v[244:245], v[150:151], v[206:207], v[134:135] op_sel:[0,0,0] op_sel_hi:[1,1,1]
	v_pk_mul_f32 v[242:243], v[242:243], v[238:239] op_sel:[0,0] op_sel_hi:[1,1]
	v_pk_mul_f32 v[244:245], v[244:245], v[240:241] op_sel:[0,0] op_sel_hi:[1,1]
	v_cvt_pk_bf16_f32 v246, v242, v243
	v_cvt_pk_bf16_f32 v247, v244, v245
	global_store_dwordx2 v229, v[246:247], s[48:49] offset:0
	v_lshlrev_b32_e32 v238, 16, v168
	v_and_b32_e32 v239, s22, v168
	v_lshlrev_b32_e32 v240, 16, v169
	v_and_b32_e32 v241, s22, v169
	v_pk_fma_f32 v[242:243], v[116:117], v[208:209], v[92:93] op_sel:[0,0,0] op_sel_hi:[1,1,1]
	v_pk_fma_f32 v[244:245], v[118:119], v[210:211], v[94:95] op_sel:[0,0,0] op_sel_hi:[1,1,1]
	v_pk_mul_f32 v[242:243], v[242:243], v[238:239] op_sel:[0,0] op_sel_hi:[1,1]
	v_pk_mul_f32 v[244:245], v[244:245], v[240:241] op_sel:[0,0] op_sel_hi:[1,1]
	v_cvt_pk_bf16_f32 v246, v242, v243
	v_cvt_pk_bf16_f32 v247, v244, v245
	global_store_dwordx2 v229, v[246:247], s[48:49] offset:32
	v_lshlrev_b32_e32 v238, 16, v170
	v_and_b32_e32 v239, s22, v170
	v_lshlrev_b32_e32 v240, 16, v171
	v_and_b32_e32 v241, s22, v171
	v_pk_fma_f32 v[242:243], v[144:145], v[204:205], v[128:129] op_sel:[0,0,0] op_sel_hi:[1,1,1]
	v_pk_fma_f32 v[244:245], v[146:147], v[206:207], v[130:131] op_sel:[0,0,0] op_sel_hi:[1,1,1]
	v_pk_mul_f32 v[242:243], v[242:243], v[238:239] op_sel:[0,0] op_sel_hi:[1,1]
	v_pk_mul_f32 v[244:245], v[244:245], v[240:241] op_sel:[0,0] op_sel_hi:[1,1]
	v_cvt_pk_bf16_f32 v246, v242, v243
	v_cvt_pk_bf16_f32 v247, v244, v245
	global_store_dwordx2 v230, v[246:247], s[48:49] offset:0
	v_lshlrev_b32_e32 v238, 16, v172
	v_and_b32_e32 v239, s22, v172
	v_lshlrev_b32_e32 v240, 16, v173
	v_and_b32_e32 v241, s22, v173
	v_pk_fma_f32 v[242:243], v[112:113], v[208:209], v[84:85] op_sel:[0,0,0] op_sel_hi:[1,1,1]
	v_pk_fma_f32 v[244:245], v[114:115], v[210:211], v[86:87] op_sel:[0,0,0] op_sel_hi:[1,1,1]
	v_pk_mul_f32 v[242:243], v[242:243], v[238:239] op_sel:[0,0] op_sel_hi:[1,1]
	v_pk_mul_f32 v[244:245], v[244:245], v[240:241] op_sel:[0,0] op_sel_hi:[1,1]
	v_cvt_pk_bf16_f32 v246, v242, v243
	v_cvt_pk_bf16_f32 v247, v244, v245
	global_store_dwordx2 v230, v[246:247], s[48:49] offset:32
	v_lshlrev_b32_e32 v238, 16, v174
	v_and_b32_e32 v239, s22, v174
	v_lshlrev_b32_e32 v240, 16, v175
	v_and_b32_e32 v241, s22, v175
	v_pk_fma_f32 v[242:243], v[140:141], v[204:205], v[124:125] op_sel:[0,0,0] op_sel_hi:[1,1,1]
	v_pk_fma_f32 v[244:245], v[142:143], v[206:207], v[126:127] op_sel:[0,0,0] op_sel_hi:[1,1,1]
	v_pk_mul_f32 v[242:243], v[242:243], v[238:239] op_sel:[0,0] op_sel_hi:[1,1]
	v_pk_mul_f32 v[244:245], v[244:245], v[240:241] op_sel:[0,0] op_sel_hi:[1,1]
	v_cvt_pk_bf16_f32 v246, v242, v243
	v_cvt_pk_bf16_f32 v247, v244, v245
	global_store_dwordx2 v231, v[246:247], s[48:49] offset:0
	v_lshlrev_b32_e32 v238, 16, v176
	v_and_b32_e32 v239, s22, v176
	v_lshlrev_b32_e32 v240, 16, v177
	v_and_b32_e32 v241, s22, v177
	v_pk_fma_f32 v[242:243], v[108:109], v[208:209], v[80:81] op_sel:[0,0,0] op_sel_hi:[1,1,1]
	v_pk_fma_f32 v[244:245], v[110:111], v[210:211], v[82:83] op_sel:[0,0,0] op_sel_hi:[1,1,1]
	v_pk_mul_f32 v[242:243], v[242:243], v[238:239] op_sel:[0,0] op_sel_hi:[1,1]
	v_pk_mul_f32 v[244:245], v[244:245], v[240:241] op_sel:[0,0] op_sel_hi:[1,1]
	v_cvt_pk_bf16_f32 v246, v242, v243
	v_cvt_pk_bf16_f32 v247, v244, v245
	global_store_dwordx2 v231, v[246:247], s[48:49] offset:32
	v_lshlrev_b32_e32 v238, 16, v178
	v_and_b32_e32 v239, s22, v178
	v_lshlrev_b32_e32 v240, 16, v179
	v_and_b32_e32 v241, s22, v179
	v_pk_fma_f32 v[242:243], v[136:137], v[204:205], v[120:121] op_sel:[0,0,0] op_sel_hi:[1,1,1]
	v_pk_fma_f32 v[244:245], v[138:139], v[206:207], v[122:123] op_sel:[0,0,0] op_sel_hi:[1,1,1]
	v_pk_mul_f32 v[242:243], v[242:243], v[238:239] op_sel:[0,0] op_sel_hi:[1,1]
	v_pk_mul_f32 v[244:245], v[244:245], v[240:241] op_sel:[0,0] op_sel_hi:[1,1]
	v_cvt_pk_bf16_f32 v246, v242, v243
	v_cvt_pk_bf16_f32 v247, v244, v245
	global_store_dwordx2 v232, v[246:247], s[48:49] offset:0
	v_lshlrev_b32_e32 v238, 16, v180
	v_and_b32_e32 v239, s22, v180
	v_lshlrev_b32_e32 v240, 16, v181
	v_and_b32_e32 v241, s22, v181
	v_pk_fma_f32 v[242:243], v[96:97], v[208:209], v[76:77] op_sel:[0,0,0] op_sel_hi:[1,1,1]
	v_pk_fma_f32 v[244:245], v[98:99], v[210:211], v[78:79] op_sel:[0,0,0] op_sel_hi:[1,1,1]
	v_pk_mul_f32 v[242:243], v[242:243], v[238:239] op_sel:[0,0] op_sel_hi:[1,1]
	v_pk_mul_f32 v[244:245], v[244:245], v[240:241] op_sel:[0,0] op_sel_hi:[1,1]
	v_cvt_pk_bf16_f32 v246, v242, v243
	v_cvt_pk_bf16_f32 v247, v244, v245
	global_store_dwordx2 v232, v[246:247], s[48:49] offset:32
	ds_read_b128 v[204:207], v202
	ds_read_b128 v[208:211], v202 offset:64
	s_waitcnt lgkmcnt(0)
	ds_read_b128 v[212:215], v203 offset:0
	ds_read_b128 v[216:219], v203 offset:16
	s_waitcnt lgkmcnt(0)
	v_fma_f32 v204, v212, v204, v213
	v_fma_f32 v205, v214, v205, v215
	v_fma_f32 v206, v216, v206, v217
	v_fma_f32 v207, v218, v207, v219
	ds_read_b128 v[212:215], v203 offset:128
	ds_read_b128 v[216:219], v203 offset:144
	s_waitcnt lgkmcnt(0)
	v_fma_f32 v208, v212, v208, v213
	v_fma_f32 v209, v214, v209, v215
	v_fma_f32 v210, v216, v210, v217
	v_fma_f32 v211, v218, v211, v219
	ds_read_b128 v[212:215], v203 offset:1024
	ds_read_b128 v[216:219], v203 offset:1040
	s_waitcnt lgkmcnt(0)
	v_fma_f32 v204, v212, v204, v213
	v_fma_f32 v205, v214, v205, v215
	v_fma_f32 v206, v216, v206, v217
	v_fma_f32 v207, v218, v207, v219
	ds_read_b128 v[212:215], v203 offset:1152
	ds_read_b128 v[216:219], v203 offset:1168
	s_waitcnt lgkmcnt(0)
	v_fma_f32 v208, v212, v208, v213
	v_fma_f32 v209, v214, v209, v215
	v_fma_f32 v210, v216, v210, v217
	v_fma_f32 v211, v218, v211, v219
	s_cmp_eq_u32 s9, 0
	s_cbranch_scc1 .Lp9_fin1
	ds_read_b128 v[212:215], v203 offset:2048
	ds_read_b128 v[216:219], v203 offset:2064
	s_waitcnt lgkmcnt(0)
	v_fma_f32 v204, v212, v204, v213
	v_fma_f32 v205, v214, v205, v215
	v_fma_f32 v206, v216, v206, v217
	v_fma_f32 v207, v218, v207, v219
	ds_read_b128 v[212:215], v203 offset:2176
	ds_read_b128 v[216:219], v203 offset:2192
	s_waitcnt lgkmcnt(0)
	v_fma_f32 v208, v212, v208, v213
	v_fma_f32 v209, v214, v209, v215
	v_fma_f32 v210, v216, v210, v217
	v_fma_f32 v211, v218, v211, v219
; #define LAS __attribute__((address_space(3)))
; __device__ __forceinline__ unsigned cvt_pk_bf16(float lo, float hi) { unsigned r; asm volatile("v_cvt_pk_bf16_f32 %0, %1, %2" : "=v"(r) : "v"(lo), "v"(hi)); return r; }
;     __device__ __forceinline__ void operator()(Acc& acc, const Unit& u, int wr, int wc, int fr_, int fq_, LAS unsigned char* le, int wid, int lane, int&) const {
;     ...
;         for (int ai = 0; ai < 2; ++ai) { float cl[2][4];
;             if (ai == 0) {
; #pragma unroll
;                 for (int m = 0; m < 4; ++m)
; #pragma unroll
;                     for (int n = 0; n < 2; ++n) gpre[1][m][n] = *(const u32x2*)(gg + roff + (size_t)(128 + m) * DM + n * 16); }
; #pragma unroll
;             for (int n = 0; n < 2; ++n)
; #pragma unroll
;                 for (int j = 0; j < 4; ++j) { const int c = wc * 32 + n * 16 + fq * 4 + j; float s = C0[c];
;                     if (ai == 1) { const f32x2 b0 = *(const LAS f32x2*)(X + (0 * 128 + c) * 2), b1 = *(const LAS f32x2*)(X + (1 * 128 + c) * 2); s = b0.x * s + b0.y; s = b1.x * s + b1.y; }
;                     if (wr == 1) { const f32x2 b2 = *(const LAS f32x2*)(X + ((ai * 2) * 128 + c) * 2); s = b2.x * s + b2.y; }
;                     cl[n][j] = EA[ai][n][j] * s + EH[ai][n][j]; }
; #pragma unroll
;             for (int m = 0; m < 4; ++m) {
; #pragma unroll
;                 for (int n = 0; n < 2; ++n) { const u32x2 gw = gpre[ai][m][n]; const float gv[4] = {bflo(gw.x), bfhi(gw.x), bflo(gw.y), bfhi(gw.y)}; float y[4];
; #pragma unroll
;                     for (int j = 0; j < 4; ++j) y[j] = (acc[ai][0][m][n][j] * cl[n][j] + acc[ai][1][m][n][j]) * gv[j];
;                     u32x2 w; w.x = cvt_pk_bf16(y[0], y[1]); w.y = cvt_pk_bf16(y[2], y[3]);
;                     *(u32x2*)(yb + roff + n * 16) = w; }
;                 roff += (size_t)(m == 3 ? 125 : 1) * DM; asm volatile("" : "+v"(roff) :: "memory"); } }
.Lp9_fin1:
	v_lshlrev_b32_e32 v238, 16, v182
	v_and_b32_e32 v239, s22, v182
	v_lshlrev_b32_e32 v240, 16, v183
	v_and_b32_e32 v241, s22, v183
	v_pk_fma_f32 v[242:243], v[64:65], v[204:205], v[44:45] op_sel:[0,0,0] op_sel_hi:[1,1,1]
	v_pk_fma_f32 v[244:245], v[66:67], v[206:207], v[46:47] op_sel:[0,0,0] op_sel_hi:[1,1,1]
	v_pk_mul_f32 v[242:243], v[242:243], v[238:239] op_sel:[0,0] op_sel_hi:[1,1]
	v_pk_mul_f32 v[244:245], v[244:245], v[240:241] op_sel:[0,0] op_sel_hi:[1,1]
	v_cvt_pk_bf16_f32 v246, v242, v243
	v_cvt_pk_bf16_f32 v247, v244, v245
	global_store_dwordx2 v233, v[246:247], s[48:49] offset:0
	v_lshlrev_b32_e32 v238, 16, v184
	v_and_b32_e32 v239, s22, v184
	v_lshlrev_b32_e32 v240, 16, v185
	v_and_b32_e32 v241, s22, v185
	v_pk_fma_f32 v[242:243], v[28:29], v[208:209], v[12:13] op_sel:[0,0,0] op_sel_hi:[1,1,1]
	v_pk_fma_f32 v[244:245], v[30:31], v[210:211], v[14:15] op_sel:[0,0,0] op_sel_hi:[1,1,1]
	v_pk_mul_f32 v[242:243], v[242:243], v[238:239] op_sel:[0,0] op_sel_hi:[1,1]
	v_pk_mul_f32 v[244:245], v[244:245], v[240:241] op_sel:[0,0] op_sel_hi:[1,1]
	v_cvt_pk_bf16_f32 v246, v242, v243
	v_cvt_pk_bf16_f32 v247, v244, v245
	global_store_dwordx2 v233, v[246:247], s[48:49] offset:32
	v_lshlrev_b32_e32 v238, 16, v186
	v_and_b32_e32 v239, s22, v186
	v_lshlrev_b32_e32 v240, 16, v187
	v_and_b32_e32 v241, s22, v187
	v_pk_fma_f32 v[242:243], v[60:61], v[204:205], v[40:41] op_sel:[0,0,0] op_sel_hi:[1,1,1]
	v_pk_fma_f32 v[244:245], v[62:63], v[206:207], v[42:43] op_sel:[0,0,0] op_sel_hi:[1,1,1]
	v_pk_mul_f32 v[242:243], v[242:243], v[238:239] op_sel:[0,0] op_sel_hi:[1,1]
	v_pk_mul_f32 v[244:245], v[244:245], v[240:241] op_sel:[0,0] op_sel_hi:[1,1]
	v_cvt_pk_bf16_f32 v246, v242, v243
	v_cvt_pk_bf16_f32 v247, v244, v245
	global_store_dwordx2 v234, v[246:247], s[48:49] offset:0
	v_lshlrev_b32_e32 v238, 16, v188
	v_and_b32_e32 v239, s22, v188
	v_lshlrev_b32_e32 v240, 16, v189
	v_and_b32_e32 v241, s22, v189
	v_pk_fma_f32 v[242:243], v[24:25], v[208:209], v[8:9] op_sel:[0,0,0] op_sel_hi:[1,1,1]
	v_pk_fma_f32 v[244:245], v[26:27], v[210:211], v[10:11] op_sel:[0,0,0] op_sel_hi:[1,1,1]
	v_pk_mul_f32 v[242:243], v[242:243], v[238:239] op_sel:[0,0] op_sel_hi:[1,1]
	v_pk_mul_f32 v[244:245], v[244:245], v[240:241] op_sel:[0,0] op_sel_hi:[1,1]
	v_cvt_pk_bf16_f32 v246, v242, v243
	v_cvt_pk_bf16_f32 v247, v244, v245
	global_store_dwordx2 v234, v[246:247], s[48:49] offset:32
	v_lshlrev_b32_e32 v238, 16, v190
	v_and_b32_e32 v239, s22, v190
	v_lshlrev_b32_e32 v240, 16, v191
	v_and_b32_e32 v241, s22, v191
	v_pk_fma_f32 v[242:243], v[52:53], v[204:205], v[36:37] op_sel:[0,0,0] op_sel_hi:[1,1,1]
	v_pk_fma_f32 v[244:245], v[54:55], v[206:207], v[38:39] op_sel:[0,0,0] op_sel_hi:[1,1,1]
	v_pk_mul_f32 v[242:243], v[242:243], v[238:239] op_sel:[0,0] op_sel_hi:[1,1]
	v_pk_mul_f32 v[244:245], v[244:245], v[240:241] op_sel:[0,0] op_sel_hi:[1,1]
	v_cvt_pk_bf16_f32 v246, v242, v243
	v_cvt_pk_bf16_f32 v247, v244, v245
	global_store_dwordx2 v235, v[246:247], s[48:49] offset:0
	v_lshlrev_b32_e32 v238, 16, v192
	v_and_b32_e32 v239, s22, v192
	v_lshlrev_b32_e32 v240, 16, v193
	v_and_b32_e32 v241, s22, v193
	v_pk_fma_f32 v[242:243], v[20:21], v[208:209], v[4:5] op_sel:[0,0,0] op_sel_hi:[1,1,1]
	v_pk_fma_f32 v[244:245], v[22:23], v[210:211], v[6:7] op_sel:[0,0,0] op_sel_hi:[1,1,1]
	v_pk_mul_f32 v[242:243], v[242:243], v[238:239] op_sel:[0,0] op_sel_hi:[1,1]
	v_pk_mul_f32 v[244:245], v[244:245], v[240:241] op_sel:[0,0] op_sel_hi:[1,1]
	v_cvt_pk_bf16_f32 v246, v242, v243
	v_cvt_pk_bf16_f32 v247, v244, v245
	global_store_dwordx2 v235, v[246:247], s[48:49] offset:32
	v_lshlrev_b32_e32 v238, 16, v194
	v_and_b32_e32 v239, s22, v194
	v_lshlrev_b32_e32 v240, 16, v195
	v_and_b32_e32 v241, s22, v195
	v_pk_fma_f32 v[242:243], v[48:49], v[204:205], v[32:33] op_sel:[0,0,0] op_sel_hi:[1,1,1]
	v_pk_fma_f32 v[244:245], v[50:51], v[206:207], v[34:35] op_sel:[0,0,0] op_sel_hi:[1,1,1]
	v_pk_mul_f32 v[242:243], v[242:243], v[238:239] op_sel:[0,0] op_sel_hi:[1,1]
	v_pk_mul_f32 v[244:245], v[244:245], v[240:241] op_sel:[0,0] op_sel_hi:[1,1]
	v_cvt_pk_bf16_f32 v246, v242, v243
	v_cvt_pk_bf16_f32 v247, v244, v245
	global_store_dwordx2 v236, v[246:247], s[48:49] offset:0
	v_lshlrev_b32_e32 v238, 16, v196
	v_and_b32_e32 v239, s22, v196
	v_lshlrev_b32_e32 v240, 16, v197
	v_and_b32_e32 v241, s22, v197
	v_pk_fma_f32 v[242:243], v[16:17], v[208:209], v[0:1] op_sel:[0,0,0] op_sel_hi:[1,1,1]
	v_pk_fma_f32 v[244:245], v[18:19], v[210:211], v[2:3] op_sel:[0,0,0] op_sel_hi:[1,1,1]
	v_pk_mul_f32 v[242:243], v[242:243], v[238:239] op_sel:[0,0] op_sel_hi:[1,1]
	v_pk_mul_f32 v[244:245], v[244:245], v[240:241] op_sel:[0,0] op_sel_hi:[1,1]
	v_cvt_pk_bf16_f32 v246, v242, v243
	v_cvt_pk_bf16_f32 v247, v244, v245
	global_store_dwordx2 v236, v[246:247], s[48:49] offset:32
	s_andn2_b64 vcc, exec, s[66:67]
	s_mov_b64 s[8:9], -1
	s_cbranch_vccnz .LBB0_1585
	s_and_b64 vcc, exec, s[6:7]
	s_cbranch_vccnz .LBB0_1584
	s_barrier
	s_branch .LBB0_1584
